# P2/P10/P13 row loops: flat->global loads, counted vmcnt so next-row prefetch overlaps compute
# speedup vs baseline: 1.0052x; 1.0052x over previous
; __device__ __forceinline__ void ph2(LAS unsigned char* lds, int tid, int lane, int wave, int G, int bid) {
;     ...
;     for (int i = tid; i < 5 * 2 * 512; i += NWAVES * 64) { const int b = i >> 10, which = (i >> 9) & 1, q = i & 511; f32x4 t = *((const f32x4*)(modv + (size_t)b * 12288 + which * D) + q); if (which) t = t + 1.0f; MV[i] = t; }
;     __syncthreads();
;     const int gw = bid * NWAVES + wave, NGW = G * NWAVES; const float* XP = AIN(IX); const float* CP = AIN(ICTX);
;     f32x4 v[8];
;     { const int m = T + TC - 1 - gw; const f32x4* xq = (const f32x4*)(m < T ? XP + (size_t)m * D : CP + (size_t)(m - T) * D) + lane;
; #pragma unroll
;       for (int j = 0; j < 8; ++j) v[j] = __builtin_nontemporal_load(xq + 64 * j); }
;     for (int m = T + TC - 1 - gw; m >= 0; m -= NGW) {
;         f32x4 vn[8]; const int mn = m - NGW;
;         if (mn >= 0) { const f32x4* xq = (const f32x4*)(mn < T ? XP + (size_t)mn * D : CP + (size_t)(mn - T) * D) + lane;
; #pragma unroll
;             for (int j = 0; j < 8; ++j) vn[j] = __builtin_nontemporal_load(xq + 64 * j); }
;         else {
; #pragma unroll
;             for (int j = 0; j < 8; ++j) vn[j] = (f32x4){0.f, 0.f, 0.f, 0.f}; }
;         bf16* orow; int bsel;
;         if (m < T) { orow = (bf16*)(ws + WS_R3) + (size_t)m * D; bsel = m >> 13; }
;         else { orow = (bf16*)(ws + WS_HC) + (size_t)(m - T) * D; bsel = 4; }
;         float s = 0.f;
; #pragma unroll
;         for (int j = 0; j < 8; ++j) s += (v[j].x + v[j].y) + (v[j].z + v[j].w);
;         const float mean = wave_sum(s) * (1.f / D); float s2 = 0.f;
; #pragma unroll
;         for (int j = 0; j < 8; ++j) { v[j] = v[j] - mean; s2 += (v[j].x * v[j].x + v[j].y * v[j].y) + (v[j].z * v[j].z + v[j].w * v[j].w); }
;         const float rstd = 1.f / sqrtf(wave_sum(s2) * (1.f / D) + LN_EPS);
;         const LAS f32x4* shq = MV + bsel * 1024 + lane; const LAS f32x4* scq = shq + 512; u32x2* o8 = (u32x2*)orow + lane;
;         unsigned char* o4 = ws + WS_RA + ((size_t)((m < T ? m : 0) >> 8) * 16 << 15) + ((size_t)(m & 255) << 7) + ((lane >> 5) << 15) + 4 * (lane & 31);
; #pragma unroll
;         for (int j = 0; j < 8; ++j) { const f32x4 sh = shq[64 * j], sc = scq[64 * j]; const f32x4 y = v[j] * rstd * sc + sh; if (m < T) *(unsigned*)(o4 + ((size_t)(2 * j) << 15)) = pk4_fp8(y.x, y.y, y.z, y.w); else o8[64 * j] = (u32x2){pk_bf16(y.x, y.y), pk_bf16(y.z, y.w)}; }
.LBB0_261:
	v_lshrrev_b32_e32 v2, 10, v8
	v_and_b32_e32 v9, 1, v7
	v_mul_u32_u24_e32 v2, 0x3000, v2
	v_lshl_add_u64 v[10:11], v[2:3], 2, s[6:7]
	v_lshlrev_b32_e32 v2, 13, v9
	v_lshl_add_u64 v[10:11], v[10:11], 0, v[2:3]
	v_lshl_add_u64 v[10:11], v[10:11], 0, v[4:5]
	flat_load_dwordx4 v[10:13], v[10:11]
	v_cmp_lt_u32_e32 vcc, s10, v8
	s_or_b64 s[8:9], vcc, s[8:9]
	v_cmp_eq_u32_e32 vcc, 0, v9
	v_add_u32_e32 v2, 0x200, v8
	v_add_u32_e32 v7, 1, v7
	v_mov_b32_e32 v8, v2
	s_waitcnt vmcnt(0) lgkmcnt(0)
	v_pk_add_f32 v[14:15], v[12:13], 1.0 op_sel_hi:[1,0]
	v_pk_add_f32 v[16:17], v[10:11], 1.0 op_sel_hi:[1,0]
	v_cndmask_b32_e32 v13, v15, v13, vcc
	v_cndmask_b32_e32 v11, v17, v11, vcc
	v_cndmask_b32_e32 v10, v16, v10, vcc
	v_cndmask_b32_e32 v12, v14, v12, vcc
	ds_write_b128 v6, v[10:13]
	v_add_u32_e32 v6, 0x2000, v6
	s_andn2_b64 exec, exec, s[8:9]
	s_cbranch_execnz .LBB0_261
	s_or_b64 exec, exec, s[8:9]
	s_lshl_b32 s6, s2, 3
	s_add_i32 s8, s3, s6
	s_add_i32 s6, 0, 0x24400
	v_mov_b32_e32 v2, s6
	s_add_i32 s6, 0, 0x24404
	v_mov_b32_e32 v3, s6
	s_add_i32 s6, 0, 0x24410
	v_mov_b32_e32 v4, s6
	s_add_i32 s6, 0, 0x24414
	v_mov_b32_e32 v5, s6
	s_waitcnt lgkmcnt(0)
	s_barrier
	ds_read_b32 v2, v2
	ds_read_b32 v3, v3
	ds_read_b32 v4, v4
	ds_read_b32 v5, v5
	s_mov_b32 s7, 0
	s_waitcnt lgkmcnt(3)
	v_readfirstlane_b32 s14, v2
	s_waitcnt lgkmcnt(2)
	v_readfirstlane_b32 s15, v3
	s_waitcnt lgkmcnt(1)
	v_readfirstlane_b32 s16, v4
	s_cmp_lt_i32 s8, 0x8400
	s_waitcnt lgkmcnt(0)
	v_readfirstlane_b32 s17, v5
	s_cbranch_scc0 .LBB0_308
	s_lshl_b32 s18, s33, 3
	s_sub_i32 s19, 0x83ff, s8
	s_sub_i32 s6, 0x3ff, s8
	s_cmpk_gt_i32 s8, 0x3ff
	s_cselect_b32 s6, s19, s6
	s_cselect_b32 s9, s15, s17
	s_cselect_b32 s12, s14, s16
	s_lshl_b64 s[10:11], s[6:7], 13
	s_add_u32 s10, s12, s10
	v_mov_b32_e32 v3, 0
	v_lshlrev_b32_e32 v2, 4, v170
	s_addc_u32 s11, s9, s11
	v_lshl_add_u64 v[4:5], s[10:11], 0, v[2:3]
	s_movk_i32 s6, 0x1000
	v_add_co_u32_e32 v14, vcc, s6, v4
	v_add_u32_e32 v82, 0, v2
	s_nop 0
	v_addc_co_u32_e32 v15, vcc, 0, v5, vcc
	global_load_dwordx4 v[6:9], v[14:15], off offset:3072 nt
	global_load_dwordx4 v[10:13], v[14:15], off offset:2048 nt
	global_load_dwordx4 v[30:33], v[14:15], off offset:1024 nt
	global_load_dwordx4 v[50:53], v[14:15], off nt
	global_load_dwordx4 v[54:57], v[4:5], off offset:3072 nt
	global_load_dwordx4 v[58:61], v[4:5], off offset:2048 nt
	global_load_dwordx4 v[62:65], v[4:5], off offset:1024 nt
	global_load_dwordx4 v[66:69], v[4:5], off nt
	v_mbcnt_lo_u32_b32 v2, -1, 0
	v_mbcnt_hi_u32_b32 v2, -1, v2
	v_and_b32_e32 v4, 64, v2
	v_add_u32_e32 v4, 64, v4
	v_xor_b32_e32 v5, 1, v2
	v_cmp_lt_i32_e32 vcc, v5, v4
	s_add_u32 s20, s0, 0x1300000
	s_addc_u32 s21, s1, 0
	v_cndmask_b32_e32 v5, v2, v5, vcc
	v_lshlrev_b32_e32 v83, 2, v5
	v_xor_b32_e32 v5, 2, v2
	v_cmp_lt_i32_e32 vcc, v5, v4
	s_add_u32 s22, s0, 0x1e000000
	s_addc_u32 s23, s1, 0
	v_cndmask_b32_e32 v5, v2, v5, vcc
	v_lshlrev_b32_e32 v84, 2, v5
	v_xor_b32_e32 v5, 4, v2
	v_cmp_lt_i32_e32 vcc, v5, v4
	s_add_u32 s24, s0, 0x26000000
	s_addc_u32 s25, s1, 0
	v_cndmask_b32_e32 v5, v2, v5, vcc
	v_lshlrev_b32_e32 v85, 2, v5
	v_xor_b32_e32 v5, 8, v2
	v_cmp_lt_i32_e32 vcc, v5, v4
	s_add_i32 s8, s8, s18
	s_sub_i32 s0, 0x83ff, s8
	v_cndmask_b32_e32 v5, v2, v5, vcc
	v_lshlrev_b32_e32 v86, 2, v5
	v_xor_b32_e32 v5, 16, v2
	v_cmp_lt_i32_e32 vcc, v5, v4
	v_mov_b32_e32 v71, v3
	v_mov_b32_e32 v73, v3
	v_cndmask_b32_e32 v5, v2, v5, vcc
	v_lshlrev_b32_e32 v87, 2, v5
	v_xor_b32_e32 v5, 32, v2
	v_cmp_lt_i32_e32 vcc, v5, v4
	s_lshl_b32 s26, s19, 12
	s_lshl_b32 s27, s33, 15
	v_cndmask_b32_e32 v2, v2, v5, vcc
	v_lshlrev_b32_e32 v88, 2, v2
	v_lshlrev_b32_e32 v2, 10, v0
	v_and_b32_e32 v70, 0x8000, v2
	v_lshlrev_b32_e32 v2, 2, v0
	v_and_b32_e32 v72, 0x7c, v2
	s_lshl_b32 s28, s19, 7
	s_lshl_b32 s29, s33, 10
	s_sub_i32 s30, 0, s18
	s_lshl_b32 s31, s0, 13
	s_lshl_b32 s40, s33, 16
	v_mov_b32_e32 v89, 0x3727c5ac
	s_mov_b32 s41, 0xf800000
	v_mov_b32_e32 v90, 0x260
	s_mov_b32 s42, 0xc3e00000
	v_mov_b32_e32 v91, 0x43e00000
	s_waitcnt vmcnt(0)
	s_branch .LBB0_265
.LBB0_264:
	s_waitcnt vmcnt(8)
	s_sub_i32 s19, s19, s18
	s_sub_i32 s26, s26, s27
	s_sub_i32 s28, s28, s29
	s_sub_i32 s31, s31, s40
	v_mov_b64_e32 v[6:7], v[46:47]
	v_mov_b64_e32 v[10:11], v[42:43]
	v_mov_b64_e32 v[30:31], v[38:39]
	v_mov_b64_e32 v[52:53], v[36:37]
	v_mov_b64_e32 v[56:57], v[28:29]
	v_mov_b64_e32 v[60:61], v[24:25]
	v_mov_b64_e32 v[64:65], v[20:21]
	v_mov_b64_e32 v[68:69], v[16:17]
	s_cmp_gt_i32 s19, -1
	v_mov_b64_e32 v[8:9], v[48:49]
	v_mov_b64_e32 v[12:13], v[44:45]
	v_mov_b64_e32 v[32:33], v[40:41]
	v_mov_b64_e32 v[50:51], v[34:35]
	v_mov_b64_e32 v[54:55], v[26:27]
	v_mov_b64_e32 v[58:59], v[22:23]
	v_mov_b64_e32 v[62:63], v[18:19]
	v_mov_b64_e32 v[66:67], v[14:15]
	s_cbranch_scc0 .LBB0_308

; __device__ __forceinline__ void ph2(LAS unsigned char* lds, int tid, int lane, int wave, int G, int bid) {
;     ...
;         f32x4 vn[8]; const int mn = m - NGW;
;         if (mn >= 0) { const f32x4* xq = (const f32x4*)(mn < T ? XP + (size_t)mn * D : CP + (size_t)(mn - T) * D) + lane;
; #pragma unroll
;             for (int j = 0; j < 8; ++j) vn[j] = __builtin_nontemporal_load(xq + 64 * j); }
.LBB0_270:
	v_lshlrev_b32_e32 v2, 4, v170
	v_lshl_add_u64 v[4:5], s[0:1], 0, v[2:3]
	global_load_dwordx4 v[14:17], v[4:5], off nt
	global_load_dwordx4 v[18:21], v[4:5], off offset:1024 nt
	global_load_dwordx4 v[22:25], v[4:5], off offset:2048 nt
	global_load_dwordx4 v[26:29], v[4:5], off offset:3072 nt
	v_add_co_u32_e32 v4, vcc, 0x1000, v4
	s_nop 1
	v_addc_co_u32_e32 v5, vcc, 0, v5, vcc
	global_load_dwordx4 v[34:37], v[4:5], off nt
	global_load_dwordx4 v[38:41], v[4:5], off offset:1024 nt
	global_load_dwordx4 v[42:45], v[4:5], off offset:2048 nt
	global_load_dwordx4 v[46:49], v[4:5], off offset:3072 nt
	s_branch .LBB0_272

; #define LAS __attribute__((address_space(3)))
; __device__ __forceinline__ void ph2(LAS unsigned char* lds, int tid, int lane, int wave, int G, int bid) {
;     ...
;         float s = 0.f;
; #pragma unroll
;         for (int j = 0; j < 8; ++j) s += (v[j].x + v[j].y) + (v[j].z + v[j].w);
;         const float mean = wave_sum(s) * (1.f / D); float s2 = 0.f;
; #pragma unroll
;         for (int j = 0; j < 8; ++j) { v[j] = v[j] - mean; s2 += (v[j].x * v[j].x + v[j].y * v[j].y) + (v[j].z * v[j].z + v[j].w * v[j].w); }
;         const float rstd = 1.f / sqrtf(wave_sum(s2) * (1.f / D) + LN_EPS);
;         const LAS f32x4* shq = MV + bsel * 1024 + lane; const LAS f32x4* scq = shq + 512; u32x2* o8 = (u32x2*)orow + lane;
.LBB0_276:
	s_waitcnt lgkmcnt(0)
	v_mov_b32_e32 v4, v62
	v_mov_b32_e32 v5, v66
	v_mov_b32_e32 v74, v63
	v_mov_b32_e32 v75, v67
	v_pk_add_f32 v[4:5], v[4:5], v[74:75]
	v_mov_b32_e32 v74, v64
	v_mov_b32_e32 v75, v68
	v_mov_b32_e32 v76, v65
	v_mov_b32_e32 v77, v69
	v_pk_add_f32 v[74:75], v[74:75], v[76:77]
	v_mov_b32_e32 v76, v58
	v_pk_add_f32 v[4:5], v[4:5], v[74:75]
	v_mov_b32_e32 v74, v59
	v_mov_b32_e32 v75, v60
	v_mov_b32_e32 v77, v61
	v_pk_add_f32 v[74:75], v[74:75], v[76:77]
	v_add_f32_e32 v2, 0, v5
	v_pk_add_f32 v[74:75], v[74:75], v[74:75] op_sel_hi:[0,1]
	v_add_f32_e32 v5, v4, v2
	v_add_f32_e32 v77, v54, v55
	v_add_f32_e32 v79, v56, v57
	v_mov_b32_e32 v76, v50
	v_mov_b32_e32 v78, v51
	v_mov_b32_e32 v74, v52
	v_mov_b32_e32 v4, v53
	v_pk_add_f32 v[76:77], v[76:77], v[78:79]
	v_pk_add_f32 v[4:5], v[74:75], v[4:5]
	v_mov_b32_e32 v74, v31
	v_pk_add_f32 v[4:5], v[76:77], v[4:5]
	v_mov_b32_e32 v75, v32
	v_mov_b32_e32 v76, v30
	v_mov_b32_e32 v77, v33
	v_pk_add_f32 v[74:75], v[74:75], v[76:77]
	v_pk_add_f32 v[4:5], v[4:5], v[4:5] op_sel_hi:[0,1]
	v_pk_add_f32 v[74:75], v[74:75], v[74:75] op_sel_hi:[0,1]
	v_add_f32_e32 v77, v10, v11
	v_add_f32_e32 v79, v12, v13
	v_mov_b32_e32 v76, v6
	v_mov_b32_e32 v78, v7
	v_mov_b32_e32 v74, v8
	v_mov_b32_e32 v4, v9
	v_pk_add_f32 v[76:77], v[76:77], v[78:79]
	v_pk_add_f32 v[4:5], v[74:75], v[4:5]
	s_nop 0
	v_pk_add_f32 v[4:5], v[76:77], v[4:5]
	s_nop 0
	v_add_f32_e32 v2, v4, v5
	ds_bpermute_b32 v4, v83, v2
	s_waitcnt lgkmcnt(0)
	v_add_f32_e32 v2, v2, v4
	ds_bpermute_b32 v4, v84, v2
	s_waitcnt lgkmcnt(0)
	v_add_f32_e32 v2, v2, v4
	ds_bpermute_b32 v4, v85, v2
	s_waitcnt lgkmcnt(0)
	v_add_f32_e32 v2, v2, v4
	ds_bpermute_b32 v4, v86, v2
	s_waitcnt lgkmcnt(0)
	v_add_f32_e32 v2, v2, v4
	ds_bpermute_b32 v4, v87, v2
	s_waitcnt lgkmcnt(0)
	v_add_f32_e32 v2, v2, v4
	ds_bpermute_b32 v4, v88, v2
	s_waitcnt lgkmcnt(0)
	v_add_f32_e32 v96, v2, v4
	v_fmamk_f32 v67, v96, 0xba000000, v67
	v_fmamk_f32 v81, v96, 0xba000000, v69
	v_fmac_f32_e32 v66, 0xba000000, v96
	v_fmamk_f32 v79, v96, 0xba000000, v63
	v_fmac_f32_e32 v62, 0xba000000, v96
	v_mov_b32_e32 v78, v67
	v_fmamk_f32 v80, v96, 0xba000000, v68
	v_fmamk_f32 v75, v96, 0xba000000, v65
	v_fmamk_f32 v77, v96, 0xba000000, v64
	v_mov_b32_e32 v4, v66
	v_mov_b32_e32 v5, v62
	v_pk_mul_f32 v[64:65], v[78:79], v[78:79]
	v_mov_b32_e32 v74, v81
	v_pk_fma_f32 v[4:5], v[4:5], v[4:5], v[64:65]
	v_mov_b32_e32 v76, v80
	v_pk_mul_f32 v[64:65], v[74:75], v[74:75]
	v_fmamk_f32 v69, v96, 0xba000000, v61
	v_pk_fma_f32 v[64:65], v[76:77], v[76:77], v[64:65]
	v_fmamk_f32 v68, v96, 0xba000000, v60
	v_fmamk_f32 v59, v96, 0xba000000, v59
	v_fmac_f32_e32 v58, 0xba000000, v96
	v_pk_add_f32 v[4:5], v[4:5], v[64:65]
	v_pk_mul_f32 v[60:61], v[68:69], v[68:69]
	v_pk_mul_f32 v[64:65], v[58:59], v[58:59]
	v_fmac_f32_e32 v54, 0xba000000, v96
	v_pk_mov_b32 v[92:93], v[64:65], v[60:61] op_sel:[1,0]
	v_mov_b32_e32 v65, v61
	v_pk_add_f32 v[60:61], v[92:93], v[64:65]
	v_fmamk_f32 v64, v96, 0xba000000, v56
	v_fmamk_f32 v55, v96, 0xba000000, v55
	v_mul_f32_e32 v2, v54, v54
	v_fmamk_f32 v65, v96, 0xba000000, v57
	v_pk_fma_f32 v[56:57], v[54:55], v[54:55], v[2:3] op_sel_hi:[1,1,0]
	v_mul_f32_e32 v2, v64, v64
	v_pk_add_f32 v[4:5], v[4:5], v[4:5] op_sel_hi:[0,1]
	v_pk_add_f32 v[92:93], v[60:61], v[60:61] op_sel_hi:[0,1]
	v_pk_fma_f32 v[94:95], v[64:65], v[64:65], v[2:3] op_sel_hi:[1,1,0]
	v_fmamk_f32 v61, v96, 0xba000000, v53
	v_fmamk_f32 v60, v96, 0xba000000, v52
	v_fmamk_f32 v51, v96, 0xba000000, v51
	v_fmac_f32_e32 v50, 0xba000000, v96
	v_mul_f32_e32 v56, v50, v50
	v_mul_f32_e32 v94, v51, v51
	v_mul_f32_e32 v92, v60, v60
	v_mul_f32_e32 v4, v61, v61
	v_pk_add_f32 v[52:53], v[56:57], v[94:95]
	v_pk_add_f32 v[4:5], v[92:93], v[4:5]
	v_fmamk_f32 v31, v96, 0xba000000, v31
	v_pk_add_f32 v[4:5], v[52:53], v[4:5]
	v_fmamk_f32 v53, v96, 0xba000000, v33
	v_fmamk_f32 v52, v96, 0xba000000, v32
	v_fmac_f32_e32 v30, 0xba000000, v96
	v_pk_add_f32 v[56:57], v[4:5], v[4:5] op_sel_hi:[0,1]
	v_pk_mul_f32 v[4:5], v[52:53], v[52:53]
	v_pk_mul_f32 v[32:33], v[30:31], v[30:31]
	v_fmac_f32_e32 v10, 0xba000000, v96
	v_pk_mov_b32 v[92:93], v[32:33], v[4:5] op_sel:[1,0]
	v_mov_b32_e32 v33, v5
	v_fmamk_f32 v12, v96, 0xba000000, v12
	v_fmamk_f32 v11, v96, 0xba000000, v11
	v_mul_f32_e32 v2, v10, v10
	v_pk_add_f32 v[4:5], v[92:93], v[32:33]
	v_fmamk_f32 v13, v96, 0xba000000, v13
	v_pk_fma_f32 v[92:93], v[10:11], v[10:11], v[2:3] op_sel_hi:[1,1,0]
	v_mul_f32_e32 v2, v12, v12
	v_pk_add_f32 v[32:33], v[4:5], v[4:5] op_sel_hi:[0,1]
	v_pk_fma_f32 v[94:95], v[12:13], v[12:13], v[2:3] op_sel_hi:[1,1,0]
	v_fmamk_f32 v5, v96, 0xba000000, v9
	v_fmamk_f32 v4, v96, 0xba000000, v8
	v_fmamk_f32 v7, v96, 0xba000000, v7
	v_fmac_f32_e32 v6, 0xba000000, v96
	v_mul_f32_e32 v92, v6, v6
	v_mul_f32_e32 v94, v7, v7
	v_mul_f32_e32 v32, v4, v4
	v_mul_f32_e32 v56, v5, v5
	v_pk_add_f32 v[8:9], v[92:93], v[94:95]
	v_pk_add_f32 v[32:33], v[32:33], v[56:57]
	v_lshl_add_u32 v76, s6, 4, v82
	v_pk_add_f32 v[8:9], v[8:9], v[32:33]
	ds_read_b128 v[92:95], v76
	ds_read_b128 v[96:99], v76 offset:8192
	v_add_f32_e32 v2, v8, v9
	ds_bpermute_b32 v8, v83, v2
	s_waitcnt lgkmcnt(0)
	v_add_f32_e32 v2, v2, v8
	ds_bpermute_b32 v8, v84, v2
	s_waitcnt lgkmcnt(0)
	v_add_f32_e32 v2, v2, v8
	ds_bpermute_b32 v8, v85, v2
	s_waitcnt lgkmcnt(0)
	v_add_f32_e32 v2, v2, v8
	ds_bpermute_b32 v8, v86, v2
	s_waitcnt lgkmcnt(0)
	v_add_f32_e32 v2, v2, v8
	ds_bpermute_b32 v8, v87, v2
	s_waitcnt lgkmcnt(0)
	v_add_f32_e32 v2, v2, v8
	ds_bpermute_b32 v8, v88, v2
	s_waitcnt lgkmcnt(0)
; #define LAS __attribute__((address_space(3)))
; __device__ __forceinline__ unsigned pk_bf16(float lo, float hi) { const bf16x2_t r = __builtin_convertvector((f32x2){lo, hi}, bf16x2_t); return __builtin_bit_cast(unsigned, r); }
; __device__ __forceinline__ unsigned pk4_fp8(float a, float b, float c, float d) { int w = 0; w = __builtin_amdgcn_cvt_pk_fp8_f32(clamp8(a), clamp8(b), w, false); w = __builtin_amdgcn_cvt_pk_fp8_f32(clamp8(c), clamp8(d), w, true); return (unsigned)w; }
; __device__ __forceinline__ void ph2(LAS unsigned char* lds, int tid, int lane, int wave, int G, int bid) {
;     ...
;         const float rstd = 1.f / sqrtf(wave_sum(s2) * (1.f / D) + LN_EPS);
;         const LAS f32x4* shq = MV + bsel * 1024 + lane; const LAS f32x4* scq = shq + 512; u32x2* o8 = (u32x2*)orow + lane;
;         unsigned char* o4 = ws + WS_RA + ((size_t)((m < T ? m : 0) >> 8) * 16 << 15) + ((size_t)(m & 255) << 7) + ((lane >> 5) << 15) + 4 * (lane & 31);
; #pragma unroll
;         for (int j = 0; j < 8; ++j) { const f32x4 sh = shq[64 * j], sc = scq[64 * j]; const f32x4 y = v[j] * rstd * sc + sh; if (m < T) *(unsigned*)(o4 + ((size_t)(2 * j) << 15)) = pk4_fp8(y.x, y.y, y.z, y.w); else o8[64 * j] = (u32x2){pk_bf16(y.x, y.y), pk_bf16(y.z, y.w)}; }
	v_add_f32_e32 v2, v2, v8
	v_fmamk_f32 v2, v2, 0x3a000000, v89
	v_mul_f32_e32 v8, 0x4f800000, v2
	v_cmp_gt_f32_e32 vcc, s41, v2
	s_nop 1
	v_cndmask_b32_e32 v2, v2, v8, vcc
	v_sqrt_f32_e32 v8, v2
	s_nop 0
	v_add_u32_e32 v9, -1, v8
	v_fma_f32 v32, -v9, v8, v2
	v_cmp_ge_f32_e64 s[0:1], 0, v32
	v_add_u32_e32 v32, 1, v8
	s_nop 0
	v_cndmask_b32_e64 v9, v8, v9, s[0:1]
	v_fma_f32 v8, -v32, v8, v2
	v_cmp_lt_f32_e64 s[0:1], 0, v8
	s_nop 1
	v_cndmask_b32_e64 v8, v9, v32, s[0:1]
	v_mul_f32_e32 v9, 0x37800000, v8
	v_cndmask_b32_e32 v8, v8, v9, vcc
	v_cmp_class_f32_e32 vcc, v2, v90
	s_nop 1
	v_cndmask_b32_e32 v2, v8, v2, vcc
	v_div_scale_f32 v8, s[0:1], v2, v2, 1.0
	v_rcp_f32_e32 v9, v8
	s_lshr_b32 s0, s19, 4
	s_and_b32 s6, s0, 0x7fffff0
	s_and_b64 s[0:1], s[10:11], exec
	v_fma_f32 v32, -v8, v9, 1.0
	v_fmac_f32_e32 v9, v32, v9
	v_div_scale_f32 v32, vcc, 1.0, v2, 1.0
	v_mul_f32_e32 v33, v32, v9
	v_fma_f32 v56, -v8, v33, v32
	v_fmac_f32_e32 v33, v56, v9
	s_cselect_b32 s6, s6, 0
	v_fma_f32 v8, -v8, v33, v32
	s_lshl_b64 s[0:1], s[6:7], 15
	v_div_fmas_f32 v8, v8, v9, v33
	s_add_u32 s0, s24, s0
	v_div_fixup_f32 v32, v8, v2, 1.0
	s_addc_u32 s1, s25, s1
	s_and_b32 s6, s28, 0x7f80
	v_lshlrev_b32_e32 v2, 3, v170
	s_add_u32 s0, s0, s6
	v_pk_mul_f32 v[56:57], v[66:67], v[32:33] op_sel_hi:[1,0]
	v_pk_mul_f32 v[66:67], v[80:81], v[32:33] op_sel_hi:[1,0]
	v_lshl_add_u64 v[8:9], s[12:13], 0, v[2:3]
	s_addc_u32 s1, s1, 0
	v_pk_fma_f32 v[66:67], v[98:99], v[66:67], v[94:95]
	v_pk_fma_f32 v[80:81], v[96:97], v[56:57], v[92:93]
	s_mov_b64 s[10:11], -1
	s_and_b64 vcc, exec, s[8:9]
	s_cbranch_vccz .LBB0_278
	v_cvt_pk_bf16_f32 v56, v80, v81
	v_cvt_pk_bf16_f32 v57, v66, v67
	global_store_dwordx2 v[8:9], v[56:57], off
	s_mov_b64 s[10:11], 0
.LBB0_278:
	v_lshl_add_u64 v[56:57], s[0:1], 0, v[70:71]
	s_andn2_b64 vcc, exec, s[10:11]
	v_lshl_add_u64 v[56:57], v[56:57], 0, v[72:73]
	s_cbranch_vccnz .LBB0_280
	v_med3_f32 v2, v80, s42, v91
	v_med3_f32 v33, v81, s42, v91
	v_mov_b32_e32 v63, v3
	v_cvt_pk_fp8_f32 v63, v2, v33
	v_med3_f32 v2, v66, s42, v91
	v_med3_f32 v33, v67, s42, v91
	v_cvt_pk_fp8_f32 v63, v2, v33 op_sel:[0,0,1]
	global_store_dword v[56:57], v63, off
.LBB0_280:
	v_mov_b32_e32 v63, v79
	ds_read_b128 v[78:81], v76 offset:1024
	ds_read_b128 v[92:95], v76 offset:9216
	v_mov_b32_e32 v33, v32
	v_mov_b32_e32 v66, v32
	v_mov_b32_e32 v67, v32
	v_mov_b32_e32 v74, v77
	v_pk_mul_f32 v[66:67], v[74:75], v[66:67]
	v_pk_mul_f32 v[74:75], v[62:63], v[32:33]
	v_cndmask_b32_e64 v2, 0, 1, s[8:9]
	s_waitcnt lgkmcnt(0)
	v_pk_fma_f32 v[62:63], v[66:67], v[94:95], v[80:81]
	v_pk_fma_f32 v[66:67], v[74:75], v[92:93], v[78:79]
	v_cmp_ne_u32_e64 s[0:1], 1, v2
	s_andn2_b64 vcc, exec, s[8:9]
	s_mov_b64 s[8:9], -1
	s_cbranch_vccnz .LBB0_282
	v_cvt_pk_bf16_f32 v74, v66, v67
	v_cvt_pk_bf16_f32 v75, v62, v63
	s_mov_b64 s[8:9], 0
	global_store_dwordx2 v[8:9], v[74:75], off offset:512
.LBB0_282:
	s_andn2_b64 vcc, exec, s[8:9]
	s_cbranch_vccnz .LBB0_284
	v_med3_f32 v2, v66, s42, v91
	v_med3_f32 v66, v67, s42, v91
	v_mov_b32_e32 v67, v3
	v_cvt_pk_fp8_f32 v67, v2, v66
	v_med3_f32 v2, v62, s42, v91
	v_med3_f32 v62, v63, s42, v91
	v_cvt_pk_fp8_f32 v67, v2, v62 op_sel:[0,0,1]
	v_add_co_u32_e32 v62, vcc, 0x10000, v56
	s_nop 1
	v_addc_co_u32_e32 v63, vcc, 0, v57, vcc
	global_store_dword v[62:63], v67, off
.LBB0_284:
	ds_read_b128 v[78:81], v76 offset:2048
	ds_read_b128 v[92:95], v76 offset:10240
	v_mov_b32_e32 v62, v32
	v_mov_b32_e32 v63, v32
	v_pk_mul_f32 v[62:63], v[68:69], v[62:63]
	v_pk_mul_f32 v[66:67], v[58:59], v[32:33]
	s_waitcnt lgkmcnt(0)
	v_pk_fma_f32 v[58:59], v[62:63], v[94:95], v[80:81]
	v_pk_fma_f32 v[62:63], v[66:67], v[92:93], v[78:79]
	s_and_b64 vcc, exec, s[0:1]
	s_mov_b64 s[8:9], -1
	s_cbranch_vccnz .LBB0_286
	v_cvt_pk_bf16_f32 v66, v62, v63
	v_cvt_pk_bf16_f32 v67, v58, v59
	s_mov_b64 s[8:9], 0
	global_store_dwordx2 v[8:9], v[66:67], off offset:1024
.LBB0_286:
	s_andn2_b64 vcc, exec, s[8:9]
	s_cbranch_vccnz .LBB0_288
	v_med3_f32 v2, v62, s42, v91
	v_med3_f32 v62, v63, s42, v91
	v_mov_b32_e32 v63, v3
	v_cvt_pk_fp8_f32 v63, v2, v62
	v_med3_f32 v2, v58, s42, v91
	v_med3_f32 v58, v59, s42, v91
	v_cvt_pk_fp8_f32 v63, v2, v58 op_sel:[0,0,1]
	v_add_co_u32_e32 v58, vcc, 0x20000, v56
	s_nop 1
	v_addc_co_u32_e32 v59, vcc, 0, v57, vcc
	global_store_dword v[58:59], v63, off
.LBB0_288:
	ds_read_b128 v[66:69], v76 offset:3072
	ds_read_b128 v[78:81], v76 offset:11264
	v_mov_b32_e32 v58, v32
	v_mov_b32_e32 v59, v32
	v_pk_mul_f32 v[58:59], v[64:65], v[58:59]
	v_pk_mul_f32 v[62:63], v[54:55], v[32:33]
	s_waitcnt lgkmcnt(0)
	v_pk_fma_f32 v[54:55], v[58:59], v[80:81], v[68:69]
	v_pk_fma_f32 v[58:59], v[62:63], v[78:79], v[66:67]
	s_and_b64 vcc, exec, s[0:1]
	s_mov_b64 s[8:9], -1
	s_cbranch_vccnz .LBB0_290
	v_cvt_pk_bf16_f32 v62, v58, v59
	v_cvt_pk_bf16_f32 v63, v54, v55
	s_mov_b64 s[8:9], 0
	global_store_dwordx2 v[8:9], v[62:63], off offset:1536
; __device__ __forceinline__ unsigned pk_bf16(float lo, float hi) { const bf16x2_t r = __builtin_convertvector((f32x2){lo, hi}, bf16x2_t); return __builtin_bit_cast(unsigned, r); }
; __device__ __forceinline__ unsigned pk4_fp8(float a, float b, float c, float d) { int w = 0; w = __builtin_amdgcn_cvt_pk_fp8_f32(clamp8(a), clamp8(b), w, false); w = __builtin_amdgcn_cvt_pk_fp8_f32(clamp8(c), clamp8(d), w, true); return (unsigned)w; }
; __device__ __forceinline__ void ph2(LAS unsigned char* lds, int tid, int lane, int wave, int G, int bid) {
;     ...
; #pragma unroll
;         for (int j = 0; j < 8; ++j) { const f32x4 sh = shq[64 * j], sc = scq[64 * j]; const f32x4 y = v[j] * rstd * sc + sh; if (m < T) *(unsigned*)(o4 + ((size_t)(2 * j) << 15)) = pk4_fp8(y.x, y.y, y.z, y.w); else o8[64 * j] = (u32x2){pk_bf16(y.x, y.y), pk_bf16(y.z, y.w)}; }
.LBB0_290:
	s_andn2_b64 vcc, exec, s[8:9]
	s_cbranch_vccnz .LBB0_292
	v_med3_f32 v2, v58, s42, v91
	v_med3_f32 v58, v59, s42, v91
	v_mov_b32_e32 v59, v3
	v_cvt_pk_fp8_f32 v59, v2, v58
	v_med3_f32 v2, v54, s42, v91
	v_med3_f32 v54, v55, s42, v91
	v_cvt_pk_fp8_f32 v59, v2, v54 op_sel:[0,0,1]
	v_add_co_u32_e32 v54, vcc, 0x30000, v56
	s_nop 1
	v_addc_co_u32_e32 v55, vcc, 0, v57, vcc
	global_store_dword v[54:55], v59, off
.LBB0_292:
	ds_read_b128 v[62:65], v76 offset:4096
	ds_read_b128 v[66:69], v76 offset:12288
	v_mov_b32_e32 v54, v32
	v_mov_b32_e32 v55, v32
	v_pk_mul_f32 v[54:55], v[60:61], v[54:55]
	v_pk_mul_f32 v[58:59], v[50:51], v[32:33]
	s_waitcnt lgkmcnt(0)
	v_pk_fma_f32 v[50:51], v[54:55], v[68:69], v[64:65]
	v_pk_fma_f32 v[54:55], v[58:59], v[66:67], v[62:63]
	s_and_b64 vcc, exec, s[0:1]
	s_mov_b64 s[8:9], -1
	s_cbranch_vccnz .LBB0_294
	v_cvt_pk_bf16_f32 v58, v54, v55
	v_cvt_pk_bf16_f32 v59, v50, v51
	s_mov_b64 s[8:9], 0
	global_store_dwordx2 v[8:9], v[58:59], off offset:2048
.LBB0_294:
	s_andn2_b64 vcc, exec, s[8:9]
	s_cbranch_vccnz .LBB0_296
	v_med3_f32 v2, v54, s42, v91
	v_med3_f32 v54, v55, s42, v91
	v_mov_b32_e32 v55, v3
	v_cvt_pk_fp8_f32 v55, v2, v54
	v_med3_f32 v2, v50, s42, v91
	v_med3_f32 v50, v51, s42, v91
	v_cvt_pk_fp8_f32 v55, v2, v50 op_sel:[0,0,1]
	v_add_co_u32_e32 v50, vcc, 0x40000, v56
	s_nop 1
	v_addc_co_u32_e32 v51, vcc, 0, v57, vcc
	global_store_dword v[50:51], v55, off
.LBB0_296:
	ds_read_b128 v[58:61], v76 offset:5120
	ds_read_b128 v[62:65], v76 offset:13312
	v_mov_b32_e32 v50, v32
	v_mov_b32_e32 v51, v32
	v_pk_mul_f32 v[50:51], v[52:53], v[50:51]
	v_pk_mul_f32 v[52:53], v[30:31], v[32:33]
	s_waitcnt lgkmcnt(0)
	v_pk_fma_f32 v[30:31], v[50:51], v[64:65], v[60:61]
	v_pk_fma_f32 v[50:51], v[52:53], v[62:63], v[58:59]
	s_and_b64 vcc, exec, s[0:1]
	s_mov_b64 s[8:9], -1
	s_cbranch_vccnz .LBB0_298
	v_cvt_pk_bf16_f32 v52, v50, v51
	v_cvt_pk_bf16_f32 v53, v30, v31
	s_mov_b64 s[8:9], 0
	global_store_dwordx2 v[8:9], v[52:53], off offset:2560
.LBB0_298:
	s_andn2_b64 vcc, exec, s[8:9]
	s_cbranch_vccnz .LBB0_300
	v_med3_f32 v2, v50, s42, v91
	v_med3_f32 v50, v51, s42, v91
	v_mov_b32_e32 v51, v3
	v_cvt_pk_fp8_f32 v51, v2, v50
	v_med3_f32 v2, v30, s42, v91
	v_med3_f32 v30, v31, s42, v91
	v_cvt_pk_fp8_f32 v51, v2, v30 op_sel:[0,0,1]
	v_add_co_u32_e32 v30, vcc, 0x50000, v56
	s_nop 1
	v_addc_co_u32_e32 v31, vcc, 0, v57, vcc
	global_store_dword v[30:31], v51, off
.LBB0_300:
	ds_read_b128 v[50:53], v76 offset:6144
	ds_read_b128 v[58:61], v76 offset:14336
	v_mov_b32_e32 v30, v32
	v_mov_b32_e32 v31, v32
	v_pk_mul_f32 v[12:13], v[12:13], v[30:31]
	v_pk_mul_f32 v[30:31], v[10:11], v[32:33]
	s_waitcnt lgkmcnt(0)
	v_pk_fma_f32 v[10:11], v[12:13], v[60:61], v[52:53]
	v_pk_fma_f32 v[12:13], v[30:31], v[58:59], v[50:51]
	s_and_b64 vcc, exec, s[0:1]
	s_mov_b64 s[8:9], -1
	s_cbranch_vccnz .LBB0_302
	v_cvt_pk_bf16_f32 v30, v12, v13
	v_cvt_pk_bf16_f32 v31, v10, v11
	s_mov_b64 s[8:9], 0
	global_store_dwordx2 v[8:9], v[30:31], off offset:3072
.LBB0_302:
	s_andn2_b64 vcc, exec, s[8:9]
	s_cbranch_vccnz .LBB0_304
	v_med3_f32 v2, v12, s42, v91
	v_med3_f32 v12, v13, s42, v91
	v_mov_b32_e32 v13, v3
	v_cvt_pk_fp8_f32 v13, v2, v12
	v_med3_f32 v2, v10, s42, v91
	v_med3_f32 v10, v11, s42, v91
	v_cvt_pk_fp8_f32 v13, v2, v10 op_sel:[0,0,1]
	v_add_co_u32_e32 v10, vcc, 0x60000, v56
	s_nop 1
	v_addc_co_u32_e32 v11, vcc, 0, v57, vcc
	global_store_dword v[10:11], v13, off
.LBB0_304:
	ds_read_b128 v[10:13], v76 offset:7168
	ds_read_b128 v[50:53], v76 offset:15360
	v_mov_b32_e32 v30, v32
	v_mov_b32_e32 v31, v32
	v_pk_mul_f32 v[4:5], v[4:5], v[30:31]
	v_pk_mul_f32 v[6:7], v[6:7], v[32:33]
	s_waitcnt lgkmcnt(0)
	v_pk_fma_f32 v[4:5], v[4:5], v[52:53], v[12:13]
	v_pk_fma_f32 v[6:7], v[6:7], v[50:51], v[10:11]
	s_and_b64 vcc, exec, s[0:1]
	s_mov_b64 s[0:1], -1
	s_cbranch_vccnz .LBB0_306
	v_cvt_pk_bf16_f32 v10, v6, v7
	v_cvt_pk_bf16_f32 v11, v4, v5
	s_mov_b64 s[0:1], 0
	global_store_dwordx2 v[8:9], v[10:11], off offset:3584
.LBB0_306:
	s_andn2_b64 vcc, exec, s[0:1]
	s_cbranch_vccnz .LBB0_264
	v_med3_f32 v2, v6, s42, v91
	v_med3_f32 v6, v7, s42, v91
	v_mov_b32_e32 v7, v3
	v_cvt_pk_fp8_f32 v7, v2, v6
	v_med3_f32 v2, v4, s42, v91
	v_med3_f32 v4, v5, s42, v91
	v_cvt_pk_fp8_f32 v7, v2, v4 op_sel:[0,0,1]
	v_add_co_u32_e32 v4, vcc, 0x70000, v56
	s_nop 1
	v_addc_co_u32_e32 v5, vcc, 0, v57, vcc
	global_store_dword v[4:5], v7, off
	s_branch .LBB0_264

; __device__ __forceinline__ void ph10(LAS unsigned char* lds, int tid, int lane, int wave, int G, int bid) {
;     ...
;     auto load_row = [&](size_t gtok, f32x4 (&xv)[8], unsigned (&mv_)[8]) {
;         const f32x4* xin = XIN4 + gtok * (D / 4); const unsigned* mgq = MG2 + gtok * (D / 4);
; #pragma unroll
;         for (int j = 0; j < 8; ++j) { mv_[j] = __builtin_nontemporal_load(mgq + 64 * j); xv[j] = __builtin_nontemporal_load(xin + 64 * j); } };
;     ...
;     for (int batch = bid; batch < 256; batch += G) {
;         if (tid < 32) lcnt[tid] = 0;
;         { const float* mv = modv + (size_t)((batch * 128) >> 13) * 12288;
;           for (int i = tid; i < 4 * 512; i += NWAVES * 64) { const int r = i >> 9, q = i & 511;
;               f32x4 t = *((const f32x4*)(r == 0 ? ln1g : r == 1 ? ln1b : r == 2 ? mv + 4 * D : mv + 3 * D) + q); if (r == 2) t = t + 1.0f; VEC[i] = t; } }
;         __syncthreads();
;         const size_t tokB = (size_t)batch * 128 + 2 * wave;
;         f32x4 xa[8], xb[8]; unsigned ma[8], mb[8];
;         load_row(tokB, xa, ma);
.LBB0_971:
	s_cmpk_eq_i32 s16, 0x400
	s_cselect_b64 vcc, -1, 0
	s_and_b64 s[10:11], vcc, exec
	s_cselect_b32 s10, s66, 0x6000
	s_add_u32 s10, s14, s10
	s_addc_u32 s11, s15, 0
	s_cmpk_eq_i32 s16, 0x200
	v_add_u32_e32 v99, s16, v0
	s_cselect_b32 s10, s58, s10
	s_cselect_b32 s11, s59, s11
	v_mov_b32_e32 v100, s47
	v_mov_b32_e32 v102, s45
	v_mov_b32_e32 v101, s11
	v_mov_b32_e32 v103, s10
	v_cmp_gt_u32_e64 s[10:11], s65, v99
	s_addk_i32 s16, 0x200
	v_add_u32_e32 v99, s16, v0
	v_cndmask_b32_e64 v101, v101, v100, s[10:11]
	v_cndmask_b32_e64 v100, v103, v102, s[10:11]
	v_lshl_add_u64 v[100:101], v[100:101], 0, v[162:163]
	flat_load_dwordx4 v[100:103], v[100:101]
	v_add_u32_e32 v99, 0xfffffe00, v99
	v_cmp_lt_u32_e64 s[10:11], s67, v99
	s_or_b64 s[12:13], s[10:11], s[12:13]
	s_waitcnt vmcnt(0) lgkmcnt(0)
	v_pk_add_f32 v[104:105], v[102:103], 1.0 op_sel_hi:[1,0]
	v_pk_add_f32 v[106:107], v[100:101], 1.0 op_sel_hi:[1,0]
	v_cndmask_b32_e32 v103, v103, v105, vcc
	v_cndmask_b32_e32 v101, v101, v107, vcc
	v_cndmask_b32_e32 v100, v100, v106, vcc
	v_cndmask_b32_e32 v102, v102, v104, vcc
	ds_write_b128 v98, v[100:103]
	v_add_u32_e32 v98, 0x2000, v98
	s_andn2_b64 exec, exec, s[12:13]
	s_cbranch_execnz .LBB0_971
	s_or_b64 exec, exec, s[12:13]
	s_ashr_i32 s49, s48, 31
	s_lshl_b64 s[10:11], s[48:49], 7
	s_add_u32 s50, s10, s63
	s_addc_u32 s51, s11, 0
	s_lshl_b64 s[10:11], s[50:51], 13
	v_lshl_add_u64 v[114:115], v[164:165], 0, s[10:11]
	s_lshl_b64 s[10:11], s[50:51], 11
	v_add_co_u32_e32 v126, vcc, s68, v114
	v_lshl_add_u64 v[122:123], v[166:167], 0, s[10:11]
	s_nop 0
	v_addc_co_u32_e32 v127, vcc, 0, v115, vcc
	s_waitcnt lgkmcnt(0)
	s_barrier
	global_load_dwordx4 v[98:101], v[114:115], off nt
	global_load_dwordx4 v[102:105], v[114:115], off offset:1024 nt
	global_load_dwordx4 v[106:109], v[114:115], off offset:2048 nt
	global_load_dwordx4 v[110:113], v[114:115], off offset:3072 nt
	s_nop 0
	global_load_dwordx4 v[114:117], v[126:127], off nt
	global_load_dwordx4 v[118:121], v[126:127], off offset:1024 nt
	global_load_dword v215, v[122:123], off nt
	global_load_dword v216, v[122:123], off offset:256 nt
	global_load_dword v217, v[122:123], off offset:512 nt
	global_load_dword v218, v[122:123], off offset:768 nt
	global_load_dword v219, v[122:123], off offset:1024 nt
	global_load_dword v220, v[122:123], off offset:1280 nt
	global_load_dword v221, v[122:123], off offset:1536 nt
	global_load_dword v222, v[122:123], off offset:1792 nt
	s_nop 0
	global_load_dwordx4 v[122:125], v[126:127], off offset:2048 nt
	s_nop 0
	global_load_dwordx4 v[126:129], v[126:127], off offset:3072 nt
	s_mov_b32 s49, 0
	s_branch .LBB0_974

; __device__ __forceinline__ void ph10(LAS unsigned char* lds, int tid, int lane, int wave, int G, int bid) {
;     ...
;     auto do_row = [&](f32x4 (&v)[8], const unsigned (&mg)[8], size_t gtok, int row) {
;         u32x2* xq = (u32x2*)(XM + gtok * D) + lane; float s = 0.f;
; #pragma unroll
;         for (int j = 0; j < 8; ++j) { const f32x2 m0 = __builtin_amdgcn_cvt_pk_f32_fp8((int)mg[j], false), m1 = __builtin_amdgcn_cvt_pk_f32_fp8((int)mg[j], true);
;             v[j] = v[j] * DN_ALPHA + (f32x4){m0.x, m0.y, m1.x, m1.y} * MG8_INV; s += (v[j].x + v[j].y) + (v[j].z + v[j].w); }
;         float mean = wave_sum(s) * (1.f / D), s2 = 0.f;
.LBB0_974:
	s_waitcnt vmcnt(0) lgkmcnt(0)
	v_cvt_pk_f32_fp8_e32 v[130:131], v215
	v_cvt_pk_f32_fp8_sdwa v[132:133], v215 src0_sel:WORD_1
	v_cvt_pk_f32_fp8_e32 v[134:135], v216
	v_cvt_pk_f32_fp8_sdwa v[136:137], v216 src0_sel:WORD_1
	v_pk_mul_f32 v[130:131], v[130:131], s[44:45] op_sel_hi:[1,0]
	v_pk_mul_f32 v[132:133], v[132:133], s[44:45] op_sel_hi:[1,0]
	v_pk_fma_f32 v[98:99], v[98:99], s[46:47], v[130:131] op_sel_hi:[1,0,1]
	v_pk_mul_f32 v[130:131], v[134:135], s[44:45] op_sel_hi:[1,0]
	v_pk_fma_f32 v[100:101], v[100:101], s[46:47], v[132:133] op_sel_hi:[1,0,1]
	v_pk_mul_f32 v[132:133], v[136:137], s[44:45] op_sel_hi:[1,0]
	v_pk_fma_f32 v[102:103], v[102:103], s[46:47], v[130:131] op_sel_hi:[1,0,1]
	v_pk_fma_f32 v[104:105], v[104:105], s[46:47], v[132:133] op_sel_hi:[1,0,1]
	v_mov_b32_e32 v130, v98
	v_mov_b32_e32 v131, v102
	v_mov_b32_e32 v132, v99
	v_mov_b32_e32 v133, v103
	v_pk_add_f32 v[130:131], v[130:131], v[132:133]
	v_mov_b32_e32 v132, v100
	v_mov_b32_e32 v133, v104
	v_mov_b32_e32 v134, v101
	v_mov_b32_e32 v135, v105
	v_pk_add_f32 v[132:133], v[132:133], v[134:135]
	v_cvt_pk_f32_fp8_sdwa v[134:135], v217 src0_sel:WORD_1
	v_pk_add_f32 v[130:131], v[130:131], v[132:133]
	v_cvt_pk_f32_fp8_e32 v[132:133], v217
	v_cvt_pk_f32_fp8_e32 v[136:137], v218
	v_cvt_pk_f32_fp8_sdwa v[138:139], v218 src0_sel:WORD_1
	v_pk_mul_f32 v[134:135], v[134:135], s[44:45] op_sel_hi:[1,0]
	v_pk_mul_f32 v[132:133], v[132:133], s[44:45] op_sel_hi:[1,0]
	v_pk_fma_f32 v[108:109], v[108:109], s[46:47], v[134:135] op_sel_hi:[1,0,1]
	v_pk_fma_f32 v[106:107], v[106:107], s[46:47], v[132:133] op_sel_hi:[1,0,1]
	v_mov_b32_e32 v135, v109
	v_pk_mov_b32 v[132:133], v[106:107], v[108:109] op_sel:[1,0]
	v_mov_b32_e32 v134, v106
	v_pk_add_f32 v[132:133], v[132:133], v[134:135]
	v_pk_mul_f32 v[134:135], v[136:137], s[44:45] op_sel_hi:[1,0]
	v_pk_mul_f32 v[136:137], v[138:139], s[44:45] op_sel_hi:[1,0]
	v_pk_fma_f32 v[110:111], v[110:111], s[46:47], v[134:135] op_sel_hi:[1,0,1]
	v_pk_fma_f32 v[112:113], v[112:113], s[46:47], v[136:137] op_sel_hi:[1,0,1]
	v_cvt_pk_f32_fp8_e32 v[134:135], v219
	v_cvt_pk_f32_fp8_sdwa v[136:137], v219 src0_sel:WORD_1
	v_add_f32_e32 v130, 0, v130
	v_pk_add_f32 v[132:133], v[132:133], v[132:133] op_sel:[0,1] op_sel_hi:[1,0]
	v_pk_mul_f32 v[134:135], v[134:135], s[44:45] op_sel_hi:[1,0]
	v_pk_mul_f32 v[136:137], v[136:137], s[44:45] op_sel_hi:[1,0]
	v_pk_fma_f32 v[114:115], v[114:115], s[46:47], v[134:135] op_sel_hi:[1,0,1]
	v_pk_fma_f32 v[116:117], v[116:117], s[46:47], v[136:137] op_sel_hi:[1,0,1]
	v_cvt_pk_f32_fp8_e32 v[134:135], v220
	v_cvt_pk_f32_fp8_sdwa v[136:137], v220 src0_sel:WORD_1
	v_add_f32_e32 v130, v130, v131
	v_add_f32_e32 v138, v110, v111
	v_add_f32_e32 v140, v112, v113
	v_mov_b32_e32 v131, v114
	v_mov_b32_e32 v133, v115
	v_mov_b32_e32 v139, v116
	v_mov_b32_e32 v141, v117
	v_pk_add_f32 v[130:131], v[130:131], v[132:133]
	v_pk_add_f32 v[132:133], v[138:139], v[140:141]
	v_cvt_pk_f32_fp8_sdwa v[138:139], v221 src0_sel:WORD_1
	v_pk_add_f32 v[130:131], v[130:131], v[132:133]
	v_pk_mul_f32 v[132:133], v[134:135], s[44:45] op_sel_hi:[1,0]
	v_pk_mul_f32 v[134:135], v[136:137], s[44:45] op_sel_hi:[1,0]
	v_cvt_pk_f32_fp8_e32 v[136:137], v221
	v_pk_fma_f32 v[120:121], v[120:121], s[46:47], v[134:135] op_sel_hi:[1,0,1]
	v_pk_fma_f32 v[118:119], v[118:119], s[46:47], v[132:133] op_sel_hi:[1,0,1]
	v_mov_b32_e32 v135, v121
	v_pk_mov_b32 v[132:133], v[118:119], v[120:121] op_sel:[1,0]
	v_mov_b32_e32 v134, v118
	v_pk_add_f32 v[132:133], v[132:133], v[134:135]
	v_pk_mul_f32 v[134:135], v[136:137], s[44:45] op_sel_hi:[1,0]
	v_pk_mul_f32 v[136:137], v[138:139], s[44:45] op_sel_hi:[1,0]
	v_pk_fma_f32 v[122:123], v[122:123], s[46:47], v[134:135] op_sel_hi:[1,0,1]
	v_pk_fma_f32 v[124:125], v[124:125], s[46:47], v[136:137] op_sel_hi:[1,0,1]
	v_cvt_pk_f32_fp8_e32 v[134:135], v222
	v_cvt_pk_f32_fp8_sdwa v[136:137], v222 src0_sel:WORD_1
	v_pk_add_f32 v[130:131], v[130:131], v[130:131] op_sel:[0,1] op_sel_hi:[1,0]
	v_pk_add_f32 v[132:133], v[132:133], v[132:133] op_sel:[0,1] op_sel_hi:[1,0]
	v_pk_mul_f32 v[134:135], v[134:135], s[44:45] op_sel_hi:[1,0]
	v_pk_mul_f32 v[136:137], v[136:137], s[44:45] op_sel_hi:[1,0]
	v_pk_fma_f32 v[126:127], v[126:127], s[46:47], v[134:135] op_sel_hi:[1,0,1]
	v_pk_fma_f32 v[128:129], v[128:129], s[46:47], v[136:137] op_sel_hi:[1,0,1]
	v_add_f32_e32 v138, v122, v123
	v_add_f32_e32 v140, v124, v125
	v_mov_b32_e32 v131, v126
	v_mov_b32_e32 v133, v127
	v_mov_b32_e32 v139, v128
	v_mov_b32_e32 v141, v129
	v_pk_add_f32 v[130:131], v[130:131], v[132:133]
	v_pk_add_f32 v[132:133], v[138:139], v[140:141]
	s_lshl_b32 s18, s49, 4
	v_pk_add_f32 v[130:131], v[130:131], v[132:133]
	s_add_u32 s16, s50, s18
	v_add_f32_e32 v130, v130, v131
	ds_bpermute_b32 v131, v191, v130
	s_addc_u32 s17, s51, 0
	s_or_b32 s14, s16, 1
	s_mov_b32 s15, s17
	s_lshl_b64 s[10:11], s[14:15], 13
	s_waitcnt lgkmcnt(0)
	v_add_f32_e32 v130, v130, v131
	ds_bpermute_b32 v131, v192, v130
	s_lshl_b64 s[12:13], s[14:15], 11
	s_waitcnt lgkmcnt(0)
	v_add_f32_e32 v130, v130, v131
	ds_bpermute_b32 v131, v193, v130
	s_waitcnt lgkmcnt(0)
	v_add_f32_e32 v130, v130, v131
	ds_bpermute_b32 v131, v194, v130
	s_waitcnt lgkmcnt(0)
	v_add_f32_e32 v130, v130, v131
	ds_bpermute_b32 v131, v195, v130
	s_waitcnt lgkmcnt(0)
	v_add_f32_e32 v130, v130, v131
	ds_bpermute_b32 v131, v196, v130
	s_waitcnt lgkmcnt(0)
; __device__ __forceinline__ void ph10(LAS unsigned char* lds, int tid, int lane, int wave, int G, int bid) {
;     ...
;         float mean = wave_sum(s) * (1.f / D), s2 = 0.f;
; #pragma unroll
;         for (int j = 0; j < 8; ++j) { v[j] = v[j] - mean; s2 += (v[j].x * v[j].x + v[j].y * v[j].y) + (v[j].z * v[j].z + v[j].w * v[j].w); }
;         float rstd = 1.f / sqrtf(wave_sum(s2) * (1.f / D) + LN_EPS);
;     ...
;             load_row(g0 + 1, xb, mb);
	v_add_f32_e32 v138, v130, v131
	v_fmamk_f32 v99, v138, 0xba000000, v99
	v_fmamk_f32 v103, v138, 0xba000000, v103
	v_fmamk_f32 v101, v138, 0xba000000, v101
	v_fmac_f32_e32 v98, 0xba000000, v138
	v_fmamk_f32 v105, v138, 0xba000000, v105
	v_fmac_f32_e32 v102, 0xba000000, v138
	v_mov_b32_e32 v132, v99
	v_mov_b32_e32 v133, v103
	v_fmac_f32_e32 v100, 0xba000000, v138
	v_fmac_f32_e32 v104, 0xba000000, v138
	v_mov_b32_e32 v130, v98
	v_mov_b32_e32 v131, v102
	v_pk_mul_f32 v[132:133], v[132:133], v[132:133]
	v_mov_b32_e32 v134, v101
	v_mov_b32_e32 v135, v105
	v_pk_fma_f32 v[130:131], v[130:131], v[130:131], v[132:133]
	v_mov_b32_e32 v132, v100
	v_mov_b32_e32 v133, v104
	v_pk_mul_f32 v[134:135], v[134:135], v[134:135]
	v_fmamk_f32 v107, v138, 0xba000000, v107
	v_pk_fma_f32 v[132:133], v[132:133], v[132:133], v[134:135]
	v_fmac_f32_e32 v106, 0xba000000, v138
	v_pk_add_f32 v[130:131], v[130:131], v[132:133]
	v_fmamk_f32 v109, v138, 0xba000000, v109
	v_fmac_f32_e32 v108, 0xba000000, v138
	v_pk_add_f32 v[130:131], v[130:131], v[130:131] op_sel_hi:[0,1]
	v_pk_mul_f32 v[132:133], v[108:109], v[108:109]
	v_pk_mul_f32 v[134:135], v[106:107], v[106:107]
	v_fmac_f32_e32 v110, 0xba000000, v138
	v_pk_mov_b32 v[136:137], v[134:135], v[132:133] op_sel:[1,0]
	v_mov_b32_e32 v135, v133
	v_fmamk_f32 v111, v138, 0xba000000, v111
	v_fmac_f32_e32 v112, 0xba000000, v138
	v_mul_f32_e32 v130, v110, v110
	v_pk_add_f32 v[132:133], v[136:137], v[134:135]
	v_fmamk_f32 v113, v138, 0xba000000, v113
	v_pk_fma_f32 v[134:135], v[110:111], v[110:111], v[130:131] op_sel_hi:[1,1,0]
	v_mul_f32_e32 v130, v112, v112
	v_pk_add_f32 v[132:133], v[132:133], v[132:133] op_sel_hi:[0,1]
	v_pk_fma_f32 v[136:137], v[112:113], v[112:113], v[130:131] op_sel_hi:[1,1,0]
	v_fmamk_f32 v117, v138, 0xba000000, v117
	v_fmac_f32_e32 v116, 0xba000000, v138
	v_fmamk_f32 v115, v138, 0xba000000, v115
	v_fmac_f32_e32 v114, 0xba000000, v138
	v_mul_f32_e32 v134, v114, v114
	v_mul_f32_e32 v136, v115, v115
	v_mul_f32_e32 v132, v116, v116
	v_mul_f32_e32 v130, v117, v117
	v_pk_add_f32 v[134:135], v[134:135], v[136:137]
	v_pk_add_f32 v[130:131], v[132:133], v[130:131]
	v_fmamk_f32 v119, v138, 0xba000000, v119
	v_pk_add_f32 v[130:131], v[134:135], v[130:131]
	v_fmac_f32_e32 v118, 0xba000000, v138
	v_fmamk_f32 v121, v138, 0xba000000, v121
	v_fmac_f32_e32 v120, 0xba000000, v138
	v_pk_add_f32 v[130:131], v[130:131], v[130:131] op_sel_hi:[0,1]
	v_pk_mul_f32 v[132:133], v[120:121], v[120:121]
	v_pk_mul_f32 v[134:135], v[118:119], v[118:119]
	v_fmac_f32_e32 v122, 0xba000000, v138
	v_pk_mov_b32 v[136:137], v[134:135], v[132:133] op_sel:[1,0]
	v_mov_b32_e32 v135, v133
	v_fmamk_f32 v123, v138, 0xba000000, v123
	v_fmac_f32_e32 v124, 0xba000000, v138
	v_mul_f32_e32 v130, v122, v122
	v_pk_add_f32 v[132:133], v[136:137], v[134:135]
	v_fmamk_f32 v125, v138, 0xba000000, v125
	v_pk_fma_f32 v[134:135], v[122:123], v[122:123], v[130:131] op_sel_hi:[1,1,0]
	v_mul_f32_e32 v130, v124, v124
	v_pk_add_f32 v[132:133], v[132:133], v[132:133] op_sel_hi:[0,1]
	v_pk_fma_f32 v[136:137], v[124:125], v[124:125], v[130:131] op_sel_hi:[1,1,0]
	v_fmamk_f32 v129, v138, 0xba000000, v129
	v_fmac_f32_e32 v128, 0xba000000, v138
	v_fmamk_f32 v127, v138, 0xba000000, v127
	v_fmac_f32_e32 v126, 0xba000000, v138
	v_mul_f32_e32 v134, v126, v126
	v_mul_f32_e32 v136, v127, v127
	v_mul_f32_e32 v132, v128, v128
	v_mul_f32_e32 v130, v129, v129
	v_pk_add_f32 v[134:135], v[134:135], v[136:137]
	v_pk_add_f32 v[130:131], v[132:133], v[130:131]
	s_nop 0
	v_pk_add_f32 v[130:131], v[134:135], v[130:131]
	v_lshl_add_u64 v[134:135], v[166:167], 0, s[12:13]
	v_add_f32_e32 v130, v130, v131
	ds_bpermute_b32 v131, v191, v130
	s_waitcnt lgkmcnt(0)
	v_add_f32_e32 v130, v130, v131
	ds_bpermute_b32 v131, v192, v130
	s_waitcnt lgkmcnt(0)
	v_add_f32_e32 v130, v130, v131
	ds_bpermute_b32 v131, v193, v130
	s_waitcnt lgkmcnt(0)
	v_add_f32_e32 v132, v130, v131
	ds_bpermute_b32 v133, v194, v132
	v_lshl_add_u64 v[130:131], v[164:165], 0, s[10:11]
	v_add_co_u32_e32 v136, vcc, s68, v130
	global_load_dwordx4 v[158:161], v[130:131], off nt
	global_load_dwordx4 v[154:157], v[130:131], off offset:1024 nt
	global_load_dwordx4 v[150:153], v[130:131], off offset:2048 nt
	global_load_dwordx4 v[146:149], v[130:131], off offset:3072 nt
	s_waitcnt lgkmcnt(0)
	v_add_f32_e32 v132, v132, v133
	ds_bpermute_b32 v133, v195, v132
	v_addc_co_u32_e32 v137, vcc, 0, v131, vcc
	s_waitcnt lgkmcnt(0)
	v_add_f32_e32 v138, v132, v133
	ds_bpermute_b32 v139, v196, v138
	global_load_dwordx4 v[142:145], v[136:137], off nt
	global_load_dwordx4 v[130:133], v[136:137], off offset:1024 nt
	global_load_dword v186, v[134:135], off nt
	global_load_dword v185, v[134:135], off offset:256 nt
	global_load_dword v184, v[134:135], off offset:512 nt
	global_load_dword v183, v[134:135], off offset:768 nt
	global_load_dword v182, v[134:135], off offset:1024 nt
	global_load_dword v181, v[134:135], off offset:1280 nt
	global_load_dword v180, v[134:135], off offset:1536 nt
	global_load_dword v224, v[134:135], off offset:1792 nt
	s_waitcnt lgkmcnt(0)
; #define LAS __attribute__((address_space(3)))
; __device__ __forceinline__ unsigned pk_bf16(float lo, float hi) { const bf16x2_t r = __builtin_convertvector((f32x2){lo, hi}, bf16x2_t); return __builtin_bit_cast(unsigned, r); }
; __device__ __forceinline__ void ph10(LAS unsigned char* lds, int tid, int lane, int wave, int G, int bid) {
;     ...
;         float rstd = 1.f / sqrtf(wave_sum(s2) * (1.f / D) + LN_EPS);
;         const LAS f32x4* gq = VEC + lane; const LAS f32x4* bq = VEC + 512 + lane; s = 0.f;
; #pragma unroll
;         for (int j = 0; j < 8; ++j) { v[j] = v[j] * rstd * gq[64 * j] + bq[64 * j]; xq[64 * j] = (u32x2){pk_bf16(v[j].x, v[j].y), pk_bf16(v[j].z, v[j].w)}; s += (v[j].x + v[j].y) + (v[j].z + v[j].w); }
	v_add_f32_e32 v138, v138, v139
	v_fmamk_f32 v138, v138, 0x3a000000, v207
	v_mul_f32_e32 v139, 0x4f800000, v138
	v_cmp_gt_f32_e32 vcc, s69, v138
	s_nop 1
	v_cndmask_b32_e32 v138, v138, v139, vcc
	v_sqrt_f32_e32 v139, v138
	s_nop 0
	v_add_u32_e32 v134, -1, v139
	v_fma_f32 v135, -v134, v139, v138
	v_cmp_ge_f32_e64 s[10:11], 0, v135
	v_add_u32_e32 v135, 1, v139
	s_nop 0
	v_cndmask_b32_e64 v134, v139, v134, s[10:11]
	v_fma_f32 v139, -v135, v139, v138
	v_cmp_lt_f32_e64 s[10:11], 0, v139
	s_nop 1
	v_cndmask_b32_e64 v134, v134, v135, s[10:11]
	v_mul_f32_e32 v135, 0x37800000, v134
	v_cndmask_b32_e32 v134, v134, v135, vcc
	v_cmp_class_f32_e32 vcc, v138, v208
	s_nop 1
	v_cndmask_b32_e32 v187, v134, v138, vcc
	v_div_scale_f32 v188, s[10:11], v187, v187, 1.0
	v_rcp_f32_e32 v189, v188
	global_load_dwordx4 v[138:141], v[136:137], off offset:2048 nt
	s_nop 0
	global_load_dwordx4 v[134:137], v[136:137], off offset:3072 nt
	s_lshl_b64 s[10:11], s[16:17], 12
	v_lshl_add_u64 v[178:179], v[172:173], 0, s[10:11]
	v_fma_f32 v223, -v188, v189, 1.0
	v_fmac_f32_e32 v189, v223, v189
	v_div_scale_f32 v223, vcc, 1.0, v187, 1.0
	v_mul_f32_e32 v225, v223, v189
	v_fma_f32 v226, -v188, v225, v223
	v_fmac_f32_e32 v225, v226, v189
	ds_read_b128 v[226:229], v169
	ds_read_b128 v[230:233], v197
	v_fma_f32 v188, -v188, v225, v223
	v_div_fmas_f32 v188, v188, v189, v225
	v_div_fixup_f32 v188, v188, v187, 1.0
	v_pk_mul_f32 v[98:99], v[98:99], v[188:189] op_sel_hi:[1,0]
	v_pk_mul_f32 v[100:101], v[100:101], v[188:189] op_sel_hi:[1,0]
	s_waitcnt lgkmcnt(0)
	v_pk_fma_f32 v[98:99], v[226:227], v[98:99], v[230:231]
	v_pk_fma_f32 v[100:101], v[228:229], v[100:101], v[232:233]
	v_cvt_pk_bf16_f32 v226, v98, v99
	v_cvt_pk_bf16_f32 v227, v100, v101
	global_store_dwordx2 v[178:179], v[226:227], off
	ds_read_b128 v[226:229], v169 offset:1024
	ds_read_b128 v[230:233], v197 offset:1024
	v_pk_mul_f32 v[102:103], v[102:103], v[188:189] op_sel_hi:[1,0]
	v_pk_mul_f32 v[104:105], v[104:105], v[188:189] op_sel_hi:[1,0]
	v_pk_mul_f32 v[106:107], v[106:107], v[188:189] op_sel_hi:[1,0]
	v_pk_mul_f32 v[108:109], v[108:109], v[188:189] op_sel_hi:[1,0]
	s_waitcnt lgkmcnt(0)
	v_pk_fma_f32 v[104:105], v[228:229], v[104:105], v[232:233]
	v_pk_fma_f32 v[102:103], v[226:227], v[102:103], v[230:231]
	v_cvt_pk_bf16_f32 v227, v104, v105
	v_cvt_pk_bf16_f32 v226, v102, v103
	global_store_dwordx2 v[178:179], v[226:227], off offset:512
	v_mov_b32_e32 v226, v102
	v_mov_b32_e32 v227, v98
	v_mov_b32_e32 v228, v103
	v_mov_b32_e32 v229, v99
	v_pk_add_f32 v[226:227], v[226:227], v[228:229]
	v_mov_b32_e32 v228, v104
	v_mov_b32_e32 v229, v100
	v_mov_b32_e32 v230, v105
	v_mov_b32_e32 v231, v101
	v_pk_add_f32 v[228:229], v[228:229], v[230:231]
	v_pk_mul_f32 v[110:111], v[110:111], v[188:189] op_sel_hi:[1,0]
	v_pk_add_f32 v[234:235], v[226:227], v[228:229]
	ds_read_b128 v[226:229], v169 offset:2048
	ds_read_b128 v[230:233], v197 offset:2048
	v_pk_mul_f32 v[112:113], v[112:113], v[188:189] op_sel_hi:[1,0]
	v_pk_mul_f32 v[114:115], v[114:115], v[188:189] op_sel_hi:[1,0]
	v_pk_mul_f32 v[116:117], v[116:117], v[188:189] op_sel_hi:[1,0]
	v_pk_mul_f32 v[118:119], v[118:119], v[188:189] op_sel_hi:[1,0]
	s_waitcnt lgkmcnt(0)
	v_pk_fma_f32 v[108:109], v[228:229], v[108:109], v[232:233]
	v_pk_fma_f32 v[106:107], v[226:227], v[106:107], v[230:231]
	v_cvt_pk_bf16_f32 v227, v108, v109
	v_cvt_pk_bf16_f32 v226, v106, v107
	global_store_dwordx2 v[178:179], v[226:227], off offset:1024
	ds_read_b128 v[226:229], v169 offset:3072
	ds_read_b128 v[230:233], v197 offset:3072
	v_pk_mul_f32 v[120:121], v[120:121], v[188:189] op_sel_hi:[1,0]
	v_pk_mul_f32 v[122:123], v[122:123], v[188:189] op_sel_hi:[1,0]
	v_pk_mul_f32 v[124:125], v[124:125], v[188:189] op_sel_hi:[1,0]
	v_pk_mov_b32 v[236:237], v[106:107], v[108:109] op_sel:[1,0]
	s_waitcnt lgkmcnt(0)
	v_pk_fma_f32 v[112:113], v[228:229], v[112:113], v[232:233]
	v_pk_fma_f32 v[110:111], v[226:227], v[110:111], v[230:231]
	v_cvt_pk_bf16_f32 v227, v112, v113
	v_cvt_pk_bf16_f32 v226, v110, v111
	global_store_dwordx2 v[178:179], v[226:227], off offset:1536
	ds_read_b128 v[226:229], v169 offset:4096
	ds_read_b128 v[230:233], v197 offset:4096
	v_mov_b32_e32 v238, v106
	v_mov_b32_e32 v239, v109
	v_pk_add_f32 v[236:237], v[236:237], v[238:239]
	v_add_f32_e32 v187, 0, v235
	s_waitcnt lgkmcnt(0)
	v_pk_fma_f32 v[116:117], v[228:229], v[116:117], v[232:233]
	v_pk_fma_f32 v[114:115], v[226:227], v[114:115], v[230:231]
	v_cvt_pk_bf16_f32 v227, v116, v117
	v_cvt_pk_bf16_f32 v226, v114, v115
	global_store_dwordx2 v[178:179], v[226:227], off offset:2048
	ds_read_b128 v[226:229], v169 offset:5120
	ds_read_b128 v[230:233], v197 offset:5120
	v_pk_add_f32 v[236:237], v[236:237], v[236:237] op_sel_hi:[0,1]
	v_add_f32_e32 v235, v234, v187
	v_add_f32_e32 v239, v110, v111
	v_add_f32_e32 v241, v112, v113
	s_waitcnt lgkmcnt(0)
	v_pk_fma_f32 v[120:121], v[228:229], v[120:121], v[232:233]
	v_pk_fma_f32 v[118:119], v[226:227], v[118:119], v[230:231]
	v_cvt_pk_bf16_f32 v227, v120, v121
	v_cvt_pk_bf16_f32 v226, v118, v119
	global_store_dwordx2 v[178:179], v[226:227], off offset:2560
	ds_read_b128 v[226:229], v169 offset:6144
	ds_read_b128 v[230:233], v197 offset:6144
	v_mov_b32_e32 v238, v114
	v_mov_b32_e32 v240, v115
	v_mov_b32_e32 v236, v116
	v_mov_b32_e32 v234, v117
	s_waitcnt lgkmcnt(0)
; __device__ __forceinline__ unsigned pk_bf16(float lo, float hi) { const bf16x2_t r = __builtin_convertvector((f32x2){lo, hi}, bf16x2_t); return __builtin_bit_cast(unsigned, r); }
; __device__ __forceinline__ void ph10(LAS unsigned char* lds, int tid, int lane, int wave, int G, int bid) {
;     ...
;         for (int j = 0; j < 8; ++j) { v[j] = v[j] * rstd * gq[64 * j] + bq[64 * j]; xq[64 * j] = (u32x2){pk_bf16(v[j].x, v[j].y), pk_bf16(v[j].z, v[j].w)}; s += (v[j].x + v[j].y) + (v[j].z + v[j].w); }
;         mean = wave_sum(s) * (1.f / D); s2 = 0.f;
; #pragma unroll
;         for (int j = 0; j < 8; ++j) { v[j] = v[j] - mean; s2 += (v[j].x * v[j].x + v[j].y * v[j].y) + (v[j].z * v[j].z + v[j].w * v[j].w); }
	v_pk_fma_f32 v[124:125], v[228:229], v[124:125], v[232:233]
	v_pk_fma_f32 v[122:123], v[226:227], v[122:123], v[230:231]
	v_cvt_pk_bf16_f32 v227, v124, v125
	v_cvt_pk_bf16_f32 v226, v122, v123
	global_store_dwordx2 v[178:179], v[226:227], off offset:3072
	ds_read_b128 v[226:229], v169 offset:7168
	ds_read_b128 v[230:233], v197 offset:7168
	v_pk_add_f32 v[238:239], v[238:239], v[240:241]
	v_pk_add_f32 v[234:235], v[236:237], v[234:235]
	v_pk_mov_b32 v[236:237], v[118:119], v[120:121] op_sel:[1,0]
	v_pk_add_f32 v[234:235], v[238:239], v[234:235]
	v_mov_b32_e32 v238, v118
	v_mov_b32_e32 v239, v121
	v_add_f32_e32 v189, v122, v123
	v_pk_add_f32 v[236:237], v[236:237], v[238:239]
	v_pk_mul_f32 v[126:127], v[126:127], v[188:189] op_sel_hi:[1,0]
	v_pk_mul_f32 v[128:129], v[128:129], v[188:189] op_sel_hi:[1,0]
	v_pk_add_f32 v[234:235], v[234:235], v[234:235] op_sel_hi:[0,1]
	v_pk_add_f32 v[236:237], v[236:237], v[236:237] op_sel_hi:[0,1]
	s_waitcnt lgkmcnt(0)
	v_pk_fma_f32 v[128:129], v[228:229], v[128:129], v[232:233]
	v_pk_fma_f32 v[126:127], v[226:227], v[126:127], v[230:231]
	v_add_f32_e32 v239, v124, v125
	v_mov_b32_e32 v188, v126
	v_mov_b32_e32 v238, v127
	v_mov_b32_e32 v236, v128
	v_mov_b32_e32 v234, v129
	v_pk_add_f32 v[188:189], v[188:189], v[238:239]
	v_pk_add_f32 v[226:227], v[236:237], v[234:235]
	s_nop 0
	v_pk_add_f32 v[188:189], v[188:189], v[226:227]
	s_nop 0
	v_add_f32_e32 v187, v188, v189
	ds_bpermute_b32 v188, v191, v187
	v_cvt_pk_bf16_f32 v189, v128, v129
	s_waitcnt lgkmcnt(0)
	v_add_f32_e32 v187, v187, v188
	ds_bpermute_b32 v188, v192, v187
	s_waitcnt lgkmcnt(0)
	v_add_f32_e32 v187, v187, v188
	ds_bpermute_b32 v188, v193, v187
	s_waitcnt lgkmcnt(0)
	v_add_f32_e32 v187, v187, v188
	ds_bpermute_b32 v188, v194, v187
	s_waitcnt lgkmcnt(0)
	v_add_f32_e32 v187, v187, v188
	ds_bpermute_b32 v188, v195, v187
	s_waitcnt lgkmcnt(0)
	v_add_f32_e32 v187, v187, v188
	ds_bpermute_b32 v223, v196, v187
	v_cvt_pk_bf16_f32 v188, v126, v127
	global_store_dwordx2 v[178:179], v[188:189], off offset:3584
	s_waitcnt lgkmcnt(0)
	v_add_f32_e32 v187, v187, v223
	v_fmamk_f32 v99, v187, 0xba000000, v99
	v_fmamk_f32 v103, v187, 0xba000000, v103
	v_fmamk_f32 v101, v187, 0xba000000, v101
	v_fmac_f32_e32 v98, 0xba000000, v187
	v_fmamk_f32 v105, v187, 0xba000000, v105
	v_fmac_f32_e32 v102, 0xba000000, v187
	v_mov_b32_e32 v228, v99
	v_mov_b32_e32 v229, v103
	v_fmac_f32_e32 v100, 0xba000000, v187
	v_fmac_f32_e32 v104, 0xba000000, v187
	v_mov_b32_e32 v226, v98
	v_mov_b32_e32 v227, v102
	v_pk_mul_f32 v[228:229], v[228:229], v[228:229]
	v_mov_b32_e32 v230, v101
	v_mov_b32_e32 v231, v105
	v_pk_fma_f32 v[226:227], v[226:227], v[226:227], v[228:229]
	v_mov_b32_e32 v228, v100
	v_mov_b32_e32 v229, v104
	v_pk_mul_f32 v[230:231], v[230:231], v[230:231]
	v_fmamk_f32 v107, v187, 0xba000000, v107
	v_pk_fma_f32 v[228:229], v[228:229], v[228:229], v[230:231]
	v_fmac_f32_e32 v106, 0xba000000, v187
	v_pk_add_f32 v[226:227], v[226:227], v[228:229]
	v_fmamk_f32 v109, v187, 0xba000000, v109
	v_fmac_f32_e32 v108, 0xba000000, v187
	v_pk_add_f32 v[226:227], v[226:227], v[226:227] op_sel_hi:[0,1]
	v_pk_mul_f32 v[228:229], v[108:109], v[108:109]
	v_pk_mul_f32 v[230:231], v[106:107], v[106:107]
	v_fmac_f32_e32 v110, 0xba000000, v187
	v_pk_mov_b32 v[232:233], v[230:231], v[228:229] op_sel:[1,0]
	v_mov_b32_e32 v231, v229
	v_fmamk_f32 v111, v187, 0xba000000, v111
	v_fmac_f32_e32 v112, 0xba000000, v187
	v_mul_f32_e32 v226, v110, v110
	v_pk_add_f32 v[228:229], v[232:233], v[230:231]
	v_fmamk_f32 v113, v187, 0xba000000, v113
	v_pk_fma_f32 v[230:231], v[110:111], v[110:111], v[226:227] op_sel_hi:[1,1,0]
	v_mul_f32_e32 v226, v112, v112
	v_pk_add_f32 v[228:229], v[228:229], v[228:229] op_sel_hi:[0,1]
	v_pk_fma_f32 v[232:233], v[112:113], v[112:113], v[226:227] op_sel_hi:[1,1,0]
	v_fmamk_f32 v117, v187, 0xba000000, v117
	v_fmac_f32_e32 v116, 0xba000000, v187
	v_fmamk_f32 v115, v187, 0xba000000, v115
	v_fmac_f32_e32 v114, 0xba000000, v187
	v_mul_f32_e32 v230, v114, v114
	v_mul_f32_e32 v232, v115, v115
	v_mul_f32_e32 v228, v116, v116
	v_mul_f32_e32 v226, v117, v117
	v_pk_add_f32 v[230:231], v[230:231], v[232:233]
	v_pk_add_f32 v[226:227], v[228:229], v[226:227]
	v_fmamk_f32 v119, v187, 0xba000000, v119
	v_pk_add_f32 v[226:227], v[230:231], v[226:227]
	v_fmac_f32_e32 v118, 0xba000000, v187
	v_fmamk_f32 v121, v187, 0xba000000, v121
	v_fmac_f32_e32 v120, 0xba000000, v187
	v_pk_add_f32 v[226:227], v[226:227], v[226:227] op_sel_hi:[0,1]
	v_pk_mul_f32 v[228:229], v[120:121], v[120:121]
	v_pk_mul_f32 v[230:231], v[118:119], v[118:119]
	v_fmac_f32_e32 v122, 0xba000000, v187
	v_pk_mov_b32 v[232:233], v[230:231], v[228:229] op_sel:[1,0]
	v_mov_b32_e32 v231, v229
	v_fmamk_f32 v123, v187, 0xba000000, v123
	v_fmac_f32_e32 v124, 0xba000000, v187
	v_mul_f32_e32 v226, v122, v122
	v_pk_add_f32 v[228:229], v[232:233], v[230:231]
	v_fmamk_f32 v125, v187, 0xba000000, v125
	v_pk_fma_f32 v[230:231], v[122:123], v[122:123], v[226:227] op_sel_hi:[1,1,0]
	v_mul_f32_e32 v226, v124, v124
	v_pk_add_f32 v[228:229], v[228:229], v[228:229] op_sel_hi:[0,1]
	v_pk_fma_f32 v[232:233], v[124:125], v[124:125], v[226:227] op_sel_hi:[1,1,0]
	v_fmamk_f32 v129, v187, 0xba000000, v129
	v_fmac_f32_e32 v128, 0xba000000, v187
	v_fmamk_f32 v127, v187, 0xba000000, v127
	v_fmac_f32_e32 v126, 0xba000000, v187
	v_mul_f32_e32 v230, v126, v126
	v_mul_f32_e32 v232, v127, v127
	v_mul_f32_e32 v228, v128, v128
	v_mul_f32_e32 v226, v129, v129
	v_pk_add_f32 v[230:231], v[230:231], v[232:233]
	v_pk_add_f32 v[226:227], v[228:229], v[226:227]
	s_nop 0
	v_pk_add_f32 v[226:227], v[230:231], v[226:227]
	s_nop 0
	v_add_f32_e32 v187, v226, v227
	ds_bpermute_b32 v223, v191, v187
	s_waitcnt lgkmcnt(0)
; #define LAS __attribute__((address_space(3)))
; __device__ __forceinline__ unsigned pk_bf16(float lo, float hi) { const bf16x2_t r = __builtin_convertvector((f32x2){lo, hi}, bf16x2_t); return __builtin_bit_cast(unsigned, r); }
; __device__ __forceinline__ unsigned pk4_fp8(float a, float b, float c, float d) { int w = 0; w = __builtin_amdgcn_cvt_pk_fp8_f32(clamp8(a), clamp8(b), w, false); w = __builtin_amdgcn_cvt_pk_fp8_f32(clamp8(c), clamp8(d), w, true); return (unsigned)w; }
; __device__ __forceinline__ void ph10(LAS unsigned char* lds, int tid, int lane, int wave, int G, int bid) {
;     ...
;         rstd = 1.f / sqrtf(wave_sum(s2) * (1.f / D) + LN_EPS);
;         const LAS f32x4* scq = VEC + 1024 + lane; const LAS f32x4* shq = VEC + 1536 + lane; unsigned* o8 = (unsigned*)(H2 + gtok * D) + lane;
; #pragma unroll
;         for (int j = 0; j < 8; ++j) { const f32x4 y = v[j] * rstd * scq[64 * j] + shq[64 * j];
;             const u32x2 hi = (u32x2){pk_bf16(y.x, y.y), pk_bf16(y.z, y.w)};
;             o8[64 * j] = pk4_fp8(y.x, y.y, y.z, y.w);
;             *(LAS u32x2*)(Hhi + row * RS + (256 * j + 4 * lane) * 2) = hi; } };
	v_add_f32_e32 v187, v187, v223
	ds_bpermute_b32 v223, v192, v187
	s_waitcnt lgkmcnt(0)
	v_add_f32_e32 v187, v187, v223
	ds_bpermute_b32 v223, v193, v187
	s_waitcnt lgkmcnt(0)
	v_add_f32_e32 v187, v187, v223
	ds_bpermute_b32 v223, v194, v187
	s_waitcnt lgkmcnt(0)
	v_add_f32_e32 v187, v187, v223
	ds_bpermute_b32 v223, v195, v187
	s_waitcnt lgkmcnt(0)
	v_add_f32_e32 v187, v187, v223
	ds_bpermute_b32 v223, v196, v187
	s_waitcnt lgkmcnt(0)
	v_add_f32_e32 v187, v187, v223
	v_fmamk_f32 v187, v187, 0x3a000000, v207
	v_mul_f32_e32 v223, 0x4f800000, v187
	v_cmp_gt_f32_e32 vcc, s69, v187
	s_nop 1
	v_cndmask_b32_e32 v187, v187, v223, vcc
	v_sqrt_f32_e32 v223, v187
	s_nop 0
	v_add_u32_e32 v225, -1, v223
	v_fma_f32 v226, -v225, v223, v187
	v_cmp_ge_f32_e64 s[10:11], 0, v226
	v_add_u32_e32 v226, 1, v223
	s_nop 0
	v_cndmask_b32_e64 v225, v223, v225, s[10:11]
	v_fma_f32 v223, -v226, v223, v187
	v_cmp_lt_f32_e64 s[10:11], 0, v223
	s_nop 1
	v_cndmask_b32_e64 v223, v225, v226, s[10:11]
	v_mul_f32_e32 v225, 0x37800000, v223
	v_cndmask_b32_e32 v223, v223, v225, vcc
	v_cmp_class_f32_e32 vcc, v187, v208
	ds_read_b128 v[226:229], v198
	ds_read_b128 v[230:233], v199
	v_cndmask_b32_e32 v187, v223, v187, vcc
	v_div_scale_f32 v223, s[10:11], v187, v187, 1.0
	v_rcp_f32_e32 v225, v223
	s_lshl_b64 s[10:11], s[16:17], 11
	s_cmp_eq_u32 s49, 7
	v_fma_f32 v178, -v223, v225, 1.0
	v_fmac_f32_e32 v225, v178, v225
	v_div_scale_f32 v178, vcc, 1.0, v187, 1.0
	v_mul_f32_e32 v179, v178, v225
	v_fma_f32 v188, -v223, v179, v178
	v_fmac_f32_e32 v179, v188, v225
	v_fma_f32 v178, -v223, v179, v178
	v_div_fmas_f32 v178, v178, v225, v179
	v_div_fixup_f32 v178, v178, v187, 1.0
	v_pk_mul_f32 v[188:189], v[98:99], v[178:179] op_sel_hi:[1,0]
	v_pk_mul_f32 v[234:235], v[100:101], v[178:179] op_sel_hi:[1,0]
	s_waitcnt lgkmcnt(0)
	v_pk_fma_f32 v[188:189], v[226:227], v[188:189], v[230:231]
	v_mov_b32_e32 v223, v163
	v_med3_f32 v179, v188, s70, v212
	v_med3_f32 v187, v189, s70, v212
	v_cvt_pk_fp8_f32 v223, v179, v187
	v_pk_fma_f32 v[226:227], v[228:229], v[234:235], v[232:233]
	v_lshl_add_u64 v[234:235], v[174:175], 0, s[10:11]
	v_med3_f32 v179, v226, s70, v212
	v_med3_f32 v187, v227, s70, v212
	v_cvt_pk_fp8_f32 v223, v179, v187 op_sel:[0,0,1]
	v_cvt_pk_bf16_f32 v188, v188, v189
	v_cvt_pk_bf16_f32 v189, v226, v227
	v_pk_mul_f32 v[236:237], v[104:105], v[178:179] op_sel_hi:[1,0]
	global_store_dword v[234:235], v223, off
	v_add_u32_e32 v223, s64, v168
	ds_write_b64 v223, v[188:189]
	ds_read_b128 v[226:229], v198 offset:1024
	ds_read_b128 v[230:233], v199 offset:1024
	v_pk_mul_f32 v[188:189], v[102:103], v[178:179] op_sel_hi:[1,0]
	v_mov_b32_e32 v225, v163
	s_waitcnt lgkmcnt(0)
	v_pk_fma_f32 v[188:189], v[226:227], v[188:189], v[230:231]
	s_nop 0
	v_med3_f32 v179, v188, s70, v212
	v_med3_f32 v187, v189, s70, v212
	v_cvt_pk_fp8_f32 v225, v179, v187
	v_pk_fma_f32 v[226:227], v[228:229], v[236:237], v[232:233]
	v_cvt_pk_bf16_f32 v188, v188, v189
	v_med3_f32 v179, v226, s70, v212
	v_med3_f32 v187, v227, s70, v212
	v_cvt_pk_fp8_f32 v225, v179, v187 op_sel:[0,0,1]
	v_cvt_pk_bf16_f32 v189, v226, v227
	v_pk_mul_f32 v[236:237], v[108:109], v[178:179] op_sel_hi:[1,0]
	global_store_dword v[234:235], v225, off offset:256
	ds_write_b64 v223, v[188:189] offset:512
	ds_read_b128 v[226:229], v198 offset:2048
	ds_read_b128 v[230:233], v199 offset:2048
	v_pk_mul_f32 v[188:189], v[106:107], v[178:179] op_sel_hi:[1,0]
	v_mov_b32_e32 v225, v163
	s_waitcnt lgkmcnt(0)
	v_pk_fma_f32 v[188:189], v[226:227], v[188:189], v[230:231]
	s_nop 0
	v_med3_f32 v179, v188, s70, v212
	v_med3_f32 v187, v189, s70, v212
	v_cvt_pk_fp8_f32 v225, v179, v187
	v_pk_fma_f32 v[226:227], v[228:229], v[236:237], v[232:233]
	v_cvt_pk_bf16_f32 v188, v188, v189
	v_med3_f32 v179, v226, s70, v212
	v_med3_f32 v187, v227, s70, v212
	v_cvt_pk_fp8_f32 v225, v179, v187 op_sel:[0,0,1]
	v_cvt_pk_bf16_f32 v189, v226, v227
	v_pk_mul_f32 v[236:237], v[112:113], v[178:179] op_sel_hi:[1,0]
	global_store_dword v[234:235], v225, off offset:512
	ds_write_b64 v223, v[188:189] offset:1024
	ds_read_b128 v[226:229], v198 offset:3072
	ds_read_b128 v[230:233], v199 offset:3072
	v_pk_mul_f32 v[188:189], v[110:111], v[178:179] op_sel_hi:[1,0]
	v_mov_b32_e32 v225, v163
	s_waitcnt lgkmcnt(0)
	v_pk_fma_f32 v[188:189], v[226:227], v[188:189], v[230:231]
	s_nop 0
	v_med3_f32 v179, v188, s70, v212
	v_med3_f32 v187, v189, s70, v212
	v_cvt_pk_fp8_f32 v225, v179, v187
	v_pk_fma_f32 v[226:227], v[228:229], v[236:237], v[232:233]
	v_cvt_pk_bf16_f32 v188, v188, v189
	v_med3_f32 v179, v226, s70, v212
	v_med3_f32 v187, v227, s70, v212
	v_cvt_pk_fp8_f32 v225, v179, v187 op_sel:[0,0,1]
	v_cvt_pk_bf16_f32 v189, v226, v227
	v_pk_mul_f32 v[236:237], v[116:117], v[178:179] op_sel_hi:[1,0]
	global_store_dword v[234:235], v225, off offset:768
	ds_write_b64 v223, v[188:189] offset:1536
	ds_read_b128 v[226:229], v198 offset:4096
	ds_read_b128 v[230:233], v199 offset:4096
	v_pk_mul_f32 v[188:189], v[114:115], v[178:179] op_sel_hi:[1,0]
	v_mov_b32_e32 v225, v163
	s_waitcnt lgkmcnt(0)
	v_pk_fma_f32 v[188:189], v[226:227], v[188:189], v[230:231]
	s_nop 0
	v_med3_f32 v179, v188, s70, v212
	v_med3_f32 v187, v189, s70, v212
	v_cvt_pk_fp8_f32 v225, v179, v187
	v_pk_fma_f32 v[226:227], v[228:229], v[236:237], v[232:233]
	v_cvt_pk_bf16_f32 v188, v188, v189
	v_med3_f32 v179, v226, s70, v212
	v_med3_f32 v187, v227, s70, v212
	v_cvt_pk_fp8_f32 v225, v179, v187 op_sel:[0,0,1]
	v_cvt_pk_bf16_f32 v189, v226, v227
	v_pk_mul_f32 v[236:237], v[120:121], v[178:179] op_sel_hi:[1,0]
	global_store_dword v[234:235], v225, off offset:1024
	ds_write_b64 v223, v[188:189] offset:2048
	ds_read_b128 v[226:229], v198 offset:5120
	ds_read_b128 v[230:233], v199 offset:5120
	v_pk_mul_f32 v[188:189], v[118:119], v[178:179] op_sel_hi:[1,0]
	v_mov_b32_e32 v225, v163
	s_waitcnt lgkmcnt(0)
; __device__ __forceinline__ void ph10(LAS unsigned char* lds, int tid, int lane, int wave, int G, int bid) {
;     ...
;     auto do_row = [&](f32x4 (&v)[8], const unsigned (&mg)[8], size_t gtok, int row) {
;         u32x2* xq = (u32x2*)(XM + gtok * D) + lane; float s = 0.f;
; #pragma unroll
;         for (int j = 0; j < 8; ++j) { const f32x2 m0 = __builtin_amdgcn_cvt_pk_f32_fp8((int)mg[j], false), m1 = __builtin_amdgcn_cvt_pk_f32_fp8((int)mg[j], true);
;             v[j] = v[j] * DN_ALPHA + (f32x4){m0.x, m0.y, m1.x, m1.y} * MG8_INV; s += (v[j].x + v[j].y) + (v[j].z + v[j].w); }
;     ...
;             if (grp < 7) load_row(g0 + 16, xa, ma);
;             do_row(xb, mb, g0 + 1, 2 * wave + 1);
	v_pk_fma_f32 v[188:189], v[226:227], v[188:189], v[230:231]
	s_nop 0
	v_med3_f32 v179, v188, s70, v212
	v_med3_f32 v187, v189, s70, v212
	v_cvt_pk_fp8_f32 v225, v179, v187
	v_pk_fma_f32 v[226:227], v[228:229], v[236:237], v[232:233]
	v_cvt_pk_bf16_f32 v188, v188, v189
	v_med3_f32 v179, v226, s70, v212
	v_med3_f32 v187, v227, s70, v212
	v_cvt_pk_fp8_f32 v225, v179, v187 op_sel:[0,0,1]
	v_cvt_pk_bf16_f32 v189, v226, v227
	v_pk_mul_f32 v[236:237], v[124:125], v[178:179] op_sel_hi:[1,0]
	global_store_dword v[234:235], v225, off offset:1280
	ds_write_b64 v223, v[188:189] offset:2560
	ds_read_b128 v[226:229], v198 offset:6144
	ds_read_b128 v[230:233], v199 offset:6144
	v_pk_mul_f32 v[188:189], v[122:123], v[178:179] op_sel_hi:[1,0]
	v_mov_b32_e32 v225, v163
	s_waitcnt lgkmcnt(0)
	v_pk_fma_f32 v[188:189], v[226:227], v[188:189], v[230:231]
	s_nop 0
	v_med3_f32 v179, v188, s70, v212
	v_med3_f32 v187, v189, s70, v212
	v_cvt_pk_fp8_f32 v225, v179, v187
	v_pk_fma_f32 v[226:227], v[228:229], v[236:237], v[232:233]
	v_cvt_pk_bf16_f32 v188, v188, v189
	v_med3_f32 v179, v226, s70, v212
	v_med3_f32 v187, v227, s70, v212
	v_cvt_pk_fp8_f32 v225, v179, v187 op_sel:[0,0,1]
	v_cvt_pk_bf16_f32 v189, v226, v227
	global_store_dword v[234:235], v225, off offset:1536
	ds_write_b64 v223, v[188:189] offset:3072
	ds_read_b128 v[226:229], v198 offset:7168
	ds_read_b128 v[230:233], v199 offset:7168
	v_pk_mul_f32 v[188:189], v[126:127], v[178:179] op_sel_hi:[1,0]
	v_pk_mul_f32 v[178:179], v[128:129], v[178:179] op_sel_hi:[1,0]
	s_waitcnt lgkmcnt(0)
	v_pk_fma_f32 v[188:189], v[188:189], v[226:227], v[230:231]
	s_nop 0
	v_med3_f32 v187, v188, s70, v212
	v_med3_f32 v225, v189, s70, v212
	v_mov_b32_e32 v226, v163
	v_cvt_pk_fp8_f32 v226, v187, v225
	v_pk_fma_f32 v[178:179], v[178:179], v[228:229], v[232:233]
	v_cvt_pk_bf16_f32 v188, v188, v189
	v_med3_f32 v187, v178, s70, v212
	v_med3_f32 v225, v179, s70, v212
	v_cvt_pk_fp8_f32 v226, v187, v225 op_sel:[0,0,1]
	v_cvt_pk_bf16_f32 v189, v178, v179
	global_store_dword v[234:235], v226, off offset:1792
	ds_write_b64 v223, v[188:189] offset:3584
	s_cbranch_scc1 .LBB0_976
	s_lshl_b64 s[10:11], s[16:17], 9
	s_add_u32 s10, s10, 0x2000
	s_addc_u32 s11, s11, 0
	v_lshl_add_u64 v[114:115], s[10:11], 4, v[164:165]
	v_add_co_u32_e32 v126, vcc, s68, v114
	v_lshl_add_u64 v[122:123], s[10:11], 2, v[166:167]
	s_nop 0
	v_addc_co_u32_e32 v127, vcc, 0, v115, vcc
	global_load_dwordx4 v[98:101], v[114:115], off nt
	global_load_dwordx4 v[102:105], v[114:115], off offset:1024 nt
	global_load_dwordx4 v[106:109], v[114:115], off offset:2048 nt
	global_load_dwordx4 v[110:113], v[114:115], off offset:3072 nt
	s_nop 0
	global_load_dwordx4 v[114:117], v[126:127], off nt
	global_load_dwordx4 v[118:121], v[126:127], off offset:1024 nt
	global_load_dword v215, v[122:123], off nt
	global_load_dword v216, v[122:123], off offset:256 nt
	global_load_dword v217, v[122:123], off offset:512 nt
	global_load_dword v218, v[122:123], off offset:768 nt
	global_load_dword v219, v[122:123], off offset:1024 nt
	global_load_dword v220, v[122:123], off offset:1280 nt
	global_load_dword v221, v[122:123], off offset:1536 nt
	global_load_dword v222, v[122:123], off offset:1792 nt
	s_nop 0
	global_load_dwordx4 v[122:125], v[126:127], off offset:2048 nt
	s_nop 0
	global_load_dwordx4 v[126:129], v[126:127], off offset:3072 nt
	s_waitcnt vmcnt(32)
	s_branch .Lp10_rowb
.LBB0_976:
	s_waitcnt vmcnt(16)
.Lp10_rowb:
	v_cvt_pk_f32_fp8_e32 v[178:179], v186
	v_cvt_pk_f32_fp8_sdwa v[186:187], v186 src0_sel:WORD_1
	v_cvt_pk_f32_fp8_e32 v[188:189], v185
	v_cvt_pk_f32_fp8_sdwa v[226:227], v185 src0_sel:WORD_1
	v_pk_mul_f32 v[178:179], v[178:179], s[44:45] op_sel_hi:[1,0]
	v_pk_mul_f32 v[186:187], v[186:187], s[44:45] op_sel_hi:[1,0]
	v_pk_fma_f32 v[178:179], v[158:159], s[46:47], v[178:179] op_sel_hi:[1,0,1]
	v_pk_mul_f32 v[158:159], v[188:189], s[44:45] op_sel_hi:[1,0]
	v_pk_fma_f32 v[160:161], v[160:161], s[46:47], v[186:187] op_sel_hi:[1,0,1]
	v_pk_mul_f32 v[186:187], v[226:227], s[44:45] op_sel_hi:[1,0]
	v_pk_fma_f32 v[188:189], v[154:155], s[46:47], v[158:159] op_sel_hi:[1,0,1]
	v_pk_fma_f32 v[186:187], v[156:157], s[46:47], v[186:187] op_sel_hi:[1,0,1]
	v_mov_b32_e32 v154, v178
	v_mov_b32_e32 v155, v188
	v_mov_b32_e32 v156, v179
	v_mov_b32_e32 v157, v189
	v_pk_add_f32 v[154:155], v[154:155], v[156:157]
	v_mov_b32_e32 v156, v160
	v_mov_b32_e32 v157, v186
	v_mov_b32_e32 v158, v161
	v_mov_b32_e32 v159, v187
	v_pk_add_f32 v[156:157], v[156:157], v[158:159]
	v_cvt_pk_f32_fp8_sdwa v[158:159], v184 src0_sel:WORD_1
	v_pk_add_f32 v[154:155], v[154:155], v[156:157]
	v_cvt_pk_f32_fp8_e32 v[156:157], v184
	v_add_f32_e32 v154, 0, v154
	v_add_f32_e32 v226, v154, v155
	v_pk_mul_f32 v[154:155], v[158:159], s[44:45] op_sel_hi:[1,0]
	v_pk_mul_f32 v[156:157], v[156:157], s[44:45] op_sel_hi:[1,0]
	v_cvt_pk_f32_fp8_sdwa v[184:185], v183 src0_sel:WORD_1
	v_pk_fma_f32 v[154:155], v[152:153], s[46:47], v[154:155] op_sel_hi:[1,0,1]
	v_pk_fma_f32 v[158:159], v[150:151], s[46:47], v[156:157] op_sel_hi:[1,0,1]
	v_mov_b32_e32 v153, v155
	v_pk_mov_b32 v[150:151], v[158:159], v[154:155] op_sel:[1,0]
	v_mov_b32_e32 v152, v158
	v_cvt_pk_f32_fp8_e32 v[156:157], v183
	v_pk_add_f32 v[150:151], v[150:151], v[152:153]
	v_pk_mul_f32 v[156:157], v[156:157], s[44:45] op_sel_hi:[1,0]
	v_pk_add_f32 v[152:153], v[150:151], v[150:151] op_sel:[0,1] op_sel_hi:[1,0]
	v_pk_mul_f32 v[150:151], v[184:185], s[44:45] op_sel_hi:[1,0]
	v_pk_fma_f32 v[146:147], v[146:147], s[46:47], v[156:157] op_sel_hi:[1,0,1]
	v_pk_fma_f32 v[150:151], v[148:149], s[46:47], v[150:151] op_sel_hi:[1,0,1]
	v_cvt_pk_f32_fp8_e32 v[148:149], v182
; __device__ __forceinline__ void ph10(LAS unsigned char* lds, int tid, int lane, int wave, int G, int bid) {
;     ...
;         for (int j = 0; j < 8; ++j) { const f32x2 m0 = __builtin_amdgcn_cvt_pk_f32_fp8((int)mg[j], false), m1 = __builtin_amdgcn_cvt_pk_f32_fp8((int)mg[j], true);
;             v[j] = v[j] * DN_ALPHA + (f32x4){m0.x, m0.y, m1.x, m1.y} * MG8_INV; s += (v[j].x + v[j].y) + (v[j].z + v[j].w); }
;         float mean = wave_sum(s) * (1.f / D), s2 = 0.f;
; #pragma unroll
;         for (int j = 0; j < 8; ++j) { v[j] = v[j] - mean; s2 += (v[j].x * v[j].x + v[j].y * v[j].y) + (v[j].z * v[j].z + v[j].w * v[j].w); }
;         float rstd = 1.f / sqrtf(wave_sum(s2) * (1.f / D) + LN_EPS);
	v_cvt_pk_f32_fp8_sdwa v[156:157], v182 src0_sel:WORD_1
	v_add_f32_e32 v228, v146, v147
	v_add_f32_e32 v230, v150, v151
	v_pk_mul_f32 v[148:149], v[148:149], s[44:45] op_sel_hi:[1,0]
	v_pk_mul_f32 v[156:157], v[156:157], s[44:45] op_sel_hi:[1,0]
	v_pk_fma_f32 v[184:185], v[142:143], s[46:47], v[148:149] op_sel_hi:[1,0,1]
	v_pk_fma_f32 v[182:183], v[144:145], s[46:47], v[156:157] op_sel_hi:[1,0,1]
	v_mov_b32_e32 v227, v184
	v_mov_b32_e32 v153, v185
	v_pk_add_f32 v[142:143], v[226:227], v[152:153]
	v_cvt_pk_f32_fp8_e32 v[148:149], v181
	v_cvt_pk_f32_fp8_sdwa v[152:153], v181 src0_sel:WORD_1
	v_mov_b32_e32 v229, v182
	v_mov_b32_e32 v231, v183
	v_pk_add_f32 v[144:145], v[228:229], v[230:231]
	s_nop 0
	v_pk_add_f32 v[142:143], v[142:143], v[144:145]
	v_pk_mul_f32 v[144:145], v[148:149], s[44:45] op_sel_hi:[1,0]
	v_pk_add_f32 v[156:157], v[142:143], v[142:143] op_sel:[0,1] op_sel_hi:[1,0]
	v_pk_mul_f32 v[142:143], v[152:153], s[44:45] op_sel_hi:[1,0]
	v_cvt_pk_f32_fp8_e32 v[148:149], v180
	v_cvt_pk_f32_fp8_sdwa v[152:153], v180 src0_sel:WORD_1
	v_pk_fma_f32 v[142:143], v[132:133], s[46:47], v[142:143] op_sel_hi:[1,0,1]
	v_pk_fma_f32 v[144:145], v[130:131], s[46:47], v[144:145] op_sel_hi:[1,0,1]
	v_mov_b32_e32 v133, v143
	v_pk_mov_b32 v[130:131], v[144:145], v[142:143] op_sel:[1,0]
	v_mov_b32_e32 v132, v144
	v_pk_add_f32 v[130:131], v[130:131], v[132:133]
	v_pk_mul_f32 v[132:133], v[152:153], s[44:45] op_sel_hi:[1,0]
	v_pk_add_f32 v[226:227], v[130:131], v[130:131] op_sel:[0,1] op_sel_hi:[1,0]
	v_pk_mul_f32 v[130:131], v[148:149], s[44:45] op_sel_hi:[1,0]
	v_pk_fma_f32 v[180:181], v[140:141], s[46:47], v[132:133] op_sel_hi:[1,0,1]
	v_pk_fma_f32 v[138:139], v[138:139], s[46:47], v[130:131] op_sel_hi:[1,0,1]
	v_cvt_pk_f32_fp8_e32 v[130:131], v224
	v_cvt_pk_f32_fp8_sdwa v[132:133], v224 src0_sel:WORD_1
	v_add_f32_e32 v140, v138, v139
	v_add_f32_e32 v148, v180, v181
	v_pk_mul_f32 v[152:153], v[130:131], s[44:45] op_sel_hi:[1,0]
	v_pk_mul_f32 v[130:131], v[132:133], s[44:45] op_sel_hi:[1,0]
	v_pk_fma_f32 v[132:133], v[134:135], s[46:47], v[152:153] op_sel_hi:[1,0,1]
	v_pk_fma_f32 v[130:131], v[136:137], s[46:47], v[130:131] op_sel_hi:[1,0,1]
	v_mov_b32_e32 v157, v132
	v_mov_b32_e32 v227, v133
	v_mov_b32_e32 v141, v130
	v_mov_b32_e32 v149, v131
	v_pk_add_f32 v[134:135], v[156:157], v[226:227]
	v_pk_add_f32 v[136:137], v[140:141], v[148:149]
	s_nop 0
	v_pk_add_f32 v[134:135], v[134:135], v[136:137]
	s_nop 0
	v_add_f32_e32 v134, v134, v135
	ds_bpermute_b32 v135, v191, v134
	s_waitcnt lgkmcnt(0)
	v_add_f32_e32 v134, v134, v135
	ds_bpermute_b32 v135, v192, v134
	s_waitcnt lgkmcnt(0)
	v_add_f32_e32 v134, v134, v135
	ds_bpermute_b32 v135, v193, v134
	s_waitcnt lgkmcnt(0)
	v_add_f32_e32 v134, v134, v135
	ds_bpermute_b32 v135, v194, v134
	s_waitcnt lgkmcnt(0)
	v_add_f32_e32 v134, v134, v135
	ds_bpermute_b32 v135, v195, v134
	s_waitcnt lgkmcnt(0)
	v_add_f32_e32 v134, v134, v135
	ds_bpermute_b32 v135, v196, v134
	s_waitcnt lgkmcnt(0)
	v_add_f32_e32 v152, v134, v135
	v_fmamk_f32 v179, v152, 0xba000000, v179
	v_fmamk_f32 v189, v152, 0xba000000, v189
	v_fmamk_f32 v161, v152, 0xba000000, v161
	v_fmac_f32_e32 v178, 0xba000000, v152
	v_fmamk_f32 v187, v152, 0xba000000, v187
	v_fmac_f32_e32 v188, 0xba000000, v152
	v_mov_b32_e32 v136, v179
	v_mov_b32_e32 v137, v189
	v_fmac_f32_e32 v160, 0xba000000, v152
	v_fmac_f32_e32 v186, 0xba000000, v152
	v_mov_b32_e32 v134, v178
	v_mov_b32_e32 v135, v188
	v_pk_mul_f32 v[136:137], v[136:137], v[136:137]
	v_mov_b32_e32 v140, v161
	v_mov_b32_e32 v141, v187
	v_pk_fma_f32 v[134:135], v[134:135], v[134:135], v[136:137]
	v_mov_b32_e32 v136, v160
	v_mov_b32_e32 v137, v186
	v_pk_mul_f32 v[140:141], v[140:141], v[140:141]
	v_fmamk_f32 v159, v152, 0xba000000, v159
	v_pk_fma_f32 v[136:137], v[136:137], v[136:137], v[140:141]
	v_fmac_f32_e32 v158, 0xba000000, v152
	v_pk_add_f32 v[134:135], v[134:135], v[136:137]
	v_fmamk_f32 v155, v152, 0xba000000, v155
	v_fmac_f32_e32 v154, 0xba000000, v152
	v_pk_add_f32 v[134:135], v[134:135], v[134:135] op_sel_hi:[0,1]
	v_pk_mul_f32 v[136:137], v[154:155], v[154:155]
	v_pk_mul_f32 v[140:141], v[158:159], v[158:159]
	v_fmac_f32_e32 v146, 0xba000000, v152
	v_pk_mov_b32 v[148:149], v[140:141], v[136:137] op_sel:[1,0]
	v_mov_b32_e32 v141, v137
	v_fmamk_f32 v147, v152, 0xba000000, v147
	v_fmac_f32_e32 v150, 0xba000000, v152
	v_mul_f32_e32 v134, v146, v146
	v_pk_add_f32 v[136:137], v[148:149], v[140:141]
	v_fmamk_f32 v151, v152, 0xba000000, v151
	v_pk_fma_f32 v[140:141], v[146:147], v[146:147], v[134:135] op_sel_hi:[1,1,0]
	v_mul_f32_e32 v134, v150, v150
	v_pk_add_f32 v[136:137], v[136:137], v[136:137] op_sel_hi:[0,1]
	v_pk_fma_f32 v[148:149], v[150:151], v[150:151], v[134:135] op_sel_hi:[1,1,0]
	v_fmamk_f32 v183, v152, 0xba000000, v183
	v_fmac_f32_e32 v182, 0xba000000, v152
	v_fmamk_f32 v185, v152, 0xba000000, v185
	v_fmac_f32_e32 v184, 0xba000000, v152
	v_mul_f32_e32 v140, v184, v184
	v_mul_f32_e32 v148, v185, v185
	v_mul_f32_e32 v136, v182, v182
	v_mul_f32_e32 v134, v183, v183
	v_pk_add_f32 v[140:141], v[140:141], v[148:149]
	v_pk_add_f32 v[134:135], v[136:137], v[134:135]
	v_fmamk_f32 v145, v152, 0xba000000, v145
	v_pk_add_f32 v[134:135], v[140:141], v[134:135]
	v_fmac_f32_e32 v144, 0xba000000, v152
	v_fmamk_f32 v143, v152, 0xba000000, v143
	v_fmac_f32_e32 v142, 0xba000000, v152
	v_pk_add_f32 v[134:135], v[134:135], v[134:135] op_sel_hi:[0,1]
	v_pk_mul_f32 v[136:137], v[142:143], v[142:143]
	v_pk_mul_f32 v[140:141], v[144:145], v[144:145]
	v_fmac_f32_e32 v138, 0xba000000, v152
	v_pk_mov_b32 v[148:149], v[140:141], v[136:137] op_sel:[1,0]
	v_mov_b32_e32 v141, v137
	v_fmamk_f32 v139, v152, 0xba000000, v139
	v_fmac_f32_e32 v180, 0xba000000, v152
	v_mul_f32_e32 v134, v138, v138
	v_pk_add_f32 v[136:137], v[148:149], v[140:141]
	v_fmamk_f32 v181, v152, 0xba000000, v181
	v_pk_fma_f32 v[140:141], v[138:139], v[138:139], v[134:135] op_sel_hi:[1,1,0]
	v_mul_f32_e32 v134, v180, v180
	v_pk_add_f32 v[136:137], v[136:137], v[136:137] op_sel_hi:[0,1]
	v_pk_fma_f32 v[148:149], v[180:181], v[180:181], v[134:135] op_sel_hi:[1,1,0]
	v_fmamk_f32 v131, v152, 0xba000000, v131
	v_fmac_f32_e32 v130, 0xba000000, v152
	v_fmamk_f32 v133, v152, 0xba000000, v133
	v_fmac_f32_e32 v132, 0xba000000, v152
	v_mul_f32_e32 v140, v132, v132
	v_mul_f32_e32 v148, v133, v133
	v_mul_f32_e32 v136, v130, v130
	v_mul_f32_e32 v134, v131, v131
	v_pk_add_f32 v[140:141], v[140:141], v[148:149]
	v_pk_add_f32 v[134:135], v[136:137], v[134:135]
	s_nop 0
	v_pk_add_f32 v[134:135], v[140:141], v[134:135]
	s_nop 0
	v_add_f32_e32 v134, v134, v135
	ds_bpermute_b32 v135, v191, v134
	s_waitcnt lgkmcnt(0)
; #define LAS __attribute__((address_space(3)))
; __device__ __forceinline__ unsigned pk_bf16(float lo, float hi) { const bf16x2_t r = __builtin_convertvector((f32x2){lo, hi}, bf16x2_t); return __builtin_bit_cast(unsigned, r); }
; __device__ __forceinline__ void ph10(LAS unsigned char* lds, int tid, int lane, int wave, int G, int bid) {
;     ...
;         float rstd = 1.f / sqrtf(wave_sum(s2) * (1.f / D) + LN_EPS);
;         const LAS f32x4* gq = VEC + lane; const LAS f32x4* bq = VEC + 512 + lane; s = 0.f;
; #pragma unroll
;         for (int j = 0; j < 8; ++j) { v[j] = v[j] * rstd * gq[64 * j] + bq[64 * j]; xq[64 * j] = (u32x2){pk_bf16(v[j].x, v[j].y), pk_bf16(v[j].z, v[j].w)}; s += (v[j].x + v[j].y) + (v[j].z + v[j].w); }
;         mean = wave_sum(s) * (1.f / D); s2 = 0.f;
	v_add_f32_e32 v134, v134, v135
	ds_bpermute_b32 v135, v192, v134
	s_waitcnt lgkmcnt(0)
	v_add_f32_e32 v134, v134, v135
	ds_bpermute_b32 v135, v193, v134
	s_waitcnt lgkmcnt(0)
	v_add_f32_e32 v134, v134, v135
	ds_bpermute_b32 v135, v194, v134
	s_waitcnt lgkmcnt(0)
	v_add_f32_e32 v134, v134, v135
	ds_bpermute_b32 v135, v195, v134
	s_waitcnt lgkmcnt(0)
	v_add_f32_e32 v134, v134, v135
	ds_bpermute_b32 v135, v196, v134
	s_waitcnt lgkmcnt(0)
	v_add_f32_e32 v134, v134, v135
	v_fmamk_f32 v134, v134, 0x3a000000, v207
	v_mul_f32_e32 v135, 0x4f800000, v134
	v_cmp_gt_f32_e32 vcc, s69, v134
	s_nop 1
	v_cndmask_b32_e32 v134, v134, v135, vcc
	v_sqrt_f32_e32 v135, v134
	s_nop 0
	v_add_u32_e32 v136, -1, v135
	v_fma_f32 v137, -v136, v135, v134
	v_cmp_ge_f32_e64 s[10:11], 0, v137
	v_add_u32_e32 v137, 1, v135
	s_nop 0
	v_cndmask_b32_e64 v136, v135, v136, s[10:11]
	v_fma_f32 v135, -v137, v135, v134
	v_cmp_lt_f32_e64 s[10:11], 0, v135
	s_nop 1
	v_cndmask_b32_e64 v135, v136, v137, s[10:11]
	v_mul_f32_e32 v136, 0x37800000, v135
	v_cndmask_b32_e32 v135, v135, v136, vcc
	v_cmp_class_f32_e32 vcc, v134, v208
	s_nop 1
	v_cndmask_b32_e32 v140, v135, v134, vcc
	v_div_scale_f32 v134, s[10:11], v140, v140, 1.0
	v_rcp_f32_e32 v141, v134
	s_lshl_b64 s[10:11], s[14:15], 12
	v_lshl_add_u64 v[156:157], v[172:173], 0, s[10:11]
	v_fma_f32 v135, -v134, v141, 1.0
	v_fmac_f32_e32 v141, v135, v141
	v_div_scale_f32 v135, vcc, 1.0, v140, 1.0
	v_mul_f32_e32 v148, v135, v141
	v_fma_f32 v136, -v134, v148, v135
	v_fmac_f32_e32 v148, v136, v141
	v_fma_f32 v149, -v134, v148, v135
	ds_read_b128 v[134:137], v169
	ds_read_b128 v[224:227], v197
	v_div_fmas_f32 v141, v149, v141, v148
	v_div_fixup_f32 v228, v141, v140, 1.0
	v_pk_mul_f32 v[140:141], v[178:179], v[228:229] op_sel_hi:[1,0]
	v_pk_mul_f32 v[148:149], v[160:161], v[228:229] op_sel_hi:[1,0]
	s_waitcnt lgkmcnt(0)
	v_pk_fma_f32 v[178:179], v[134:135], v[140:141], v[224:225]
	v_pk_fma_f32 v[160:161], v[136:137], v[148:149], v[226:227]
	v_cvt_pk_bf16_f32 v134, v178, v179
	v_cvt_pk_bf16_f32 v135, v160, v161
	global_store_dwordx2 v[156:157], v[134:135], off
	ds_read_b128 v[134:137], v169 offset:1024
	ds_read_b128 v[224:227], v197 offset:1024
	v_pk_mul_f32 v[140:141], v[188:189], v[228:229] op_sel_hi:[1,0]
	v_pk_mul_f32 v[148:149], v[186:187], v[228:229] op_sel_hi:[1,0]
	v_pk_mul_f32 v[154:155], v[154:155], v[228:229] op_sel_hi:[1,0]
	v_pk_mul_f32 v[182:183], v[182:183], v[228:229] op_sel_hi:[1,0]
	s_waitcnt lgkmcnt(0)
	v_pk_fma_f32 v[148:149], v[136:137], v[148:149], v[226:227]
	v_pk_fma_f32 v[152:153], v[134:135], v[140:141], v[224:225]
	v_cvt_pk_bf16_f32 v135, v148, v149
	v_cvt_pk_bf16_f32 v134, v152, v153
	global_store_dwordx2 v[156:157], v[134:135], off offset:512
	v_mov_b32_e32 v134, v152
	v_mov_b32_e32 v135, v178
	v_mov_b32_e32 v136, v153
	v_mov_b32_e32 v137, v179
	v_pk_add_f32 v[134:135], v[134:135], v[136:137]
	v_mov_b32_e32 v136, v148
	v_mov_b32_e32 v137, v160
	v_mov_b32_e32 v140, v149
	v_mov_b32_e32 v141, v161
	v_pk_add_f32 v[136:137], v[136:137], v[140:141]
	v_pk_mul_f32 v[142:143], v[142:143], v[228:229] op_sel_hi:[1,0]
	v_pk_add_f32 v[140:141], v[134:135], v[136:137]
	ds_read_b128 v[134:137], v169 offset:2048
	ds_read_b128 v[186:189], v197 offset:2048
	v_add_f32_e32 v141, 0, v141
	v_add_f32_e32 v225, v140, v141
	v_pk_mul_f32 v[140:141], v[158:159], v[228:229] op_sel_hi:[1,0]
	v_pk_mul_f32 v[138:139], v[138:139], v[228:229] op_sel_hi:[1,0]
	s_waitcnt lgkmcnt(0)
	v_pk_fma_f32 v[154:155], v[136:137], v[154:155], v[188:189]
	v_pk_fma_f32 v[158:159], v[134:135], v[140:141], v[186:187]
	v_cvt_pk_bf16_f32 v135, v154, v155
	v_cvt_pk_bf16_f32 v134, v158, v159
	global_store_dwordx2 v[156:157], v[134:135], off offset:1024
	ds_read_b128 v[134:137], v169 offset:3072
	ds_read_b128 v[186:189], v197 offset:3072
	v_pk_mov_b32 v[140:141], v[158:159], v[154:155] op_sel:[1,0]
	v_mov_b32_e32 v226, v158
	v_mov_b32_e32 v227, v155
	v_pk_add_f32 v[140:141], v[140:141], v[226:227]
	s_nop 0
	v_pk_add_f32 v[226:227], v[140:141], v[140:141] op_sel_hi:[0,1]
	v_pk_mul_f32 v[140:141], v[146:147], v[228:229] op_sel_hi:[1,0]
	v_pk_mul_f32 v[146:147], v[150:151], v[228:229] op_sel_hi:[1,0]
	s_waitcnt lgkmcnt(0)
	v_pk_fma_f32 v[150:151], v[134:135], v[140:141], v[186:187]
	v_pk_fma_f32 v[146:147], v[136:137], v[146:147], v[188:189]
	v_cvt_pk_bf16_f32 v134, v150, v151
	v_cvt_pk_bf16_f32 v135, v146, v147
	global_store_dwordx2 v[156:157], v[134:135], off offset:1536
	ds_read_b128 v[134:137], v169 offset:4096
	ds_read_b128 v[186:189], v197 offset:4096
	v_pk_mul_f32 v[140:141], v[184:185], v[228:229] op_sel_hi:[1,0]
	v_add_f32_e32 v231, v150, v151
	v_add_f32_e32 v233, v146, v147
	s_waitcnt lgkmcnt(0)
	v_pk_fma_f32 v[136:137], v[136:137], v[182:183], v[188:189]
	v_pk_fma_f32 v[140:141], v[134:135], v[140:141], v[186:187]
	v_cvt_pk_bf16_f32 v135, v136, v137
	v_cvt_pk_bf16_f32 v134, v140, v141
	global_store_dwordx2 v[156:157], v[134:135], off offset:2048
	ds_read_b128 v[182:185], v169 offset:5120
	ds_read_b128 v[186:189], v197 offset:5120
	v_mov_b32_e32 v230, v140
	v_mov_b32_e32 v232, v141
	v_mov_b32_e32 v226, v136
	v_mov_b32_e32 v224, v137
	v_pk_add_f32 v[134:135], v[230:231], v[232:233]
	v_pk_add_f32 v[224:225], v[226:227], v[224:225]
	s_waitcnt lgkmcnt(0)
	v_pk_fma_f32 v[142:143], v[184:185], v[142:143], v[188:189]
	v_pk_add_f32 v[134:135], v[134:135], v[224:225]
	v_mov_b32_e32 v227, v143
	v_pk_add_f32 v[224:225], v[134:135], v[134:135] op_sel_hi:[0,1]
	v_pk_mul_f32 v[134:135], v[144:145], v[228:229] op_sel_hi:[1,0]
	s_nop 0
	v_pk_fma_f32 v[144:145], v[182:183], v[134:135], v[186:187]
	v_cvt_pk_bf16_f32 v135, v142, v143
	v_cvt_pk_bf16_f32 v134, v144, v145
	global_store_dwordx2 v[156:157], v[134:135], off offset:2560
	ds_read_b128 v[182:185], v169 offset:6144
	ds_read_b128 v[186:189], v197 offset:6144
	v_pk_mov_b32 v[134:135], v[144:145], v[142:143] op_sel:[1,0]
	v_mov_b32_e32 v226, v144
	v_pk_add_f32 v[134:135], v[134:135], v[226:227]
	s_waitcnt lgkmcnt(0)
; __device__ __forceinline__ unsigned pk_bf16(float lo, float hi) { const bf16x2_t r = __builtin_convertvector((f32x2){lo, hi}, bf16x2_t); return __builtin_bit_cast(unsigned, r); }
; __device__ __forceinline__ void ph10(LAS unsigned char* lds, int tid, int lane, int wave, int G, int bid) {
;     ...
;         for (int j = 0; j < 8; ++j) { v[j] = v[j] * rstd * gq[64 * j] + bq[64 * j]; xq[64 * j] = (u32x2){pk_bf16(v[j].x, v[j].y), pk_bf16(v[j].z, v[j].w)}; s += (v[j].x + v[j].y) + (v[j].z + v[j].w); }
;         mean = wave_sum(s) * (1.f / D); s2 = 0.f;
; #pragma unroll
;         for (int j = 0; j < 8; ++j) { v[j] = v[j] - mean; s2 += (v[j].x * v[j].x + v[j].y * v[j].y) + (v[j].z * v[j].z + v[j].w * v[j].w); }
	v_pk_fma_f32 v[138:139], v[182:183], v[138:139], v[186:187]
	v_pk_add_f32 v[226:227], v[134:135], v[134:135] op_sel_hi:[0,1]
	v_pk_mul_f32 v[134:135], v[180:181], v[228:229] op_sel_hi:[1,0]
	v_cvt_pk_bf16_f32 v180, v138, v139
	v_pk_fma_f32 v[134:135], v[184:185], v[134:135], v[188:189]
	v_add_f32_e32 v189, v138, v139
	v_cvt_pk_bf16_f32 v181, v134, v135
	global_store_dwordx2 v[156:157], v[180:181], off offset:3072
	ds_read_b128 v[180:183], v169 offset:7168
	ds_read_b128 v[184:187], v197 offset:7168
	v_add_f32_e32 v229, v134, v135
	v_pk_mul_f32 v[132:133], v[132:133], v[228:229] op_sel_hi:[1,0]
	v_pk_mul_f32 v[130:131], v[130:131], v[228:229] op_sel_hi:[1,0]
	s_waitcnt lgkmcnt(0)
	v_pk_fma_f32 v[132:133], v[180:181], v[132:133], v[184:185]
	v_pk_fma_f32 v[130:131], v[182:183], v[130:131], v[186:187]
	v_mov_b32_e32 v188, v132
	v_mov_b32_e32 v228, v133
	v_mov_b32_e32 v226, v130
	v_mov_b32_e32 v224, v131
	v_pk_add_f32 v[180:181], v[188:189], v[228:229]
	v_pk_add_f32 v[182:183], v[226:227], v[224:225]
	s_nop 0
	v_pk_add_f32 v[180:181], v[180:181], v[182:183]
	s_nop 0
	v_add_f32_e32 v180, v180, v181
	ds_bpermute_b32 v181, v191, v180
	s_waitcnt lgkmcnt(0)
	v_add_f32_e32 v180, v180, v181
	ds_bpermute_b32 v181, v192, v180
	s_waitcnt lgkmcnt(0)
	v_add_f32_e32 v180, v180, v181
	ds_bpermute_b32 v181, v193, v180
	s_waitcnt lgkmcnt(0)
	v_add_f32_e32 v180, v180, v181
	ds_bpermute_b32 v181, v194, v180
	s_waitcnt lgkmcnt(0)
	v_add_f32_e32 v180, v180, v181
	ds_bpermute_b32 v181, v195, v180
	s_waitcnt lgkmcnt(0)
	v_add_f32_e32 v182, v180, v181
	ds_bpermute_b32 v183, v196, v182
	v_cvt_pk_bf16_f32 v180, v132, v133
	v_cvt_pk_bf16_f32 v181, v130, v131
	global_store_dwordx2 v[156:157], v[180:181], off offset:3584
	s_waitcnt lgkmcnt(0)
	v_add_f32_e32 v224, v182, v183
	v_fmamk_f32 v179, v224, 0xba000000, v179
	v_fmamk_f32 v153, v224, 0xba000000, v153
	v_fmamk_f32 v161, v224, 0xba000000, v161
	v_fmac_f32_e32 v178, 0xba000000, v224
	v_fmamk_f32 v149, v224, 0xba000000, v149
	v_fmac_f32_e32 v152, 0xba000000, v224
	v_mov_b32_e32 v184, v179
	v_mov_b32_e32 v185, v153
	v_fmac_f32_e32 v160, 0xba000000, v224
	v_fmac_f32_e32 v148, 0xba000000, v224
	v_mov_b32_e32 v182, v178
	v_mov_b32_e32 v183, v152
	v_pk_mul_f32 v[184:185], v[184:185], v[184:185]
	v_mov_b32_e32 v186, v161
	v_mov_b32_e32 v187, v149
	v_pk_fma_f32 v[182:183], v[182:183], v[182:183], v[184:185]
	v_mov_b32_e32 v184, v160
	v_mov_b32_e32 v185, v148
	v_pk_mul_f32 v[186:187], v[186:187], v[186:187]
	v_fmamk_f32 v159, v224, 0xba000000, v159
	v_pk_fma_f32 v[184:185], v[184:185], v[184:185], v[186:187]
	v_fmac_f32_e32 v158, 0xba000000, v224
	v_pk_add_f32 v[182:183], v[182:183], v[184:185]
	v_fmamk_f32 v155, v224, 0xba000000, v155
	v_fmac_f32_e32 v154, 0xba000000, v224
	v_pk_add_f32 v[182:183], v[182:183], v[182:183] op_sel_hi:[0,1]
	v_pk_mul_f32 v[184:185], v[154:155], v[154:155]
	v_pk_mul_f32 v[186:187], v[158:159], v[158:159]
	v_fmac_f32_e32 v150, 0xba000000, v224
	v_pk_mov_b32 v[188:189], v[186:187], v[184:185] op_sel:[1,0]
	v_mov_b32_e32 v187, v185
	v_fmamk_f32 v151, v224, 0xba000000, v151
	v_fmac_f32_e32 v146, 0xba000000, v224
	v_mul_f32_e32 v182, v150, v150
	v_pk_add_f32 v[184:185], v[188:189], v[186:187]
	v_fmamk_f32 v147, v224, 0xba000000, v147
	v_pk_fma_f32 v[186:187], v[150:151], v[150:151], v[182:183] op_sel_hi:[1,1,0]
	v_mul_f32_e32 v182, v146, v146
	v_pk_add_f32 v[184:185], v[184:185], v[184:185] op_sel_hi:[0,1]
	v_pk_fma_f32 v[188:189], v[146:147], v[146:147], v[182:183] op_sel_hi:[1,1,0]
	v_fmamk_f32 v137, v224, 0xba000000, v137
	v_fmac_f32_e32 v136, 0xba000000, v224
	v_fmamk_f32 v141, v224, 0xba000000, v141
	v_fmac_f32_e32 v140, 0xba000000, v224
	v_mul_f32_e32 v186, v140, v140
	v_mul_f32_e32 v188, v141, v141
	v_mul_f32_e32 v184, v136, v136
	v_mul_f32_e32 v182, v137, v137
	v_pk_add_f32 v[186:187], v[186:187], v[188:189]
	v_pk_add_f32 v[182:183], v[184:185], v[182:183]
	v_fmamk_f32 v145, v224, 0xba000000, v145
	v_pk_add_f32 v[182:183], v[186:187], v[182:183]
	v_fmac_f32_e32 v144, 0xba000000, v224
	v_fmamk_f32 v143, v224, 0xba000000, v143
	v_fmac_f32_e32 v142, 0xba000000, v224
	v_pk_add_f32 v[182:183], v[182:183], v[182:183] op_sel_hi:[0,1]
	v_pk_mul_f32 v[184:185], v[142:143], v[142:143]
	v_pk_mul_f32 v[186:187], v[144:145], v[144:145]
	v_fmac_f32_e32 v138, 0xba000000, v224
	v_pk_mov_b32 v[188:189], v[186:187], v[184:185] op_sel:[1,0]
	v_mov_b32_e32 v187, v185
	v_fmamk_f32 v139, v224, 0xba000000, v139
	v_fmac_f32_e32 v134, 0xba000000, v224
	v_mul_f32_e32 v182, v138, v138
	v_pk_add_f32 v[184:185], v[188:189], v[186:187]
	v_fmamk_f32 v135, v224, 0xba000000, v135
	v_pk_fma_f32 v[186:187], v[138:139], v[138:139], v[182:183] op_sel_hi:[1,1,0]
	v_mul_f32_e32 v182, v134, v134
	v_pk_add_f32 v[184:185], v[184:185], v[184:185] op_sel_hi:[0,1]
	v_pk_fma_f32 v[188:189], v[134:135], v[134:135], v[182:183] op_sel_hi:[1,1,0]
	v_fmamk_f32 v131, v224, 0xba000000, v131
	v_fmac_f32_e32 v130, 0xba000000, v224
	v_fmamk_f32 v133, v224, 0xba000000, v133
	v_fmac_f32_e32 v132, 0xba000000, v224
	v_mul_f32_e32 v186, v132, v132
	v_mul_f32_e32 v188, v133, v133
	v_mul_f32_e32 v184, v130, v130
	v_mul_f32_e32 v182, v131, v131
	v_pk_add_f32 v[186:187], v[186:187], v[188:189]
	v_pk_add_f32 v[182:183], v[184:185], v[182:183]
	s_nop 0
	v_pk_add_f32 v[182:183], v[186:187], v[182:183]
	s_nop 0
	v_add_f32_e32 v182, v182, v183
	ds_bpermute_b32 v183, v191, v182
	s_waitcnt lgkmcnt(0)
	v_add_f32_e32 v182, v182, v183
	ds_bpermute_b32 v183, v192, v182
	s_waitcnt lgkmcnt(0)
	v_add_f32_e32 v182, v182, v183
	ds_bpermute_b32 v183, v193, v182
	s_waitcnt lgkmcnt(0)
	v_add_f32_e32 v182, v182, v183
	ds_bpermute_b32 v183, v194, v182
	s_waitcnt lgkmcnt(0)
; #define LAS __attribute__((address_space(3)))
; __device__ __forceinline__ unsigned pk_bf16(float lo, float hi) { const bf16x2_t r = __builtin_convertvector((f32x2){lo, hi}, bf16x2_t); return __builtin_bit_cast(unsigned, r); }
; __device__ __forceinline__ unsigned pk4_fp8(float a, float b, float c, float d) { int w = 0; w = __builtin_amdgcn_cvt_pk_fp8_f32(clamp8(a), clamp8(b), w, false); w = __builtin_amdgcn_cvt_pk_fp8_f32(clamp8(c), clamp8(d), w, true); return (unsigned)w; }
; __device__ __forceinline__ void ph10(LAS unsigned char* lds, int tid, int lane, int wave, int G, int bid) {
;     ...
;         rstd = 1.f / sqrtf(wave_sum(s2) * (1.f / D) + LN_EPS);
;         const LAS f32x4* scq = VEC + 1024 + lane; const LAS f32x4* shq = VEC + 1536 + lane; unsigned* o8 = (unsigned*)(H2 + gtok * D) + lane;
; #pragma unroll
;         for (int j = 0; j < 8; ++j) { const f32x4 y = v[j] * rstd * scq[64 * j] + shq[64 * j];
;             const u32x2 hi = (u32x2){pk_bf16(y.x, y.y), pk_bf16(y.z, y.w)};
;             o8[64 * j] = pk4_fp8(y.x, y.y, y.z, y.w);
;             *(LAS u32x2*)(Hhi + row * RS + (256 * j + 4 * lane) * 2) = hi; } };
	v_add_f32_e32 v182, v182, v183
	ds_bpermute_b32 v183, v195, v182
	s_waitcnt lgkmcnt(0)
	v_add_f32_e32 v182, v182, v183
	ds_bpermute_b32 v183, v196, v182
	s_waitcnt lgkmcnt(0)
	v_add_f32_e32 v182, v182, v183
	v_fmamk_f32 v182, v182, 0x3a000000, v207
	v_mul_f32_e32 v183, 0x4f800000, v182
	v_cmp_gt_f32_e32 vcc, s69, v182
	s_nop 1
	v_cndmask_b32_e32 v182, v182, v183, vcc
	v_sqrt_f32_e32 v183, v182
	s_nop 0
	v_add_u32_e32 v184, -1, v183
	v_fma_f32 v185, -v184, v183, v182
	v_cmp_ge_f32_e64 s[10:11], 0, v185
	v_add_u32_e32 v185, 1, v183
	s_nop 0
	v_cndmask_b32_e64 v184, v183, v184, s[10:11]
	v_fma_f32 v183, -v185, v183, v182
	v_cmp_lt_f32_e64 s[10:11], 0, v183
	s_nop 1
	v_cndmask_b32_e64 v183, v184, v185, s[10:11]
	v_mul_f32_e32 v184, 0x37800000, v183
	v_cndmask_b32_e32 v183, v183, v184, vcc
	v_cmp_class_f32_e32 vcc, v182, v208
	s_nop 1
	v_cndmask_b32_e32 v188, v183, v182, vcc
	v_div_scale_f32 v182, s[10:11], v188, v188, 1.0
	v_rcp_f32_e32 v189, v182
	s_nop 0
	v_fma_f32 v156, -v182, v189, 1.0
	v_fmac_f32_e32 v189, v156, v189
	v_div_scale_f32 v156, vcc, 1.0, v188, 1.0
	v_mul_f32_e32 v157, v156, v189
	v_fma_f32 v180, -v182, v157, v156
	v_fmac_f32_e32 v157, v180, v189
	v_fma_f32 v156, -v182, v157, v156
	ds_read_b128 v[180:183], v198
	ds_read_b128 v[184:187], v199
	v_div_fmas_f32 v156, v156, v189, v157
	v_div_fixup_f32 v188, v156, v188, 1.0
	v_pk_mul_f32 v[156:157], v[178:179], v[188:189] op_sel_hi:[1,0]
	v_pk_mul_f32 v[160:161], v[160:161], v[188:189] op_sel_hi:[1,0]
	s_waitcnt lgkmcnt(0)
	v_pk_fma_f32 v[156:157], v[180:181], v[156:157], v[184:185]
	v_mov_b32_e32 v180, v163
	v_med3_f32 v178, v156, s70, v212
	v_med3_f32 v179, v157, s70, v212
	v_cvt_pk_fp8_f32 v180, v178, v179
	v_pk_fma_f32 v[160:161], v[182:183], v[160:161], v[186:187]
	v_lshl_add_u64 v[186:187], v[174:175], 0, s[12:13]
	v_med3_f32 v178, v160, s70, v212
	v_med3_f32 v179, v161, s70, v212
	v_cvt_pk_fp8_f32 v180, v178, v179 op_sel:[0,0,1]
	v_cvt_pk_bf16_f32 v156, v156, v157
	v_cvt_pk_bf16_f32 v157, v160, v161
	v_pk_mul_f32 v[152:153], v[152:153], v[188:189] op_sel_hi:[1,0]
	global_store_dword v[186:187], v180, off
	ds_write_b64 v223, v[156:157] offset:4112
	ds_read_b128 v[178:181], v198 offset:1024
	ds_read_b128 v[182:185], v199 offset:1024
	v_mov_b32_e32 v160, v163
	v_pk_mul_f32 v[148:149], v[148:149], v[188:189] op_sel_hi:[1,0]
	v_pk_mul_f32 v[146:147], v[146:147], v[188:189] op_sel_hi:[1,0]
	v_pk_mul_f32 v[140:141], v[140:141], v[188:189] op_sel_hi:[1,0]
	s_waitcnt lgkmcnt(0)
	v_pk_fma_f32 v[152:153], v[178:179], v[152:153], v[182:183]
	v_pk_fma_f32 v[148:149], v[180:181], v[148:149], v[184:185]
	v_med3_f32 v156, v152, s70, v212
	v_med3_f32 v157, v153, s70, v212
	v_cvt_pk_fp8_f32 v160, v156, v157
	v_med3_f32 v156, v148, s70, v212
	v_med3_f32 v157, v149, s70, v212
	v_cvt_pk_bf16_f32 v152, v152, v153
	v_cvt_pk_fp8_f32 v160, v156, v157 op_sel:[0,0,1]
	v_cvt_pk_bf16_f32 v153, v148, v149
	v_pk_mul_f32 v[148:149], v[158:159], v[188:189] op_sel_hi:[1,0]
	v_mov_b32_e32 v156, v163
	global_store_dword v[186:187], v160, off offset:256
	ds_write_b64 v223, v[152:153] offset:4624
	ds_read_b128 v[178:181], v198 offset:2048
	ds_read_b128 v[182:185], v199 offset:2048
	v_pk_mul_f32 v[152:153], v[154:155], v[188:189] op_sel_hi:[1,0]
	v_pk_mul_f32 v[136:137], v[136:137], v[188:189] op_sel_hi:[1,0]
	v_pk_mul_f32 v[134:135], v[134:135], v[188:189] op_sel_hi:[1,0]
	v_pk_mul_f32 v[132:133], v[132:133], v[188:189] op_sel_hi:[1,0]
	s_waitcnt lgkmcnt(0)
	v_pk_fma_f32 v[148:149], v[178:179], v[148:149], v[182:183]
	v_pk_fma_f32 v[152:153], v[180:181], v[152:153], v[184:185]
	v_med3_f32 v154, v148, s70, v212
	v_med3_f32 v155, v149, s70, v212
	v_cvt_pk_fp8_f32 v156, v154, v155
	v_med3_f32 v154, v152, s70, v212
	v_med3_f32 v155, v153, s70, v212
	v_cvt_pk_bf16_f32 v148, v148, v149
	v_cvt_pk_fp8_f32 v156, v154, v155 op_sel:[0,0,1]
	v_cvt_pk_bf16_f32 v149, v152, v153
	v_pk_mul_f32 v[130:131], v[130:131], v[188:189] op_sel_hi:[1,0]
	global_store_dword v[186:187], v156, off offset:512
	ds_write_b64 v223, v[148:149] offset:5136
	ds_read_b128 v[152:155], v198 offset:3072
	ds_read_b128 v[156:159], v199 offset:3072
	v_pk_mul_f32 v[148:149], v[150:151], v[188:189] op_sel_hi:[1,0]
	s_waitcnt lgkmcnt(0)
	v_pk_fma_f32 v[146:147], v[154:155], v[146:147], v[158:159]
	v_pk_fma_f32 v[148:149], v[152:153], v[148:149], v[156:157]
	v_mov_b32_e32 v152, v163
	v_med3_f32 v150, v148, s70, v212
	v_med3_f32 v151, v149, s70, v212
	v_cvt_pk_fp8_f32 v152, v150, v151
	v_med3_f32 v150, v146, s70, v212
	v_med3_f32 v151, v147, s70, v212
	v_cvt_pk_bf16_f32 v148, v148, v149
	v_cvt_pk_fp8_f32 v152, v150, v151 op_sel:[0,0,1]
	v_cvt_pk_bf16_f32 v149, v146, v147
	global_store_dword v[186:187], v152, off offset:768
	ds_write_b64 v223, v[148:149] offset:5648
	ds_read_b128 v[146:149], v198 offset:4096
	ds_read_b128 v[150:153], v199 offset:4096
	s_waitcnt lgkmcnt(0)
; #define LAS __attribute__((address_space(3)))
; __device__ __forceinline__ unsigned pk_bf16(float lo, float hi) { const bf16x2_t r = __builtin_convertvector((f32x2){lo, hi}, bf16x2_t); return __builtin_bit_cast(unsigned, r); }
; __device__ __forceinline__ unsigned pk4_fp8(float a, float b, float c, float d) { int w = 0; w = __builtin_amdgcn_cvt_pk_fp8_f32(clamp8(a), clamp8(b), w, false); w = __builtin_amdgcn_cvt_pk_fp8_f32(clamp8(c), clamp8(d), w, true); return (unsigned)w; }
; __device__ __forceinline__ void ph10(LAS unsigned char* lds, int tid, int lane, int wave, int G, int bid) {
;     ...
;         for (int j = 0; j < 8; ++j) { const f32x4 y = v[j] * rstd * scq[64 * j] + shq[64 * j];
;             const u32x2 hi = (u32x2){pk_bf16(y.x, y.y), pk_bf16(y.z, y.w)};
;             o8[64 * j] = pk4_fp8(y.x, y.y, y.z, y.w);
;             *(LAS u32x2*)(Hhi + row * RS + (256 * j + 4 * lane) * 2) = hi; } };
;     ...
;             __syncthreads();
;             f32x4 acc[3];
; #pragma unroll
;             for (int nt = 0; nt < 3; ++nt) acc[nt] = (f32x4){0.f, 0.f, 0.f, 0.f};
; #pragma unroll
;             for (int ks = 0; ks < 8; ++ks) { const int k = 256 * wave + 32 * ks + 8 * fq;
;                 const bf16x8 ahi = *(const LAS bf16x8*)(Hhi + fr * RS + k * 2);
; #pragma unroll
;                 for (int nt = 0; nt < 3; ++nt) acc[nt] = __builtin_amdgcn_mfma_f32_16x16x32_bf16(ahi, wf[ks][nt], acc[nt], 0, 0, 0); }
;             __syncthreads();
; #pragma unroll
;             for (int nt = 0; nt < 3; ++nt)
; #pragma unroll
;                 for (int j = 0; j < 4; ++j) Pp[(wave * 16 + 4 * fq + j) * 48 + 16 * nt + fr] = acc[nt][j];
;             __syncthreads();
;             for (int i = tid; i < 16 * 36; i += 512) { const int tk = i / 36, n = i % 36; float s = 0.f;
	v_pk_fma_f32 v[140:141], v[146:147], v[140:141], v[150:151]
	s_nop 0
	v_med3_f32 v146, v140, s70, v212
	v_med3_f32 v147, v141, s70, v212
	v_mov_b32_e32 v150, v163
	v_cvt_pk_fp8_f32 v150, v146, v147
	v_pk_fma_f32 v[136:137], v[148:149], v[136:137], v[152:153]
	v_cvt_pk_bf16_f32 v140, v140, v141
	v_med3_f32 v146, v136, s70, v212
	v_med3_f32 v147, v137, s70, v212
	v_cvt_pk_fp8_f32 v150, v146, v147 op_sel:[0,0,1]
	v_cvt_pk_bf16_f32 v141, v136, v137
	v_pk_mul_f32 v[136:137], v[144:145], v[188:189] op_sel_hi:[1,0]
	v_mov_b32_e32 v144, v163
	global_store_dword v[186:187], v150, off offset:1024
	ds_write_b64 v223, v[140:141] offset:6160
	ds_read_b128 v[146:149], v198 offset:5120
	ds_read_b128 v[150:153], v199 offset:5120
	v_pk_mul_f32 v[140:141], v[142:143], v[188:189] op_sel_hi:[1,0]
	s_waitcnt lgkmcnt(0)
	v_pk_fma_f32 v[136:137], v[146:147], v[136:137], v[150:151]
	s_nop 0
	v_med3_f32 v142, v136, s70, v212
	v_med3_f32 v143, v137, s70, v212
	v_cvt_pk_fp8_f32 v144, v142, v143
	v_pk_fma_f32 v[140:141], v[148:149], v[140:141], v[152:153]
	v_cvt_pk_bf16_f32 v136, v136, v137
	v_med3_f32 v142, v140, s70, v212
	v_med3_f32 v143, v141, s70, v212
	v_cvt_pk_fp8_f32 v144, v142, v143 op_sel:[0,0,1]
	v_cvt_pk_bf16_f32 v137, v140, v141
	global_store_dword v[186:187], v144, off offset:1280
	ds_write_b64 v223, v[136:137] offset:6672
	ds_read_b128 v[140:143], v198 offset:6144
	ds_read_b128 v[144:147], v199 offset:6144
	v_pk_mul_f32 v[136:137], v[138:139], v[188:189] op_sel_hi:[1,0]
	s_waitcnt lgkmcnt(0)
	v_pk_fma_f32 v[134:135], v[142:143], v[134:135], v[146:147]
	v_pk_fma_f32 v[136:137], v[140:141], v[136:137], v[144:145]
	v_mov_b32_e32 v140, v163
	v_med3_f32 v138, v136, s70, v212
	v_med3_f32 v139, v137, s70, v212
	v_cvt_pk_fp8_f32 v140, v138, v139
	v_med3_f32 v138, v134, s70, v212
	v_med3_f32 v139, v135, s70, v212
	v_cvt_pk_bf16_f32 v136, v136, v137
	v_cvt_pk_fp8_f32 v140, v138, v139 op_sel:[0,0,1]
	v_cvt_pk_bf16_f32 v137, v134, v135
	global_store_dword v[186:187], v140, off offset:1536
	ds_write_b64 v223, v[136:137] offset:7184
	ds_read_b128 v[134:137], v198 offset:7168
	ds_read_b128 v[138:141], v199 offset:7168
	s_waitcnt lgkmcnt(0)
	v_pk_fma_f32 v[132:133], v[132:133], v[134:135], v[138:139]
	s_nop 0
	v_med3_f32 v134, v132, s70, v212
	v_med3_f32 v135, v133, s70, v212
	v_mov_b32_e32 v138, v163
	v_cvt_pk_fp8_f32 v138, v134, v135
	v_pk_fma_f32 v[130:131], v[130:131], v[136:137], v[140:141]
	v_cvt_pk_bf16_f32 v132, v132, v133
	v_med3_f32 v134, v130, s70, v212
	v_med3_f32 v135, v131, s70, v212
	v_cvt_pk_fp8_f32 v138, v134, v135 op_sel:[0,0,1]
	v_cvt_pk_bf16_f32 v133, v130, v131
	global_store_dword v[186:187], v138, off offset:1792
	ds_write_b64 v223, v[132:133] offset:7696
	s_waitcnt lgkmcnt(0)
	s_barrier
	ds_read_b128 v[130:133], v209
	ds_read_b128 v[134:137], v209 offset:64
	s_waitcnt lgkmcnt(0)
	v_mfma_f32_16x16x32_bf16 v[138:141], v[130:133], v[10:13], 0
	v_mfma_f32_16x16x32_bf16 v[142:145], v[130:133], v[2:5], 0
	v_mfma_f32_16x16x32_bf16 v[130:133], v[130:133], v[6:9], 0
	v_mfma_f32_16x16x32_bf16 v[138:141], v[134:137], v[14:17], v[138:141]
	v_mfma_f32_16x16x32_bf16 v[142:145], v[134:137], v[18:21], v[142:145]
	v_mfma_f32_16x16x32_bf16 v[130:133], v[134:137], v[22:25], v[130:133]
	ds_read_b128 v[134:137], v209 offset:128
	ds_read_b128 v[146:149], v209 offset:192
	s_waitcnt lgkmcnt(0)
	v_mfma_f32_16x16x32_bf16 v[138:141], v[134:137], v[34:37], v[138:141]
	v_mfma_f32_16x16x32_bf16 v[142:145], v[134:137], v[26:29], v[142:145]
	v_mfma_f32_16x16x32_bf16 v[130:133], v[134:137], v[30:33], v[130:133]
	v_mfma_f32_16x16x32_bf16 v[134:137], v[146:149], v[38:41], v[138:141]
	v_mfma_f32_16x16x32_bf16 v[138:141], v[146:149], v[42:45], v[142:145]
	v_mfma_f32_16x16x32_bf16 v[130:133], v[146:149], v[46:49], v[130:133]
	s_nop 3
	ds_read_b128 v[142:145], v209 offset:256
	ds_read_b128 v[146:149], v209 offset:320
	s_waitcnt lgkmcnt(0)
	v_mfma_f32_16x16x32_bf16 v[134:137], v[142:145], v[58:61], v[134:137]
	v_mfma_f32_16x16x32_bf16 v[138:141], v[142:145], v[50:53], v[138:141]
	v_mfma_f32_16x16x32_bf16 v[130:133], v[142:145], v[54:57], v[130:133]
	v_mfma_f32_16x16x32_bf16 v[134:137], v[146:149], v[62:65], v[134:137]
	v_mfma_f32_16x16x32_bf16 v[138:141], v[146:149], v[66:69], v[138:141]
	v_mfma_f32_16x16x32_bf16 v[130:133], v[146:149], v[70:73], v[130:133]
	ds_read_b128 v[142:145], v209 offset:384
	ds_read_b128 v[146:149], v209 offset:448
	s_waitcnt lgkmcnt(0)
	s_barrier
	v_mfma_f32_16x16x32_bf16 v[134:137], v[142:145], v[82:85], v[134:137]
	v_mfma_f32_16x16x32_bf16 v[138:141], v[142:145], v[74:77], v[138:141]
	v_mfma_f32_16x16x32_bf16 v[130:133], v[142:145], v[78:81], v[130:133]
	v_mfma_f32_16x16x32_bf16 v[134:137], v[146:149], v[86:89], v[134:137]
	v_mfma_f32_16x16x32_bf16 v[138:141], v[146:149], v[90:93], v[138:141]
	v_mfma_f32_16x16x32_bf16 v[130:133], v[146:149], v[94:97], v[130:133]
	s_nop 6
	ds_write2_b32 v210, v134, v138 offset1:16
	ds_write2_b32 v210, v136, v140 offset0:96 offset1:112
	ds_write2_b32 v210, v130, v135 offset0:32 offset1:48
	ds_write2_b32 v210, v139, v131 offset0:64 offset1:80
	ds_write2_b32 v210, v132, v137 offset0:128 offset1:144
	ds_write2_b32 v210, v141, v133 offset0:160 offset1:176
	s_waitcnt lgkmcnt(0)
	s_barrier
	s_and_saveexec_b64 s[10:11], s[8:9]
	s_cbranch_execz .LBB0_979
	s_mov_b64 s[12:13], 0
	v_mov_b32_e32 v130, v206
	v_mov_b32_e32 v131, v0

; #define LAS __attribute__((address_space(3)))
; #define AIN(i) ((const float*)ldp(lds, (i)))
; #define AOUT ((float*)ldp(lds, NIN))
; #define AWS ((unsigned char*)ldp(lds, NIN + 1))
; __device__ __forceinline__ void ph13(LAS unsigned char* lds, int tid, int lane_, int wave, int G, int bid) {
;     ...
;     unsigned char* ws = AWS; float* X = AOUT; const bf16* XM = (const bf16*)(ws + WS_XMID); const unsigned char* Y = (const unsigned char*)(ws + WS_RB); const float* rw = (const float*)(ws + WS_RW); const float* modv = (const float*)(ws + WS_MODV);
;     LAS f32x4* VG = (LAS f32x4*)lds;
;     { const f32x4* g2 = (const f32x4*)AIN(ILN2G); const f32x4* b2 = (const f32x4*)AIN(ILN2B);
;       for (int i = tid; i < 6 * 512; i += NWAVES * 64) { const int r = i >> 9, q = i & 511; VG[i] = r < 4 ? *((const f32x4*)(modv + (size_t)r * 12288 + 5 * D) + q) : (r == 4 ? g2[q] : b2[q]); } }
;     __syncthreads();
;     const int gw = bid * NWAVES + wave, NGW = G * NWAVES;
;     unsigned p0[8], p1[8]; u32x2 xb[8]; float w0, w1;
;     { const int m = gw; const u32x2* xm = (const u32x2*)(XM + (size_t)m * D) + lane; const unsigned* y0 = (const unsigned*)(Y + (size_t)(2 * m) * D) + lane; const unsigned* y1 = y0 + D / 4;
; #pragma unroll
;       for (int j = 0; j < 8; ++j) { p0[j] = __builtin_nontemporal_load(y0 + 64 * j); p1[j] = __builtin_nontemporal_load(y1 + 64 * j); xb[j] = __builtin_nontemporal_load(xm + 64 * j); }
;       w0 = rw[2 * m]; w1 = rw[2 * m + 1]; }
;     for (int m = gw; m < T; m += NGW) {
;         unsigned q0[8], q1[8]; u32x2 xn[8]; float wn0 = 0.f, wn1 = 0.f; const int mn = m + NGW;
;         if (mn < T) { const u32x2* xm = (const u32x2*)(XM + (size_t)mn * D) + lane; const unsigned* y0 = (const unsigned*)(Y + (size_t)(2 * mn) * D) + lane; const unsigned* y1 = y0 + D / 4;
; #pragma unroll
;             for (int j = 0; j < 8; ++j) { q0[j] = __builtin_nontemporal_load(y0 + 64 * j); q1[j] = __builtin_nontemporal_load(y1 + 64 * j); xn[j] = __builtin_nontemporal_load(xm + 64 * j); }
;             wn0 = rw[2 * mn]; wn1 = rw[2 * mn + 1]; }
.LBB0_1214:
	s_or_b64 exec, exec, s[0:1]
	s_lshl_b32 s0, s2, 3
	s_add_i32 s0, s3, s0
	s_cmp_lt_i32 s0, 0x8000
	s_waitcnt lgkmcnt(0)
	s_barrier
	s_cbranch_scc0 .LBB0_1220
	s_add_u32 s4, s8, 0x2e000000
	s_addc_u32 s5, s9, 0
	s_add_u32 s14, s8, 0xc00000
	s_addc_u32 s15, s9, 0
	s_ashr_i32 s1, s0, 31
	v_mbcnt_lo_u32_b32 v0, -1, 0
	s_lshl_b32 s2, s33, 3
	s_lshl_b64 s[6:7], s[0:1], 12
	v_mbcnt_hi_u32_b32 v1, -1, v0
	v_mov_b32_e32 v0, 0
	s_add_u32 s6, s8, s6
	s_addc_u32 s7, s9, s7
	v_lshlrev_b32_e32 v6, 3, v1
	v_mov_b32_e32 v7, v0
	v_lshl_add_u64 v[4:5], s[6:7], 0, v[6:7]
	s_lshl_b32 s6, s0, 1
	s_ashr_i32 s7, s6, 31
	s_lshl_b64 s[16:17], s[6:7], 11
	s_add_u32 s16, s4, s16
	v_lshlrev_b32_e32 v2, 2, v1
	v_mov_b32_e32 v3, v0
	s_mov_b64 s[10:11], 0xe000000
	s_addc_u32 s17, s5, s17
	s_mov_b32 s3, 0xe000000
	v_lshl_add_u64 v[8:9], v[4:5], 0, s[10:11]
	v_lshl_add_u64 v[10:11], s[16:17], 0, v[2:3]
	v_add_co_u32_e32 v4, vcc, s3, v4
	global_load_dwordx2 v[26:27], v[8:9], off offset:3584 nt
	global_load_dword v85, v[10:11], off nt
	global_load_dwordx2 v[28:29], v[8:9], off offset:3072 nt
	global_load_dwordx2 v[30:31], v[8:9], off offset:2560 nt
	global_load_dwordx2 v[40:41], v[8:9], off offset:2048 nt
	global_load_dwordx2 v[42:43], v[8:9], off offset:1536 nt
	global_load_dwordx2 v[44:45], v[8:9], off offset:1024 nt
	global_load_dwordx2 v[34:35], v[8:9], off offset:512 nt
	v_addc_co_u32_e32 v5, vcc, 0, v5, vcc
	global_load_dword v84, v[10:11], off offset:3840 nt
	global_load_dwordx2 v[32:33], v[4:5], off nt
	global_load_dword v55, v[10:11], off offset:3584 nt
	global_load_dword v53, v[10:11], off offset:3328 nt
	global_load_dword v51, v[10:11], off offset:3072 nt
	global_load_dword v49, v[10:11], off offset:2816 nt
	global_load_dword v47, v[10:11], off offset:2560 nt
	global_load_dword v39, v[10:11], off offset:2304 nt
	global_load_dword v57, v[10:11], off offset:1792 nt
	global_load_dword v86, v[10:11], off offset:2048 nt
	global_load_dword v54, v[10:11], off offset:1536 nt
	global_load_dword v52, v[10:11], off offset:1280 nt
	global_load_dword v50, v[10:11], off offset:1024 nt
	global_load_dword v48, v[10:11], off offset:768 nt
	global_load_dword v46, v[10:11], off offset:512 nt
	global_load_dword v38, v[10:11], off offset:256 nt
	s_lshl_b64 s[6:7], s[6:7], 2
	s_add_u32 s6, s14, s6
	s_addc_u32 s7, s15, s7
	v_mov_b64_e32 v[4:5], s[6:7]
	global_load_dwordx2 v[36:37], v[4:5], off
	v_and_b32_e32 v5, 64, v1
	v_add_u32_e32 v5, 64, v5
	v_xor_b32_e32 v8, 1, v1
	v_cmp_lt_i32_e32 vcc, v8, v5
	v_lshl_add_u64 v[2:3], s[4:5], 0, v[2:3]
	s_lshl_b64 s[4:5], s[0:1], 13
	v_cndmask_b32_e32 v8, v1, v8, vcc
	v_lshlrev_b32_e32 v60, 2, v8
	v_xor_b32_e32 v8, 2, v1
	v_cmp_lt_i32_e32 vcc, v8, v5
	s_add_u32 s4, s12, s4
	v_lshlrev_b32_e32 v4, 4, v1
	v_cndmask_b32_e32 v8, v1, v8, vcc
	v_lshlrev_b32_e32 v61, 2, v8
	v_xor_b32_e32 v8, 4, v1
	v_cmp_lt_i32_e32 vcc, v8, v5
	s_addc_u32 s5, s13, s5
	s_add_i32 s12, s0, s2
	v_cndmask_b32_e32 v8, v1, v8, vcc
	v_lshlrev_b32_e32 v62, 2, v8
	v_xor_b32_e32 v8, 8, v1
	v_cmp_lt_i32_e32 vcc, v8, v5
	v_add_u32_e32 v59, 0, v4
	s_ashr_i32 s3, s2, 31
	v_cndmask_b32_e32 v8, v1, v8, vcc
	v_lshlrev_b32_e32 v63, 2, v8
	v_xor_b32_e32 v8, 16, v1
	v_cmp_lt_i32_e32 vcc, v8, v5
	s_ashr_i32 s13, s12, 31
	s_lshl_b32 s6, s12, 1
	v_cndmask_b32_e32 v8, v1, v8, vcc
	v_lshlrev_b32_e32 v64, 2, v8
	v_xor_b32_e32 v8, 32, v1
	v_cmp_lt_i32_e32 vcc, v8, v5
	v_mov_b32_e32 v5, v0
	v_lshl_add_u64 v[4:5], s[4:5], 0, v[4:5]
	s_mov_b64 s[4:5], 0x1000
	v_lshl_add_u64 v[4:5], v[4:5], 0, s[4:5]
	s_lshl_b64 s[4:5], s[2:3], 13
	s_lshl_b32 s16, s33, 4
	s_lshl_b64 s[12:13], s[12:13], 12
	s_add_u32 s8, s8, s12
	s_addc_u32 s9, s9, s13
	v_cndmask_b32_e32 v1, v1, v8, vcc
	v_lshl_add_u64 v[6:7], s[8:9], 0, v[6:7]
	v_lshlrev_b32_e32 v65, 2, v1
	v_lshl_add_u64 v[6:7], v[6:7], 0, s[10:11]
	s_lshl_b64 s[8:9], s[2:3], 12
	s_mov_b32 s10, 0x3f9837f0
	v_mov_b32_e32 v66, 0x3727c5ac
	s_mov_b32 s3, 0xf800000
	v_mov_b32_e32 v67, 0x260
	s_movk_i32 s11, 0xf000
	s_movk_i32 s17, 0xf400
	s_movk_i32 s18, 0xf800
	s_movk_i32 s19, 0xfc00
	s_waitcnt vmcnt(0)
	s_branch .LBB0_1218
.LBB0_1216:
	s_ashr_i32 s7, s6, 31
	s_lshl_b64 s[22:23], s[6:7], 11
	v_lshl_add_u64 v[24:25], v[2:3], 0, s[22:23]
	global_load_dwordx2 v[8:9], v[6:7], off nt
	global_load_dwordx2 v[10:11], v[6:7], off offset:512 nt
	global_load_dwordx2 v[12:13], v[6:7], off offset:1024 nt
	global_load_dwordx2 v[14:15], v[6:7], off offset:1536 nt
	global_load_dword v68, v[24:25], off nt
	global_load_dword v69, v[24:25], off offset:256 nt
	global_load_dword v70, v[24:25], off offset:512 nt
	global_load_dword v71, v[24:25], off offset:768 nt
	global_load_dword v72, v[24:25], off offset:1024 nt
	global_load_dword v73, v[24:25], off offset:1280 nt
	global_load_dword v74, v[24:25], off offset:1536 nt
	global_load_dword v75, v[24:25], off offset:1792 nt
	global_load_dword v76, v[24:25], off offset:2048 nt
	global_load_dword v77, v[24:25], off offset:2304 nt
	global_load_dword v78, v[24:25], off offset:2560 nt
	global_load_dword v79, v[24:25], off offset:2816 nt
	global_load_dword v80, v[24:25], off offset:3072 nt
	global_load_dword v81, v[24:25], off offset:3328 nt
	global_load_dword v82, v[24:25], off offset:3584 nt
	global_load_dword v83, v[24:25], off offset:3840 nt
	global_load_dwordx2 v[18:19], v[6:7], off offset:2048 nt
	global_load_dwordx2 v[20:21], v[6:7], off offset:2560 nt
	global_load_dwordx2 v[22:23], v[6:7], off offset:3072 nt
	global_load_dwordx2 v[16:17], v[6:7], off offset:3584 nt
	s_lshl_b64 s[22:23], s[6:7], 2
	s_add_u32 s22, s14, s22
	s_addc_u32 s23, s15, s23
	v_mov_b64_e32 v[24:25], s[22:23]
	global_load_dwordx2 v[24:25], v[24:25], off
; #define LAS __attribute__((address_space(3)))
; __device__ __forceinline__ float bf_lo(unsigned u) { return __uint_as_float(u << 16); }
; __device__ __forceinline__ float bf_hi(unsigned u) { return __uint_as_float(u & 0xffff0000u); }
; __device__ __forceinline__ void ph13(LAS unsigned char* lds, int tid, int lane_, int wave, int G, int bid) {
;     ...
;         f32x4* xq = (f32x4*)(X + (size_t)m * D) + lane; const LAS f32x4* gq = VG + (m >> 13) * 512 + lane;
;         const float c0 = w0 * Y8_INV, c1 = w1 * Y8_INV;
;         f32x4 v[8]; float s = 0.f;
; #pragma unroll
;         for (int j = 0; j < 8; ++j) {
;             const f32x2 a0 = __builtin_amdgcn_cvt_pk_f32_fp8((int)p0[j], false), a1 = __builtin_amdgcn_cvt_pk_f32_fp8((int)p0[j], true), b0 = __builtin_amdgcn_cvt_pk_f32_fp8((int)p1[j], false), b1 = __builtin_amdgcn_cvt_pk_f32_fp8((int)p1[j], true);
;             const f32x4 yy = (f32x4){a0.x, a0.y, a1.x, a1.y} * c0 + (f32x4){b0.x, b0.y, b1.x, b1.y} * c1;
;             v[j] = (f32x4){bf_lo(xb[j].x), bf_hi(xb[j].x), bf_lo(xb[j].y), bf_hi(xb[j].y)} * DN_ALPHA + gq[64 * j] * yy; s += (v[j].x + v[j].y) + (v[j].z + v[j].w); }
.LBB0_1217:
	s_waitcnt lgkmcnt(0)
	v_mul_f32_e32 v56, 0x3d800000, v36
	v_mul_f32_e32 v58, 0x3d800000, v37
	v_cvt_pk_f32_fp8_sdwa v[36:37], v86 src0_sel:WORD_1
	v_cvt_pk_f32_fp8_e32 v[86:87], v86
	v_cvt_pk_f32_fp8_e32 v[88:89], v85
	s_and_b32 s0, s0, 0xffffe000
	v_add_u32_e32 v1, s0, v59
	v_pk_mul_f32 v[86:87], v[58:59], v[86:87] op_sel_hi:[0,1]
	v_cvt_pk_f32_fp8_sdwa v[90:91], v85 src0_sel:WORD_1
	v_pk_fma_f32 v[94:95], v[56:57], v[88:89], v[86:87] op_sel_hi:[0,1,1]
	ds_read_b128 v[86:89], v1
	v_pk_mul_f32 v[36:37], v[58:59], v[36:37] op_sel_hi:[0,1]
	v_pk_fma_f32 v[36:37], v[56:57], v[90:91], v[36:37] op_sel_hi:[0,1,1]
	v_lshlrev_b32_e32 v96, 16, v32
	v_and_b32_e32 v97, 0xffff0000, v32
	v_lshlrev_b32_e32 v32, 16, v33
	v_and_b32_e32 v33, 0xffff0000, v33
	ds_read_b128 v[90:93], v1 offset:1024
	s_waitcnt lgkmcnt(1)
	v_pk_mul_f32 v[36:37], v[88:89], v[36:37]
	v_pk_mul_f32 v[86:87], v[86:87], v[94:95]
	v_pk_fma_f32 v[32:33], v[32:33], s[10:11], v[36:37] op_sel_hi:[1,0,1]
	v_pk_fma_f32 v[36:37], v[96:97], s[10:11], v[86:87] op_sel_hi:[1,0,1]
	v_cvt_pk_f32_fp8_sdwa v[86:87], v39 src0_sel:WORD_1
	v_cvt_pk_f32_fp8_e32 v[88:89], v39
	v_cvt_pk_f32_fp8_e32 v[94:95], v38
	v_cvt_pk_f32_fp8_sdwa v[38:39], v38 src0_sel:WORD_1
	v_pk_mul_f32 v[86:87], v[58:59], v[86:87] op_sel_hi:[0,1]
	v_pk_mul_f32 v[88:89], v[58:59], v[88:89] op_sel_hi:[0,1]
	v_pk_fma_f32 v[88:89], v[56:57], v[94:95], v[88:89] op_sel_hi:[0,1,1]
	v_pk_fma_f32 v[38:39], v[56:57], v[38:39], v[86:87] op_sel_hi:[0,1,1]
	v_lshlrev_b32_e32 v86, 16, v34
	v_and_b32_e32 v87, 0xffff0000, v34
	v_lshlrev_b32_e32 v34, 16, v35
	v_and_b32_e32 v35, 0xffff0000, v35
	s_waitcnt lgkmcnt(0)
	v_pk_mul_f32 v[38:39], v[92:93], v[38:39]
	v_pk_mul_f32 v[88:89], v[90:91], v[88:89]
	v_pk_fma_f32 v[34:35], v[34:35], s[10:11], v[38:39] op_sel_hi:[1,0,1]
	v_pk_fma_f32 v[38:39], v[86:87], s[10:11], v[88:89] op_sel_hi:[1,0,1]
	v_mov_b32_e32 v86, v36
	v_mov_b32_e32 v87, v38
	v_mov_b32_e32 v88, v37
	v_mov_b32_e32 v89, v39
	v_pk_add_f32 v[86:87], v[86:87], v[88:89]
	v_mov_b32_e32 v88, v32
	v_mov_b32_e32 v89, v34
	v_mov_b32_e32 v90, v33
	v_mov_b32_e32 v91, v35
	v_pk_add_f32 v[88:89], v[88:89], v[90:91]
	v_cvt_pk_f32_fp8_e32 v[90:91], v46
	v_pk_add_f32 v[86:87], v[86:87], v[88:89]
	v_cvt_pk_f32_fp8_e32 v[88:89], v47
	v_add_f32_e32 v85, 0, v86
	v_add_f32_e32 v94, v85, v87
	v_cvt_pk_f32_fp8_sdwa v[86:87], v47 src0_sel:WORD_1
	v_cvt_pk_f32_fp8_sdwa v[46:47], v46 src0_sel:WORD_1
	v_pk_mul_f32 v[88:89], v[58:59], v[88:89] op_sel_hi:[0,1]
	v_pk_fma_f32 v[96:97], v[56:57], v[90:91], v[88:89] op_sel_hi:[0,1,1]
	v_pk_mul_f32 v[86:87], v[58:59], v[86:87] op_sel_hi:[0,1]
	v_pk_fma_f32 v[46:47], v[56:57], v[46:47], v[86:87] op_sel_hi:[0,1,1]
	ds_read_b128 v[86:89], v1 offset:2048
	ds_read_b128 v[90:93], v1 offset:3072
	v_lshlrev_b32_e32 v98, 16, v44
	v_and_b32_e32 v99, 0xffff0000, v44
	v_lshlrev_b32_e32 v44, 16, v45
	v_and_b32_e32 v45, 0xffff0000, v45
	s_waitcnt lgkmcnt(1)
	v_pk_mul_f32 v[46:47], v[88:89], v[46:47]
	v_pk_mul_f32 v[86:87], v[86:87], v[96:97]
	v_pk_fma_f32 v[46:47], v[44:45], s[10:11], v[46:47] op_sel_hi:[1,0,1]
	v_pk_fma_f32 v[44:45], v[98:99], s[10:11], v[86:87] op_sel_hi:[1,0,1]
	v_mov_b32_e32 v89, v47
	v_pk_mov_b32 v[86:87], v[44:45], v[46:47] op_sel:[1,0]
	v_mov_b32_e32 v88, v44
	v_pk_add_f32 v[86:87], v[86:87], v[88:89]
	v_cvt_pk_f32_fp8_e32 v[88:89], v49
	v_pk_add_f32 v[96:97], v[86:87], v[86:87] op_sel:[0,1] op_sel_hi:[1,0]
	v_cvt_pk_f32_fp8_sdwa v[86:87], v49 src0_sel:WORD_1
	v_cvt_pk_f32_fp8_e32 v[98:99], v48
	v_cvt_pk_f32_fp8_sdwa v[48:49], v48 src0_sel:WORD_1
	v_pk_mul_f32 v[88:89], v[58:59], v[88:89] op_sel_hi:[0,1]
	v_pk_mul_f32 v[86:87], v[58:59], v[86:87] op_sel_hi:[0,1]
	v_pk_fma_f32 v[88:89], v[56:57], v[98:99], v[88:89] op_sel_hi:[0,1,1]
	v_pk_fma_f32 v[48:49], v[56:57], v[48:49], v[86:87] op_sel_hi:[0,1,1]
	v_lshlrev_b32_e32 v86, 16, v42
	v_and_b32_e32 v87, 0xffff0000, v42
	v_lshlrev_b32_e32 v42, 16, v43
	v_and_b32_e32 v43, 0xffff0000, v43
	s_waitcnt lgkmcnt(0)
	v_pk_mul_f32 v[48:49], v[92:93], v[48:49]
	v_pk_mul_f32 v[88:89], v[90:91], v[88:89]
	v_pk_fma_f32 v[42:43], v[42:43], s[10:11], v[48:49] op_sel_hi:[1,0,1]
	v_pk_fma_f32 v[48:49], v[86:87], s[10:11], v[88:89] op_sel_hi:[1,0,1]
	v_cvt_pk_f32_fp8_sdwa v[86:87], v51 src0_sel:WORD_1
	v_cvt_pk_f32_fp8_e32 v[88:89], v51
	v_cvt_pk_f32_fp8_e32 v[90:91], v50
	v_cvt_pk_f32_fp8_sdwa v[50:51], v50 src0_sel:WORD_1
	v_pk_mul_f32 v[86:87], v[58:59], v[86:87] op_sel_hi:[0,1]
	v_pk_mul_f32 v[88:89], v[58:59], v[88:89] op_sel_hi:[0,1]
	v_pk_fma_f32 v[102:103], v[56:57], v[90:91], v[88:89] op_sel_hi:[0,1,1]
	v_pk_fma_f32 v[50:51], v[56:57], v[50:51], v[86:87] op_sel_hi:[0,1,1]
	ds_read_b128 v[86:89], v1 offset:4096
	ds_read_b128 v[90:93], v1 offset:5120
	v_lshlrev_b32_e32 v104, 16, v40
	v_and_b32_e32 v105, 0xffff0000, v40
	v_lshlrev_b32_e32 v40, 16, v41
	v_and_b32_e32 v41, 0xffff0000, v41
	s_waitcnt lgkmcnt(1)
	v_pk_mul_f32 v[50:51], v[88:89], v[50:51]
	v_pk_mul_f32 v[86:87], v[86:87], v[102:103]
	v_pk_fma_f32 v[50:51], v[40:41], s[10:11], v[50:51] op_sel_hi:[1,0,1]
	v_pk_fma_f32 v[40:41], v[104:105], s[10:11], v[86:87] op_sel_hi:[1,0,1]
	v_add_f32_e32 v98, v48, v49
	v_add_f32_e32 v100, v42, v43
	v_mov_b32_e32 v95, v40
	v_mov_b32_e32 v97, v41
	v_mov_b32_e32 v99, v50
	v_mov_b32_e32 v101, v51
	v_pk_add_f32 v[86:87], v[94:95], v[96:97]
	v_pk_add_f32 v[88:89], v[98:99], v[100:101]
	v_cvt_pk_f32_fp8_e32 v[96:97], v52
	v_pk_add_f32 v[86:87], v[86:87], v[88:89]
	v_cvt_pk_f32_fp8_e32 v[88:89], v53
	v_pk_add_f32 v[94:95], v[86:87], v[86:87] op_sel:[0,1] op_sel_hi:[1,0]
	v_cvt_pk_f32_fp8_sdwa v[86:87], v53 src0_sel:WORD_1
	v_cvt_pk_f32_fp8_sdwa v[52:53], v52 src0_sel:WORD_1
	v_pk_mul_f32 v[88:89], v[58:59], v[88:89] op_sel_hi:[0,1]
	v_pk_fma_f32 v[88:89], v[56:57], v[96:97], v[88:89] op_sel_hi:[0,1,1]
	v_pk_mul_f32 v[86:87], v[58:59], v[86:87] op_sel_hi:[0,1]
	v_pk_fma_f32 v[52:53], v[56:57], v[52:53], v[86:87] op_sel_hi:[0,1,1]
	v_lshlrev_b32_e32 v86, 16, v30
	v_and_b32_e32 v87, 0xffff0000, v30
	v_lshlrev_b32_e32 v30, 16, v31
	v_and_b32_e32 v31, 0xffff0000, v31
	s_waitcnt lgkmcnt(0)
; __device__ __forceinline__ void ph13(LAS unsigned char* lds, int tid, int lane_, int wave, int G, int bid) {
;     ...
;         const float mean = wave_sum(s) * (1.f / D); float s2 = 0.f;
; #pragma unroll
;         for (int j = 0; j < 8; ++j) { v[j] = v[j] - mean; s2 += (v[j].x * v[j].x + v[j].y * v[j].y) + (v[j].z * v[j].z + v[j].w * v[j].w); }
	v_pk_mul_f32 v[52:53], v[92:93], v[52:53]
	v_pk_mul_f32 v[88:89], v[90:91], v[88:89]
	v_pk_fma_f32 v[30:31], v[30:31], s[10:11], v[52:53] op_sel_hi:[1,0,1]
	v_pk_fma_f32 v[52:53], v[86:87], s[10:11], v[88:89] op_sel_hi:[1,0,1]
	v_mov_b32_e32 v89, v31
	v_pk_mov_b32 v[86:87], v[52:53], v[30:31] op_sel:[1,0]
	v_mov_b32_e32 v88, v52
	v_pk_add_f32 v[86:87], v[86:87], v[88:89]
	v_cvt_pk_f32_fp8_e32 v[88:89], v55
	v_pk_add_f32 v[96:97], v[86:87], v[86:87] op_sel:[0,1] op_sel_hi:[1,0]
	v_cvt_pk_f32_fp8_sdwa v[86:87], v55 src0_sel:WORD_1
	v_cvt_pk_f32_fp8_e32 v[90:91], v54
	v_cvt_pk_f32_fp8_sdwa v[54:55], v54 src0_sel:WORD_1
	v_pk_mul_f32 v[88:89], v[58:59], v[88:89] op_sel_hi:[0,1]
	v_pk_mul_f32 v[86:87], v[58:59], v[86:87] op_sel_hi:[0,1]
	v_pk_fma_f32 v[98:99], v[56:57], v[90:91], v[88:89] op_sel_hi:[0,1,1]
	v_pk_fma_f32 v[54:55], v[56:57], v[54:55], v[86:87] op_sel_hi:[0,1,1]
	ds_read_b128 v[86:89], v1 offset:6144
	ds_read_b128 v[90:93], v1 offset:7168
	v_lshlrev_b32_e32 v100, 16, v28
	v_and_b32_e32 v101, 0xffff0000, v28
	v_lshlrev_b32_e32 v28, 16, v29
	v_and_b32_e32 v29, 0xffff0000, v29
	s_waitcnt lgkmcnt(1)
	v_pk_mul_f32 v[54:55], v[88:89], v[54:55]
	v_pk_mul_f32 v[86:87], v[86:87], v[98:99]
	v_cvt_pk_f32_fp8_sdwa v[98:99], v84 src0_sel:WORD_1
	v_cvt_pk_f32_fp8_e32 v[84:85], v84
	v_pk_fma_f32 v[54:55], v[28:29], s[10:11], v[54:55] op_sel_hi:[1,0,1]
	v_pk_fma_f32 v[28:29], v[100:101], s[10:11], v[86:87] op_sel_hi:[1,0,1]
	v_cvt_pk_f32_fp8_e32 v[100:101], v57
	v_cvt_pk_f32_fp8_sdwa v[102:103], v57 src0_sel:WORD_1
	v_pk_mul_f32 v[98:99], v[58:59], v[98:99] op_sel_hi:[0,1]
	v_pk_mul_f32 v[84:85], v[58:59], v[84:85] op_sel_hi:[0,1]
	v_pk_fma_f32 v[84:85], v[56:57], v[100:101], v[84:85] op_sel_hi:[0,1,1]
	v_pk_fma_f32 v[56:57], v[56:57], v[102:103], v[98:99] op_sel_hi:[0,1,1]
	v_lshlrev_b32_e32 v98, 16, v26
	v_and_b32_e32 v99, 0xffff0000, v26
	v_lshlrev_b32_e32 v26, 16, v27
	v_and_b32_e32 v27, 0xffff0000, v27
	s_waitcnt lgkmcnt(0)
	v_pk_mul_f32 v[56:57], v[92:93], v[56:57]
	v_pk_mul_f32 v[84:85], v[90:91], v[84:85]
	v_pk_fma_f32 v[26:27], v[26:27], s[10:11], v[56:57] op_sel_hi:[1,0,1]
	v_pk_fma_f32 v[56:57], v[98:99], s[10:11], v[84:85] op_sel_hi:[1,0,1]
	v_add_f32_e32 v86, v28, v29
	v_add_f32_e32 v88, v54, v55
	v_mov_b32_e32 v95, v56
	v_mov_b32_e32 v97, v57
	v_mov_b32_e32 v87, v26
	v_mov_b32_e32 v89, v27
	v_pk_add_f32 v[84:85], v[94:95], v[96:97]
	v_pk_add_f32 v[86:87], v[86:87], v[88:89]
	s_add_i32 s6, s6, s16
	v_pk_add_f32 v[84:85], v[84:85], v[86:87]
	v_lshl_add_u64 v[6:7], v[6:7], 0, s[8:9]
	v_add_f32_e32 v1, v84, v85
	ds_bpermute_b32 v58, v60, v1
	s_waitcnt lgkmcnt(0)
	v_add_f32_e32 v1, v1, v58
	ds_bpermute_b32 v58, v61, v1
	s_waitcnt lgkmcnt(0)
	v_add_f32_e32 v1, v1, v58
	ds_bpermute_b32 v58, v62, v1
	s_waitcnt lgkmcnt(0)
	v_add_f32_e32 v1, v1, v58
	ds_bpermute_b32 v58, v63, v1
	s_waitcnt lgkmcnt(0)
	v_add_f32_e32 v1, v1, v58
	ds_bpermute_b32 v58, v64, v1
	s_waitcnt lgkmcnt(0)
	v_add_f32_e32 v1, v1, v58
	ds_bpermute_b32 v58, v65, v1
	s_waitcnt lgkmcnt(0)
	v_add_f32_e32 v1, v1, v58
	v_fmamk_f32 v37, v1, 0xba000000, v37
	v_fmamk_f32 v39, v1, 0xba000000, v39
	v_fmamk_f32 v33, v1, 0xba000000, v33
	v_fmac_f32_e32 v36, 0xba000000, v1
	v_fmamk_f32 v35, v1, 0xba000000, v35
	v_fmac_f32_e32 v38, 0xba000000, v1
	v_mov_b32_e32 v86, v37
	v_mov_b32_e32 v87, v39
	v_fmac_f32_e32 v32, 0xba000000, v1
	v_fmac_f32_e32 v34, 0xba000000, v1
	v_mov_b32_e32 v84, v36
	v_mov_b32_e32 v85, v38
	v_pk_mul_f32 v[86:87], v[86:87], v[86:87]
	v_mov_b32_e32 v88, v33
	v_mov_b32_e32 v89, v35
	v_pk_fma_f32 v[84:85], v[84:85], v[84:85], v[86:87]
	v_mov_b32_e32 v86, v32
	v_mov_b32_e32 v87, v34
	v_pk_mul_f32 v[88:89], v[88:89], v[88:89]
	v_fmamk_f32 v45, v1, 0xba000000, v45
	v_pk_fma_f32 v[86:87], v[86:87], v[86:87], v[88:89]
	v_fmac_f32_e32 v44, 0xba000000, v1
	v_fmamk_f32 v47, v1, 0xba000000, v47
	v_fmac_f32_e32 v46, 0xba000000, v1
	v_pk_add_f32 v[84:85], v[84:85], v[86:87]
	v_pk_mul_f32 v[86:87], v[46:47], v[46:47]
	v_pk_mul_f32 v[88:89], v[44:45], v[44:45]
	v_fmac_f32_e32 v48, 0xba000000, v1
	v_pk_mov_b32 v[90:91], v[88:89], v[86:87] op_sel:[1,0]
	v_mov_b32_e32 v89, v87
	v_fmamk_f32 v49, v1, 0xba000000, v49
	v_fmac_f32_e32 v42, 0xba000000, v1
	v_mul_f32_e32 v58, v48, v48
	v_pk_add_f32 v[86:87], v[90:91], v[88:89]
	v_fmamk_f32 v43, v1, 0xba000000, v43
	v_pk_fma_f32 v[88:89], v[48:49], v[48:49], v[58:59] op_sel_hi:[1,1,0]
	v_mul_f32_e32 v58, v42, v42
	v_pk_add_f32 v[84:85], v[84:85], v[84:85] op_sel_hi:[0,1]
	v_pk_add_f32 v[86:87], v[86:87], v[86:87] op_sel_hi:[0,1]
	v_pk_fma_f32 v[90:91], v[42:43], v[42:43], v[58:59] op_sel_hi:[1,1,0]
	v_fmamk_f32 v51, v1, 0xba000000, v51
	v_fmac_f32_e32 v50, 0xba000000, v1
	v_fmamk_f32 v41, v1, 0xba000000, v41
	v_fmac_f32_e32 v40, 0xba000000, v1
	v_mul_f32_e32 v88, v40, v40
	v_mul_f32_e32 v90, v41, v41
	v_mul_f32_e32 v86, v50, v50
	v_mul_f32_e32 v84, v51, v51
	v_pk_add_f32 v[88:89], v[88:89], v[90:91]
	v_pk_add_f32 v[84:85], v[86:87], v[84:85]
	v_fmamk_f32 v53, v1, 0xba000000, v53
	v_fmac_f32_e32 v52, 0xba000000, v1
	v_fmamk_f32 v31, v1, 0xba000000, v31
	v_fmac_f32_e32 v30, 0xba000000, v1
	v_pk_add_f32 v[84:85], v[88:89], v[84:85]
	v_pk_mul_f32 v[86:87], v[30:31], v[30:31]
	v_pk_mul_f32 v[88:89], v[52:53], v[52:53]
	v_fmac_f32_e32 v28, 0xba000000, v1
	v_pk_mov_b32 v[90:91], v[88:89], v[86:87] op_sel:[1,0]
	v_mov_b32_e32 v89, v87
	v_fmamk_f32 v29, v1, 0xba000000, v29
	v_fmac_f32_e32 v54, 0xba000000, v1
	v_mul_f32_e32 v58, v28, v28
	v_pk_add_f32 v[86:87], v[90:91], v[88:89]
	v_fmamk_f32 v55, v1, 0xba000000, v55
	v_pk_fma_f32 v[88:89], v[28:29], v[28:29], v[58:59] op_sel_hi:[1,1,0]
	v_mul_f32_e32 v58, v54, v54
	v_pk_add_f32 v[84:85], v[84:85], v[84:85] op_sel_hi:[0,1]
	v_pk_add_f32 v[86:87], v[86:87], v[86:87] op_sel_hi:[0,1]
	v_pk_fma_f32 v[90:91], v[54:55], v[54:55], v[58:59] op_sel_hi:[1,1,0]
	v_fmamk_f32 v27, v1, 0xba000000, v27
	v_fmac_f32_e32 v26, 0xba000000, v1
	v_fmamk_f32 v57, v1, 0xba000000, v57
	v_fmac_f32_e32 v56, 0xba000000, v1
	v_mul_f32_e32 v88, v56, v56
	v_mul_f32_e32 v90, v57, v57
	v_mul_f32_e32 v86, v26, v26
	v_mul_f32_e32 v84, v27, v27
	v_pk_add_f32 v[88:89], v[88:89], v[90:91]
	v_pk_add_f32 v[84:85], v[86:87], v[84:85]
	s_nop 0
	v_pk_add_f32 v[84:85], v[88:89], v[84:85]
	s_nop 0
	v_add_f32_e32 v1, v84, v85
	ds_bpermute_b32 v58, v60, v1
	s_waitcnt lgkmcnt(0)
; #define LAS __attribute__((address_space(3)))
; __device__ __forceinline__ void ph13(LAS unsigned char* lds, int tid, int lane_, int wave, int G, int bid) {
;     ...
;         const float rstd = 1.f / sqrtf(wave_sum(s2) * (1.f / D) + LN_EPS);
;         const LAS f32x4* g2 = VG + 4 * 512 + lane; const LAS f32x4* b2 = VG + 5 * 512 + lane;
; #pragma unroll
;         for (int j = 0; j < 8; ++j) __builtin_nontemporal_store(v[j] * rstd * g2[64 * j] + b2[64 * j], xq + 64 * j);
; #pragma unroll
;         for (int j = 0; j < 8; ++j) { p0[j] = q0[j]; p1[j] = q1[j]; xb[j] = xn[j]; }
;         w0 = wn0; w1 = wn1;
	v_add_f32_e32 v1, v1, v58
	ds_bpermute_b32 v58, v61, v1
	s_waitcnt lgkmcnt(0)
	v_add_f32_e32 v1, v1, v58
	ds_bpermute_b32 v58, v62, v1
	s_waitcnt lgkmcnt(0)
	v_add_f32_e32 v1, v1, v58
	ds_bpermute_b32 v58, v63, v1
	s_waitcnt lgkmcnt(0)
	v_add_f32_e32 v1, v1, v58
	ds_bpermute_b32 v58, v64, v1
	s_waitcnt lgkmcnt(0)
	v_add_f32_e32 v1, v1, v58
	ds_bpermute_b32 v58, v65, v1
	s_waitcnt lgkmcnt(0)
	v_add_f32_e32 v1, v1, v58
	v_fmamk_f32 v1, v1, 0x3a000000, v66
	v_mul_f32_e32 v58, 0x4f800000, v1
	v_cmp_gt_f32_e32 vcc, s3, v1
	s_nop 1
	v_cndmask_b32_e32 v1, v1, v58, vcc
	v_sqrt_f32_e32 v58, v1
	s_nop 0
	v_add_u32_e32 v84, -1, v58
	v_fma_f32 v85, -v84, v58, v1
	v_cmp_ge_f32_e64 s[0:1], 0, v85
	v_add_u32_e32 v85, 1, v58
	s_nop 0
	v_cndmask_b32_e64 v84, v58, v84, s[0:1]
	v_fma_f32 v58, -v85, v58, v1
	v_cmp_lt_f32_e64 s[0:1], 0, v58
	s_nop 1
	v_cndmask_b32_e64 v58, v84, v85, s[0:1]
	v_mul_f32_e32 v84, 0x37800000, v58
	v_cndmask_b32_e32 v58, v58, v84, vcc
	v_cmp_class_f32_e32 vcc, v1, v67
	s_nop 1
	v_cndmask_b32_e32 v1, v58, v1, vcc
	v_div_scale_f32 v58, s[0:1], v1, v1, 1.0
	v_rcp_f32_e32 v92, v58
	s_mov_b32 s0, s20
	v_fma_f32 v84, -v58, v92, 1.0
	v_fmac_f32_e32 v92, v84, v92
	v_div_scale_f32 v84, vcc, 1.0, v1, 1.0
	v_mul_f32_e32 v93, v84, v92
	v_fma_f32 v85, -v58, v93, v84
	v_fmac_f32_e32 v93, v85, v92
	v_fma_f32 v58, -v58, v93, v84
	ds_read_b128 v[84:87], v59 offset:32768
	ds_read_b128 v[88:91], v59 offset:40960
	v_div_fmas_f32 v58, v58, v92, v93
	v_div_fixup_f32 v58, v58, v1, 1.0
	v_pk_mul_f32 v[32:33], v[32:33], v[58:59] op_sel_hi:[1,0]
	v_pk_mul_f32 v[36:37], v[36:37], v[58:59] op_sel_hi:[1,0]
	s_waitcnt lgkmcnt(0)
	v_pk_fma_f32 v[86:87], v[86:87], v[32:33], v[90:91]
	v_add_co_u32_e32 v32, vcc, s11, v4
	v_pk_fma_f32 v[84:85], v[84:85], v[36:37], v[88:89]
	s_nop 0
	v_addc_co_u32_e32 v33, vcc, -1, v5, vcc
	global_store_dwordx4 v[32:33], v[84:87], off nt
	ds_read_b128 v[84:87], v59 offset:33792
	ds_read_b128 v[88:91], v59 offset:41984
	v_pk_mul_f32 v[34:35], v[34:35], v[58:59] op_sel_hi:[1,0]
	v_pk_mul_f32 v[32:33], v[38:39], v[58:59] op_sel_hi:[1,0]
	v_add_co_u32_e32 v36, vcc, s17, v4
	s_waitcnt lgkmcnt(0)
	v_pk_fma_f32 v[32:33], v[84:85], v[32:33], v[88:89]
	v_pk_fma_f32 v[34:35], v[86:87], v[34:35], v[90:91]
	v_addc_co_u32_e32 v37, vcc, -1, v5, vcc
	global_store_dwordx4 v[36:37], v[32:35], off nt
	ds_read_b128 v[32:35], v59 offset:34816
	ds_read_b128 v[36:39], v59 offset:43008
	v_pk_mul_f32 v[44:45], v[44:45], v[58:59] op_sel_hi:[1,0]
	v_pk_mul_f32 v[46:47], v[46:47], v[58:59] op_sel_hi:[1,0]
	v_pk_mul_f32 v[42:43], v[42:43], v[58:59] op_sel_hi:[1,0]
	v_pk_mul_f32 v[40:41], v[40:41], v[58:59] op_sel_hi:[1,0]
	s_waitcnt lgkmcnt(0)
	v_pk_fma_f32 v[32:33], v[32:33], v[44:45], v[36:37]
	v_add_co_u32_e32 v36, vcc, s18, v4
	v_pk_fma_f32 v[34:35], v[34:35], v[46:47], v[38:39]
	s_nop 0
	v_addc_co_u32_e32 v37, vcc, -1, v5, vcc
	global_store_dwordx4 v[36:37], v[32:35], off nt
	ds_read_b128 v[32:35], v59 offset:35840
	ds_read_b128 v[36:39], v59 offset:44032
	v_pk_mul_f32 v[44:45], v[48:49], v[58:59] op_sel_hi:[1,0]
	v_pk_mul_f32 v[28:29], v[28:29], v[58:59] op_sel_hi:[1,0]
	s_waitcnt lgkmcnt(0)
	v_pk_fma_f32 v[32:33], v[32:33], v[44:45], v[36:37]
	v_add_co_u32_e32 v36, vcc, s19, v4
	v_pk_fma_f32 v[34:35], v[34:35], v[42:43], v[38:39]
	s_nop 0
	v_addc_co_u32_e32 v37, vcc, -1, v5, vcc
	global_store_dwordx4 v[36:37], v[32:35], off nt
	ds_read_b128 v[32:35], v59 offset:36864
	ds_read_b128 v[36:39], v59 offset:45056
	v_pk_mul_f32 v[42:43], v[50:51], v[58:59] op_sel_hi:[1,0]
	s_andn2_b64 vcc, exec, s[12:13]
	s_waitcnt lgkmcnt(0)
	v_pk_fma_f32 v[32:33], v[32:33], v[40:41], v[36:37]
	v_pk_fma_f32 v[34:35], v[34:35], v[42:43], v[38:39]
	global_store_dwordx4 v[4:5], v[32:35], off nt
	ds_read_b128 v[32:35], v59 offset:37888
	ds_read_b128 v[36:39], v59 offset:46080
	v_pk_mul_f32 v[40:41], v[30:31], v[58:59] op_sel_hi:[1,0]
	v_pk_mul_f32 v[30:31], v[52:53], v[58:59] op_sel_hi:[1,0]
	s_waitcnt lgkmcnt(0)
	v_pk_fma_f32 v[30:31], v[32:33], v[30:31], v[36:37]
	v_pk_fma_f32 v[32:33], v[34:35], v[40:41], v[38:39]
	global_store_dwordx4 v[4:5], v[30:33], off offset:1024 nt
	ds_read_b128 v[30:33], v59 offset:38912
	ds_read_b128 v[34:37], v59 offset:47104
	v_pk_mul_f32 v[38:39], v[54:55], v[58:59] op_sel_hi:[1,0]
	s_waitcnt lgkmcnt(0)
	v_pk_fma_f32 v[28:29], v[30:31], v[28:29], v[34:35]
	v_pk_fma_f32 v[30:31], v[32:33], v[38:39], v[36:37]
	global_store_dwordx4 v[4:5], v[28:31], off offset:2048 nt
	ds_read_b128 v[28:31], v59 offset:39936
	ds_read_b128 v[32:35], v59 offset:48128
	v_pk_mul_f32 v[36:37], v[26:27], v[58:59] op_sel_hi:[1,0]
	v_pk_mul_f32 v[26:27], v[56:57], v[58:59] op_sel_hi:[1,0]
	s_waitcnt lgkmcnt(0)
	v_pk_fma_f32 v[26:27], v[28:29], v[26:27], v[32:33]
	v_pk_fma_f32 v[28:29], v[30:31], v[36:37], v[34:35]
	global_store_dwordx4 v[4:5], v[26:29], off offset:3072 nt
	v_lshl_add_u64 v[4:5], v[4:5], 0, s[4:5]
	s_waitcnt vmcnt(8)
	v_mov_b32_e32 v48, v71
	v_mov_b32_e32 v46, v70
	v_mov_b32_e32 v50, v72
	v_mov_b32_e32 v85, v68
	v_mov_b32_e32 v52, v73
	v_mov_b32_e32 v84, v83
	v_mov_b32_e32 v54, v74
	v_mov_b32_e32 v55, v82
	v_mov_b32_e32 v53, v81
	v_mov_b32_e32 v57, v75
	v_mov_b32_e32 v38, v69
	v_mov_b32_e32 v51, v80
	v_mov_b32_e32 v49, v79
	v_mov_b32_e32 v47, v78
	v_mov_b32_e32 v39, v77
	v_mov_b32_e32 v86, v76
	v_mov_b64_e32 v[26:27], v[16:17]
	v_mov_b64_e32 v[28:29], v[22:23]
	v_mov_b64_e32 v[30:31], v[20:21]
	v_mov_b64_e32 v[40:41], v[18:19]
	v_mov_b64_e32 v[42:43], v[14:15]
	v_mov_b64_e32 v[44:45], v[12:13]
	v_mov_b64_e32 v[34:35], v[10:11]
	v_mov_b64_e32 v[32:33], v[8:9]
	v_mov_b64_e32 v[36:37], v[24:25]
	s_cbranch_vccz .LBB0_1220
